# v84 + cache policy: GEMM epilogue global_store_dwordx4 (all 8 GEMM phases) marked nt so the 32 MB-per-round output stream stops evicting the A/B operand tiles from L2
# baseline (speedup 1.0000x reference)
.LBB0_151:
	s_lshl_b32 s17, s2, 8
	s_add_i32 s17, s17, s61
	v_or_b32_e32 v154, s17, v139
	s_mov_b64 s[2:3], -1
	s_cmp_gt_i32 s6, 15
	v_or_b32_e32 v164, 16, v154
	v_or_b32_e32 v162, 32, v154
	v_or_b32_e32 v160, 48, v154
	v_lshlrev_b32_e32 v136, 1, v138
	s_cbranch_scc0 .LBB0_153
	s_cmp_lt_u32 s6, 32
	s_cselect_b64 s[2:3], -1, 0
	s_and_b64 s[2:3], s[2:3], exec
	v_readlane_b32 s24, v250, 48
	s_cselect_b32 s2, -16, 0xffffffe0
	v_readlane_b32 s25, v250, 49
	s_cselect_b32 s7, s25, s60
	s_cselect_b32 s19, s24, s59
	s_add_i32 s8, s2, s6
	s_lshl_b64 s[2:3], s[8:9], 9
	s_add_u32 s2, s19, s2
	s_addc_u32 s3, s7, s3
	v_ashrrev_i32_e32 v155, 31, v154
	v_lshl_add_u64 v[158:159], s[2:3], 0, v[136:137]
	v_lshlrev_b64 v[156:157], 13, v[154:155]
	v_lshl_add_u64 v[156:157], v[158:159], 0, v[156:157]
	v_cvt_pk_bf16_f32 v180, v124, v125
	v_cvt_pk_bf16_f32 v181, v126, v127
	v_cvt_pk_bf16_f32 v182, v116, v117
	v_cvt_pk_bf16_f32 v183, v118, v119
	global_store_dwordx4 v[156:157], v[180:183], off nt
	v_ashrrev_i32_e32 v165, 31, v164
	v_ashrrev_i32_e32 v163, 31, v162
	v_cvt_pk_bf16_f32 v180, v120, v121
	v_cvt_pk_bf16_f32 v181, v122, v123
	v_cvt_pk_bf16_f32 v182, v112, v113
	v_cvt_pk_bf16_f32 v183, v114, v115
	global_store_dwordx4 v[156:157], v[180:183], off offset:256 nt
	v_ashrrev_i32_e32 v161, 31, v160
	s_mov_b64 s[2:3], 0x100000
	v_lshlrev_b64 v[180:181], 13, v[164:165]
	v_lshl_add_u64 v[184:185], v[158:159], 0, v[180:181]
	v_cvt_pk_bf16_f32 v180, v108, v109
	v_cvt_pk_bf16_f32 v181, v110, v111
	v_cvt_pk_bf16_f32 v182, v100, v101
	v_cvt_pk_bf16_f32 v183, v102, v103
	global_store_dwordx4 v[184:185], v[180:183], off nt
	s_nop 1
	v_cvt_pk_bf16_f32 v180, v104, v105
	v_cvt_pk_bf16_f32 v181, v106, v107
	v_cvt_pk_bf16_f32 v182, v96, v97
	v_cvt_pk_bf16_f32 v183, v98, v99
	global_store_dwordx4 v[184:185], v[180:183], off offset:256 nt
	s_nop 1
	v_lshlrev_b64 v[180:181], 13, v[162:163]
	v_lshl_add_u64 v[184:185], v[158:159], 0, v[180:181]
	v_cvt_pk_bf16_f32 v180, v92, v93
	v_cvt_pk_bf16_f32 v181, v94, v95
	v_cvt_pk_bf16_f32 v182, v84, v85
	v_cvt_pk_bf16_f32 v183, v86, v87
	global_store_dwordx4 v[184:185], v[180:183], off nt
	s_nop 1
	v_cvt_pk_bf16_f32 v180, v88, v89
	v_cvt_pk_bf16_f32 v181, v90, v91
	v_cvt_pk_bf16_f32 v182, v80, v81
	v_cvt_pk_bf16_f32 v183, v82, v83
	global_store_dwordx4 v[184:185], v[180:183], off offset:256 nt
	s_nop 1
	v_lshlrev_b64 v[180:181], 13, v[160:161]
	v_lshl_add_u64 v[158:159], v[158:159], 0, v[180:181]
	v_cvt_pk_bf16_f32 v180, v76, v77
	v_cvt_pk_bf16_f32 v181, v78, v79
	v_cvt_pk_bf16_f32 v182, v68, v69
	v_cvt_pk_bf16_f32 v183, v70, v71
	global_store_dwordx4 v[158:159], v[180:183], off nt
	s_nop 1
	v_cvt_pk_bf16_f32 v180, v72, v73
	v_cvt_pk_bf16_f32 v181, v74, v75
	v_cvt_pk_bf16_f32 v182, v64, v65
	v_cvt_pk_bf16_f32 v183, v66, v67
	global_store_dwordx4 v[158:159], v[180:183], off offset:256 nt
	v_lshl_add_u64 v[158:159], v[156:157], 0, s[2:3]
	s_mov_b32 s2, 0x100000
	v_add_co_u32_e32 v184, vcc, s2, v156
	v_cvt_pk_bf16_f32 v180, v60, v61
	v_cvt_pk_bf16_f32 v181, v62, v63
	v_cvt_pk_bf16_f32 v182, v52, v53
	v_cvt_pk_bf16_f32 v183, v54, v55
	s_nop 1
	v_addc_co_u32_e32 v185, vcc, 0, v157, vcc
	s_mov_b64 s[2:3], 0x120000
	global_store_dwordx4 v[184:185], v[180:183], off nt
	s_nop 1
	v_cvt_pk_bf16_f32 v180, v56, v57
	v_cvt_pk_bf16_f32 v181, v58, v59
	v_cvt_pk_bf16_f32 v182, v48, v49
	v_cvt_pk_bf16_f32 v183, v50, v51
	global_store_dwordx4 v[158:159], v[180:183], off offset:256 nt
	v_lshl_add_u64 v[158:159], v[156:157], 0, s[2:3]
	s_mov_b32 s2, 0x120000
	v_add_co_u32_e32 v184, vcc, s2, v156
	v_cvt_pk_bf16_f32 v180, v44, v45
	v_cvt_pk_bf16_f32 v181, v46, v47
	v_cvt_pk_bf16_f32 v182, v36, v37
	v_cvt_pk_bf16_f32 v183, v38, v39
	s_nop 1
	v_addc_co_u32_e32 v185, vcc, 0, v157, vcc
	s_mov_b64 s[2:3], 0x140000
	global_store_dwordx4 v[184:185], v[180:183], off nt
	s_nop 1
	v_cvt_pk_bf16_f32 v180, v40, v41
	v_cvt_pk_bf16_f32 v181, v42, v43
	v_cvt_pk_bf16_f32 v182, v32, v33
	v_cvt_pk_bf16_f32 v183, v34, v35
	global_store_dwordx4 v[158:159], v[180:183], off offset:256 nt
	v_lshl_add_u64 v[158:159], v[156:157], 0, s[2:3]
	s_mov_b32 s2, 0x140000
	v_add_co_u32_e32 v184, vcc, s2, v156
	s_mov_b64 s[2:3], 0x160000
	s_nop 0
	v_addc_co_u32_e32 v185, vcc, 0, v157, vcc
	v_cvt_pk_bf16_f32 v180, v28, v29
	v_cvt_pk_bf16_f32 v181, v30, v31
	v_cvt_pk_bf16_f32 v182, v20, v21
	v_cvt_pk_bf16_f32 v183, v22, v23
	global_store_dwordx4 v[184:185], v[180:183], off nt
	v_lshl_add_u64 v[184:185], v[156:157], 0, s[2:3]
	s_mov_b32 s2, 0x160000
	v_add_co_u32_e32 v156, vcc, s2, v156
	v_cvt_pk_bf16_f32 v180, v24, v25
	v_cvt_pk_bf16_f32 v181, v26, v27
	v_cvt_pk_bf16_f32 v182, v16, v17
	v_cvt_pk_bf16_f32 v183, v18, v19
	s_nop 1
	v_addc_co_u32_e32 v157, vcc, 0, v157, vcc
	global_store_dwordx4 v[158:159], v[180:183], off offset:256 nt
	s_mov_b64 s[2:3], 0
	s_nop 0
	v_cvt_pk_bf16_f32 v180, v12, v13
	v_cvt_pk_bf16_f32 v181, v14, v15
	v_cvt_pk_bf16_f32 v182, v4, v5
	v_cvt_pk_bf16_f32 v183, v6, v7
	global_store_dwordx4 v[156:157], v[180:183], off nt
	v_cvt_pk_bf16_f32 v156, v8, v9
	v_cvt_pk_bf16_f32 v157, v10, v11
	v_cvt_pk_bf16_f32 v158, v0, v1
	v_cvt_pk_bf16_f32 v159, v2, v3
	global_store_dwordx4 v[184:185], v[156:159], off offset:256 nt
.LBB0_153:
	s_andn2_b64 vcc, exec, s[2:3]
	s_cbranch_vccnz .LBB0_186
	s_cmp_gt_i32 s6, 7
	s_cselect_b64 s[24:25], -1, 0
	s_cmp_lt_i32 s6, 8
	s_cselect_b64 s[2:3], -1, 0
	s_and_b64 s[26:27], s[2:3], exec
	v_readlane_b32 s26, v250, 46
	v_readlane_b32 s27, v250, 47
	s_cselect_b32 s7, s27, s58
	s_cselect_b32 s8, s26, s57
	s_and_b32 s19, s6, 7
	v_cvt_f32_ubyte0_e32 v155, s19
	v_sub_f32_e32 v155, 0xc0a00000, v155
	v_exp_f32_e32 v155, v155
	s_lshl_b32 s19, s19, 9
	s_add_u32 s26, s8, s19
	s_addc_u32 s27, s7, 0
	v_sub_f32_e32 v155, 1.0, v155
	v_log_f32_e32 v155, v155
	v_lshl_add_u64 v[156:157], s[26:27], 0, v[136:137]
	v_mul_hi_i32 v136, v154, s82
	v_mov_b32_e32 v198, v124
	v_cndmask_b32_e64 v179, v155, 0, s[2:3]
	v_lshrrev_b32_e32 v155, 31, v136
	v_ashrrev_i32_e32 v136, 10, v136
	v_add_u32_e32 v136, v136, v155
	v_mul_i32_i24_e32 v136, 0x1080, v136
	v_sub_u32_e32 v136, v154, v136
	v_add_u32_e32 v155, 0xffffff90, v136
	v_cvt_f32_i32_e32 v155, v155
	v_bitop3_b32 v136, v136, s83, v176 bitop3:0x6c
	v_cvt_f32_ubyte0_e32 v136, v136
	v_mul_f32_e32 v136, v179, v136
	v_exp_f32_e32 v180, v136
	v_mul_f32_e32 v136, v143, v155
	v_fract_f32_e32 v136, v136
	v_cos_f32_e32 v182, v136
	v_sin_f32_e32 v183, v136
	v_mul_f32_e32 v136, v145, v155
	v_fract_f32_e32 v136, v136
	v_cos_f32_e32 v184, v136
	v_sin_f32_e32 v185, v136
	v_mul_f32_e32 v136, v166, v155
	v_fract_f32_e32 v136, v136
	v_cos_f32_e32 v186, v136
	v_sin_f32_e32 v187, v136
	v_mul_f32_e32 v136, v167, v155
	v_fract_f32_e32 v136, v136
	v_cos_f32_e32 v188, v136
	v_sin_f32_e32 v189, v136
	v_mul_f32_e32 v136, v168, v155
	v_fract_f32_e32 v136, v136
	v_cos_f32_e32 v190, v136
	v_sin_f32_e32 v191, v136
	v_mul_f32_e32 v136, v169, v155
	v_fract_f32_e32 v136, v136
	v_cos_f32_e32 v192, v136
	v_sin_f32_e32 v193, v136
	v_mul_f32_e32 v136, v170, v155
	v_fract_f32_e32 v136, v136
	v_mov_b32_e32 v199, v120
	v_mov_b32_e32 v202, v183
	v_mov_b32_e32 v203, v182
	v_mov_b32_e32 v120, v125
	v_sin_f32_e32 v195, v136
	v_pk_mul_f32 v[200:201], v[182:183], v[198:199]
	v_pk_mul_f32 v[182:183], v[202:203], v[198:199]
	v_pk_mul_f32 v[124:125], v[184:185], v[120:121]
	v_mov_b32_e32 v198, v185
	v_mov_b32_e32 v199, v184
	v_mov_b32_e32 v184, v126
	v_mov_b32_e32 v185, v122
	v_cos_f32_e32 v194, v136
	v_pk_mul_f32 v[120:121], v[198:199], v[120:121]
	v_pk_mul_f32 v[198:199], v[186:187], v[184:185]
	v_mov_b32_e32 v202, v187
	v_mov_b32_e32 v203, v186
	v_mov_b32_e32 v122, v127
	v_mov_b32_e32 v186, v189
	v_mov_b32_e32 v187, v188
	v_mul_f32_e32 v136, v171, v155
	v_pk_mul_f32 v[126:127], v[188:189], v[122:123]
	v_pk_mul_f32 v[122:123], v[186:187], v[122:123]
	v_mov_b32_e32 v186, v116
	v_mov_b32_e32 v187, v112
	v_fract_f32_e32 v136, v136
	v_pk_mul_f32 v[184:185], v[202:203], v[184:185]
	v_pk_mul_f32 v[188:189], v[190:191], v[186:187]
	v_mov_b32_e32 v202, v191
	v_mov_b32_e32 v203, v190
	v_mov_b32_e32 v112, v117
	v_mov_b32_e32 v190, v193
	v_mov_b32_e32 v191, v192
	v_cndmask_b32_e64 v158, v175, 1.0, s[2:3]
	v_cos_f32_e32 v196, v136
	v_sin_f32_e32 v197, v136
	v_pk_mul_f32 v[116:117], v[192:193], v[112:113]
	v_pk_mul_f32 v[112:113], v[190:191], v[112:113]
	v_mov_b32_e32 v190, v118
	v_mov_b32_e32 v191, v114
	v_mov_b32_e32 v159, v195
	v_mov_b32_e32 v181, v118
	v_pk_mul_f32 v[190:191], v[194:195], v[190:191]
	v_pk_mul_f32 v[180:181], v[158:159], v[180:181]
	v_add_f32_e32 v112, v112, v113
	v_mul_f32_e32 v155, v180, v112
	v_sub_f32_e32 v112, v190, v191
	v_sub_f32_e32 v116, v116, v117
	v_mul_f32_e32 v117, v180, v112
	v_fma_f32 v112, v194, v114, v181
	v_mov_b32_e32 v114, v119
	v_mul_f32_e32 v159, v180, v112
	v_pk_mul_f32 v[112:113], v[196:197], v[114:115]
	v_pk_mul_f32 v[186:187], v[202:203], v[186:187]
	v_sub_f32_e32 v112, v112, v113
	v_mul_f32_e32 v119, v180, v112
	v_mov_b32_e32 v112, v197
	v_mov_b32_e32 v113, v196
	v_sub_f32_e32 v118, v200, v201
	v_pk_mul_f32 v[112:113], v[112:113], v[114:115]
	v_mul_f32_e32 v118, v180, v118
	v_add_f32_e32 v136, v182, v183
	v_sub_f32_e32 v124, v124, v125
	v_add_f32_e32 v120, v120, v121
	v_sub_f32_e32 v121, v198, v199
	v_add_f32_e32 v125, v184, v185
	v_sub_f32_e32 v126, v126, v127
	v_add_f32_e32 v122, v122, v123
	v_sub_f32_e32 v123, v188, v189
	v_add_f32_e32 v127, v186, v187
	v_mul_f32_e32 v116, v180, v116
	v_add_f32_e32 v112, v112, v113
	s_mov_b64 s[2:3], -1
	s_and_b64 vcc, exec, s[24:25]
	v_mul_f32_e32 v136, v180, v136
	v_mul_f32_e32 v124, v180, v124
	v_mul_f32_e32 v120, v180, v120
	v_mul_f32_e32 v121, v180, v121
	v_mul_f32_e32 v125, v180, v125
	v_mul_f32_e32 v126, v180, v126
	v_mul_f32_e32 v122, v180, v122
	v_mul_f32_e32 v123, v180, v123
	v_mul_f32_e32 v127, v180, v127
	v_mul_f32_e32 v161, v180, v112
	v_cvt_pk_bf16_f32 v112, v118, v124
	v_cvt_pk_bf16_f32 v113, v121, v126
	v_cvt_pk_bf16_f32 v114, v123, v116
	v_cvt_pk_bf16_f32 v115, v117, v119
	v_cvt_pk_bf16_f32 v116, v136, v120
	v_cvt_pk_bf16_f32 v117, v125, v122
	v_cvt_pk_bf16_f32 v118, v127, v155
	v_cvt_pk_bf16_f32 v119, v159, v161
	s_cbranch_vccz .LBB0_156
	v_ashrrev_i32_e32 v155, 31, v154
	v_lshlrev_b64 v[120:121], 12, v[154:155]
	v_lshl_add_u64 v[120:121], v[156:157], 0, v[120:121]
	global_store_dwordx4 v[120:121], v[112:115], off nt
	global_store_dwordx4 v[120:121], v[116:119], off offset:256 nt
	s_mov_b64 s[2:3], 0
.LBB0_156:
	s_andn2_b64 vcc, exec, s[2:3]
	v_lshlrev_b32_e32 v136, 1, v144
	v_lshlrev_b32_e32 v122, 1, v140
	v_lshlrev_b32_e32 v120, 1, v142
	s_cbranch_vccnz .LBB0_158
	s_ashr_i32 s2, s17, 5
	s_ashr_i32 s3, s2, 31
	s_ashr_i32 s7, s6, 31
	s_lshl_b64 s[2:3], s[2:3], 17
	v_readlane_b32 s26, v250, 46
	v_readlane_b32 s27, v250, 47
	s_add_u32 s8, s26, s2
	s_addc_u32 s19, s27, s3
	s_lshl_b64 s[2:3], s[6:7], 14
	s_add_u32 s2, s8, s2
	s_addc_u32 s3, s19, s3
	v_lshl_add_u64 v[124:125], s[2:3], 0, v[136:137]
	v_mov_b32_e32 v123, v137
	v_lshl_add_u64 v[124:125], v[124:125], 0, v[122:123]
	v_mov_b32_e32 v121, v137
	v_lshl_add_u64 v[124:125], v[124:125], 0, v[120:121]
	global_store_dwordx4 v[124:125], v[112:115], off nt
	s_nop 1
	v_add_co_u32_e32 v112, vcc, 0x2000, v124
	s_nop 1
	v_addc_co_u32_e32 v113, vcc, 0, v125, vcc
	global_store_dwordx4 v[112:113], v[116:119], off nt
.LBB0_158:
	v_mul_hi_i32 v112, v164, s82
	v_lshrrev_b32_e32 v113, 31, v112
	v_ashrrev_i32_e32 v112, 10, v112
	v_add_u32_e32 v112, v112, v113
	v_mul_i32_i24_e32 v112, 0x1080, v112
	v_sub_u32_e32 v112, v164, v112
	v_add_u32_e32 v113, 0xffffff90, v112
	v_cvt_f32_i32_e32 v113, v113
	s_movk_i32 s2, 0x6f
	v_bitop3_b32 v112, v112, s2, v176 bitop3:0x6c
	v_cvt_f32_ubyte0_e32 v112, v112
	v_mul_f32_e32 v121, v167, v113
	v_mul_f32_e32 v114, v143, v113
	v_fract_f32_e32 v121, v121
	v_fract_f32_e32 v115, v114
	v_mul_f32_e32 v116, v145, v113
	v_cos_f32_e32 v124, v121
	v_sin_f32_e32 v125, v121
	v_mul_f32_e32 v121, v168, v113
	v_cos_f32_e32 v114, v115
	v_sin_f32_e32 v115, v115
	v_fract_f32_e32 v117, v116
	v_mul_f32_e32 v118, v166, v113
	v_fract_f32_e32 v121, v121
	v_cos_f32_e32 v116, v117
	v_sin_f32_e32 v117, v117
	v_fract_f32_e32 v119, v118
	v_cos_f32_e32 v126, v121
	v_sin_f32_e32 v127, v121
	v_mul_f32_e32 v121, v169, v113
	v_cos_f32_e32 v118, v119
	v_sin_f32_e32 v119, v119
	v_fract_f32_e32 v121, v121
	v_cos_f32_e32 v180, v121
	v_sin_f32_e32 v181, v121
	v_mul_f32_e32 v121, v170, v113
	v_fract_f32_e32 v121, v121
	v_mov_b32_e32 v186, v108
	v_mov_b32_e32 v187, v104
	v_mov_b32_e32 v190, v115
	v_mov_b32_e32 v191, v114
	v_mov_b32_e32 v104, v109
	v_mul_f32_e32 v112, v179, v112
	v_sin_f32_e32 v183, v121
	v_pk_mul_f32 v[188:189], v[114:115], v[186:187]
	v_pk_mul_f32 v[114:115], v[190:191], v[186:187]
	v_pk_mul_f32 v[108:109], v[116:117], v[104:105]
	v_mov_b32_e32 v186, v117
	v_mov_b32_e32 v187, v116
	v_mov_b32_e32 v116, v110
	v_mov_b32_e32 v117, v106
	v_exp_f32_e32 v112, v112
	v_cos_f32_e32 v182, v121
	v_pk_mul_f32 v[104:105], v[186:187], v[104:105]
	v_pk_mul_f32 v[186:187], v[118:119], v[116:117]
	v_mov_b32_e32 v190, v119
	v_mov_b32_e32 v191, v118
	v_mov_b32_e32 v106, v111
	v_mov_b32_e32 v118, v125
	v_mov_b32_e32 v119, v124
	v_mul_f32_e32 v113, v171, v113
	v_pk_mul_f32 v[110:111], v[124:125], v[106:107]
	v_pk_mul_f32 v[106:107], v[118:119], v[106:107]
	v_mov_b32_e32 v118, v100
	v_mov_b32_e32 v119, v96
	v_fract_f32_e32 v113, v113
	v_pk_mul_f32 v[116:117], v[190:191], v[116:117]
	v_pk_mul_f32 v[124:125], v[126:127], v[118:119]
	v_mov_b32_e32 v190, v127
	v_mov_b32_e32 v191, v126
	v_mov_b32_e32 v96, v101
	v_mov_b32_e32 v126, v181
	v_mov_b32_e32 v127, v180
	v_cos_f32_e32 v184, v113
	v_sin_f32_e32 v185, v113
	v_pk_mul_f32 v[100:101], v[180:181], v[96:97]
	v_pk_mul_f32 v[96:97], v[126:127], v[96:97]
	v_mov_b32_e32 v126, v102
	v_mov_b32_e32 v127, v98
	v_mov_b32_e32 v159, v183
	v_mov_b32_e32 v113, v102
	v_pk_mul_f32 v[126:127], v[182:183], v[126:127]
	v_pk_mul_f32 v[112:113], v[158:159], v[112:113]
	v_add_f32_e32 v96, v96, v97
	v_add_f32_e32 v114, v114, v115
	v_mul_f32_e32 v115, v112, v96
	v_sub_f32_e32 v96, v126, v127
	v_sub_f32_e32 v100, v100, v101
	v_mul_f32_e32 v101, v112, v96
	v_fma_f32 v96, v182, v98, v113
	v_mov_b32_e32 v98, v103
	v_mul_f32_e32 v113, v112, v96
	v_pk_mul_f32 v[96:97], v[184:185], v[98:99]
	v_pk_mul_f32 v[118:119], v[190:191], v[118:119]
	v_sub_f32_e32 v96, v96, v97
	v_mul_f32_e32 v103, v112, v96
	v_mov_b32_e32 v96, v185
	v_mov_b32_e32 v97, v184
	v_add_f32_e32 v104, v104, v105
	v_pk_mul_f32 v[96:97], v[96:97], v[98:99]
	v_sub_f32_e32 v102, v188, v189
	v_sub_f32_e32 v108, v108, v109
	v_mul_f32_e32 v104, v112, v104
	v_sub_f32_e32 v105, v186, v187
	v_add_f32_e32 v109, v116, v117
	v_sub_f32_e32 v110, v110, v111
	v_add_f32_e32 v106, v106, v107
	v_sub_f32_e32 v107, v124, v125
	v_add_f32_e32 v111, v118, v119
	v_mul_f32_e32 v100, v112, v100
	v_add_f32_e32 v96, v96, v97
	v_mul_f32_e32 v102, v112, v102
	v_mul_f32_e32 v114, v112, v114
	v_mul_f32_e32 v108, v112, v108
	v_mul_f32_e32 v105, v112, v105
	v_mul_f32_e32 v109, v112, v109
	v_mul_f32_e32 v110, v112, v110
	v_mul_f32_e32 v106, v112, v106
	v_mul_f32_e32 v107, v112, v107
	v_mul_f32_e32 v111, v112, v111
	v_mul_f32_e32 v112, v112, v96
	v_cvt_pk_bf16_f32 v96, v102, v108
	v_cvt_pk_bf16_f32 v97, v105, v110
	v_cvt_pk_bf16_f32 v98, v107, v100
	v_cvt_pk_bf16_f32 v99, v101, v103
	v_cvt_pk_bf16_f32 v100, v114, v104
	v_cndmask_b32_e64 v104, 0, 1, s[24:25]
	v_cmp_ne_u32_e64 s[2:3], 1, v104
	s_andn2_b64 vcc, exec, s[24:25]
	s_mov_b64 s[24:25], -1
	v_cvt_pk_bf16_f32 v101, v109, v106
	v_cvt_pk_bf16_f32 v102, v111, v115
	v_cvt_pk_bf16_f32 v103, v113, v112
	s_cbranch_vccnz .LBB0_160
	v_ashrrev_i32_e32 v165, 31, v164
	v_lshlrev_b64 v[104:105], 12, v[164:165]
	v_lshl_add_u64 v[104:105], v[156:157], 0, v[104:105]
	s_mov_b64 s[24:25], 0
	global_store_dwordx4 v[104:105], v[96:99], off nt
	global_store_dwordx4 v[104:105], v[100:103], off offset:256 nt
.LBB0_160:
	s_andn2_b64 vcc, exec, s[24:25]
	s_cbranch_vccnz .LBB0_162
	s_ashr_i32 s24, s17, 5
	s_ashr_i32 s25, s24, 31
	s_ashr_i32 s7, s6, 31
	s_lshl_b64 s[24:25], s[24:25], 17
	v_readlane_b32 s26, v250, 46
	v_readlane_b32 s27, v250, 47
	s_add_u32 s8, s26, s24
	s_addc_u32 s17, s27, s25
	s_lshl_b64 s[24:25], s[6:7], 14
	s_add_u32 s24, s8, s24
	v_lshlrev_b32_e32 v104, 4, v164
	s_addc_u32 s25, s17, s25
	v_and_b32_e32 v104, 0x1f0, v104
	v_mov_b32_e32 v105, v137
	v_lshl_add_u64 v[104:105], s[24:25], 0, v[104:105]
	v_mov_b32_e32 v123, v137
	v_lshl_add_u64 v[104:105], v[104:105], 0, v[122:123]
	v_mov_b32_e32 v121, v137
	v_lshl_add_u64 v[104:105], v[104:105], 0, v[120:121]
	global_store_dwordx4 v[104:105], v[96:99], off nt
	s_nop 1
	v_add_co_u32_e32 v96, vcc, 0x2000, v104
	s_nop 1
	v_addc_co_u32_e32 v97, vcc, 0, v105, vcc
	global_store_dwordx4 v[96:97], v[100:103], off nt
.LBB0_162:
	v_mul_hi_i32 v96, v162, s82
	v_lshrrev_b32_e32 v97, 31, v96
	v_ashrrev_i32_e32 v96, 10, v96
	v_add_u32_e32 v96, v96, v97
	v_mul_i32_i24_e32 v96, 0x1080, v96
	v_sub_u32_e32 v96, v162, v96
	v_add_u32_e32 v97, 0xffffff90, v96
	v_cvt_f32_i32_e32 v97, v97
	s_movk_i32 s7, 0x5f
	v_bitop3_b32 v96, v96, s7, v176 bitop3:0x6c
	v_cvt_f32_ubyte0_e32 v96, v96
	v_mul_f32_e32 v98, v143, v97
	v_fract_f32_e32 v99, v98
	v_mul_f32_e32 v100, v145, v97
	v_cos_f32_e32 v98, v99
	v_sin_f32_e32 v99, v99
	v_fract_f32_e32 v101, v100
	v_mul_f32_e32 v102, v166, v97
	v_mul_f32_e32 v104, v167, v97
	v_cos_f32_e32 v100, v101
	v_sin_f32_e32 v101, v101
	v_fract_f32_e32 v103, v102
	v_fract_f32_e32 v105, v104
	v_cos_f32_e32 v102, v103
	v_sin_f32_e32 v103, v103
	v_cos_f32_e32 v104, v105
	v_sin_f32_e32 v105, v105
	v_mul_f32_e32 v106, v168, v97
	v_mul_f32_e32 v108, v169, v97
	v_fract_f32_e32 v107, v106
	v_fract_f32_e32 v109, v108
	v_mul_f32_e32 v110, v170, v97
	v_cos_f32_e32 v106, v107
	v_sin_f32_e32 v107, v107
	v_cos_f32_e32 v108, v109
	v_sin_f32_e32 v109, v109
	v_fract_f32_e32 v111, v110
	v_mov_b32_e32 v114, v92
	v_mov_b32_e32 v115, v88
	v_mov_b32_e32 v118, v99
	v_mov_b32_e32 v119, v98
	v_mov_b32_e32 v88, v93
	v_mul_f32_e32 v96, v179, v96
	v_cos_f32_e32 v110, v111
	v_sin_f32_e32 v111, v111
	v_pk_mul_f32 v[116:117], v[98:99], v[114:115]
	v_pk_mul_f32 v[98:99], v[118:119], v[114:115]
	v_pk_mul_f32 v[92:93], v[100:101], v[88:89]
	v_mov_b32_e32 v114, v101
	v_mov_b32_e32 v115, v100
	v_mov_b32_e32 v100, v94
	v_mov_b32_e32 v101, v90
	v_exp_f32_e32 v96, v96
	v_pk_mul_f32 v[88:89], v[114:115], v[88:89]
	v_pk_mul_f32 v[114:115], v[102:103], v[100:101]
	v_mov_b32_e32 v118, v103
	v_mov_b32_e32 v119, v102
	v_mov_b32_e32 v90, v95
	v_mov_b32_e32 v102, v105
	v_mov_b32_e32 v103, v104
	v_mul_f32_e32 v97, v171, v97
	v_pk_mul_f32 v[94:95], v[104:105], v[90:91]
	v_pk_mul_f32 v[90:91], v[102:103], v[90:91]
	v_mov_b32_e32 v102, v84
	v_mov_b32_e32 v103, v80
	v_fract_f32_e32 v97, v97
	v_pk_mul_f32 v[100:101], v[118:119], v[100:101]
	v_pk_mul_f32 v[104:105], v[106:107], v[102:103]
	v_mov_b32_e32 v118, v107
	v_mov_b32_e32 v119, v106
	v_mov_b32_e32 v80, v85
	v_mov_b32_e32 v106, v109
	v_mov_b32_e32 v107, v108
	v_cos_f32_e32 v112, v97
	v_sin_f32_e32 v113, v97
	v_pk_mul_f32 v[84:85], v[108:109], v[80:81]
	v_pk_mul_f32 v[80:81], v[106:107], v[80:81]
	v_mov_b32_e32 v106, v86
	v_mov_b32_e32 v107, v82
	v_mov_b32_e32 v159, v111
	v_mov_b32_e32 v97, v86
	v_pk_mul_f32 v[106:107], v[110:111], v[106:107]
	v_pk_mul_f32 v[96:97], v[158:159], v[96:97]
	v_add_f32_e32 v80, v80, v81
	v_add_f32_e32 v98, v98, v99
	v_mul_f32_e32 v99, v96, v80
	v_sub_f32_e32 v80, v106, v107
	v_sub_f32_e32 v84, v84, v85
	v_mul_f32_e32 v85, v96, v80
	v_fma_f32 v80, v110, v82, v97
	v_mov_b32_e32 v82, v87
	v_mul_f32_e32 v97, v96, v80
	v_pk_mul_f32 v[80:81], v[112:113], v[82:83]
	v_pk_mul_f32 v[102:103], v[118:119], v[102:103]
	v_sub_f32_e32 v80, v80, v81
	v_mul_f32_e32 v87, v96, v80
	v_mov_b32_e32 v80, v113
	v_mov_b32_e32 v81, v112
	v_sub_f32_e32 v86, v116, v117
	v_pk_mul_f32 v[80:81], v[80:81], v[82:83]
	v_mul_f32_e32 v86, v96, v86
	v_sub_f32_e32 v92, v92, v93
	v_add_f32_e32 v88, v88, v89
	v_sub_f32_e32 v89, v114, v115
	v_add_f32_e32 v93, v100, v101
	v_sub_f32_e32 v94, v94, v95
	v_add_f32_e32 v90, v90, v91
	v_sub_f32_e32 v91, v104, v105
	v_add_f32_e32 v95, v102, v103
	v_mul_f32_e32 v84, v96, v84
	v_add_f32_e32 v80, v80, v81
	s_and_b64 vcc, exec, s[2:3]
	s_mov_b64 s[24:25], -1
	v_mul_f32_e32 v98, v96, v98
	v_mul_f32_e32 v92, v96, v92
	v_mul_f32_e32 v88, v96, v88
	v_mul_f32_e32 v89, v96, v89
	v_mul_f32_e32 v93, v96, v93
	v_mul_f32_e32 v94, v96, v94
	v_mul_f32_e32 v90, v96, v90
	v_mul_f32_e32 v91, v96, v91
	v_mul_f32_e32 v95, v96, v95
	v_mul_f32_e32 v96, v96, v80
	v_cvt_pk_bf16_f32 v80, v86, v92
	v_cvt_pk_bf16_f32 v81, v89, v94
	v_cvt_pk_bf16_f32 v82, v91, v84
	v_cvt_pk_bf16_f32 v83, v85, v87
	v_cvt_pk_bf16_f32 v84, v98, v88
	v_cvt_pk_bf16_f32 v85, v93, v90
	v_cvt_pk_bf16_f32 v86, v95, v99
	v_cvt_pk_bf16_f32 v87, v97, v96
	s_cbranch_vccnz .LBB0_164
	v_ashrrev_i32_e32 v163, 31, v162
	v_lshlrev_b64 v[88:89], 12, v[162:163]
	v_lshl_add_u64 v[88:89], v[156:157], 0, v[88:89]
	s_mov_b64 s[24:25], 0
	global_store_dwordx4 v[88:89], v[80:83], off nt
	global_store_dwordx4 v[88:89], v[84:87], off offset:256 nt
.LBB0_164:
	s_andn2_b64 vcc, exec, s[24:25]
	s_cbranch_vccnz .LBB0_166
	v_ashrrev_i32_e32 v88, 5, v162
	v_ashrrev_i32_e32 v89, 31, v88
	v_readlane_b32 s24, v250, 46
	s_ashr_i32 s7, s6, 31
	v_lshlrev_b64 v[88:89], 17, v[88:89]
	v_readlane_b32 s25, v250, 47
	v_mov_b32_e32 v123, v137
	v_mov_b32_e32 v121, v137
	v_lshl_add_u64 v[88:89], s[24:25], 0, v[88:89]
	s_lshl_b64 s[24:25], s[6:7], 14
	v_lshl_add_u64 v[88:89], v[88:89], 0, s[24:25]
	v_lshl_add_u64 v[88:89], v[88:89], 0, v[136:137]
	v_lshl_add_u64 v[88:89], v[88:89], 0, v[122:123]
	v_lshl_add_u64 v[88:89], v[88:89], 0, v[120:121]
	global_store_dwordx4 v[88:89], v[80:83], off nt
	s_nop 1
	v_add_co_u32_e32 v80, vcc, 0x2000, v88
	s_nop 1
	v_addc_co_u32_e32 v81, vcc, 0, v89, vcc
	global_store_dwordx4 v[80:81], v[84:87], off nt
.LBB0_166:
	v_mul_hi_i32 v80, v160, s82
	v_lshrrev_b32_e32 v81, 31, v80
	v_ashrrev_i32_e32 v80, 10, v80
	v_add_u32_e32 v80, v80, v81
	v_mul_i32_i24_e32 v80, 0x1080, v80
	v_sub_u32_e32 v80, v160, v80
	v_add_u32_e32 v81, 0xffffff90, v80
	v_cvt_f32_i32_e32 v81, v81
	s_movk_i32 s7, 0x4f
	v_bitop3_b32 v80, v80, s7, v80 bitop3:0xc
	v_cvt_f32_ubyte0_e32 v80, v80
	v_mul_f32_e32 v82, v143, v81
	v_fract_f32_e32 v83, v82
	v_mul_f32_e32 v84, v145, v81
	v_cos_f32_e32 v82, v83
	v_sin_f32_e32 v83, v83
	v_fract_f32_e32 v85, v84
	v_mul_f32_e32 v86, v166, v81
	v_mul_f32_e32 v88, v167, v81
	v_cos_f32_e32 v84, v85
	v_sin_f32_e32 v85, v85
	v_fract_f32_e32 v87, v86
	v_fract_f32_e32 v89, v88
	v_cos_f32_e32 v86, v87
	v_sin_f32_e32 v87, v87
	v_cos_f32_e32 v88, v89
	v_sin_f32_e32 v89, v89
	v_mul_f32_e32 v90, v168, v81
	v_mul_f32_e32 v92, v169, v81
	v_fract_f32_e32 v91, v90
	v_fract_f32_e32 v93, v92
	v_mul_f32_e32 v94, v170, v81
	v_cos_f32_e32 v90, v91
	v_sin_f32_e32 v91, v91
	v_cos_f32_e32 v92, v93
	v_sin_f32_e32 v93, v93
	v_fract_f32_e32 v95, v94
	v_mov_b32_e32 v98, v76
	v_mov_b32_e32 v99, v72
	v_mov_b32_e32 v102, v83
	v_mov_b32_e32 v103, v82
	v_mov_b32_e32 v72, v77
	v_mul_f32_e32 v80, v179, v80
	v_cos_f32_e32 v94, v95
	v_sin_f32_e32 v95, v95
	v_pk_mul_f32 v[100:101], v[82:83], v[98:99]
	v_pk_mul_f32 v[82:83], v[102:103], v[98:99]
	v_pk_mul_f32 v[76:77], v[84:85], v[72:73]
	v_mov_b32_e32 v98, v85
	v_mov_b32_e32 v99, v84
	v_mov_b32_e32 v84, v78
	v_mov_b32_e32 v85, v74
	v_exp_f32_e32 v80, v80
	v_pk_mul_f32 v[72:73], v[98:99], v[72:73]
	v_pk_mul_f32 v[98:99], v[86:87], v[84:85]
	v_mov_b32_e32 v102, v87
	v_mov_b32_e32 v103, v86
	v_mov_b32_e32 v74, v79
	v_mov_b32_e32 v86, v89
	v_mov_b32_e32 v87, v88
	v_mul_f32_e32 v81, v171, v81
	v_pk_mul_f32 v[78:79], v[88:89], v[74:75]
	v_pk_mul_f32 v[74:75], v[86:87], v[74:75]
	v_mov_b32_e32 v86, v68
	v_mov_b32_e32 v87, v64
	v_fract_f32_e32 v81, v81
	v_pk_mul_f32 v[84:85], v[102:103], v[84:85]
	v_pk_mul_f32 v[88:89], v[90:91], v[86:87]
	v_mov_b32_e32 v102, v91
	v_mov_b32_e32 v103, v90
	v_mov_b32_e32 v64, v69
	v_mov_b32_e32 v90, v93
	v_mov_b32_e32 v91, v92
	v_cos_f32_e32 v96, v81
	v_sin_f32_e32 v97, v81
	v_pk_mul_f32 v[68:69], v[92:93], v[64:65]
	v_pk_mul_f32 v[64:65], v[90:91], v[64:65]
	v_mov_b32_e32 v90, v70
	v_mov_b32_e32 v91, v66
	v_mov_b32_e32 v159, v95
	v_mov_b32_e32 v81, v70
	v_pk_mul_f32 v[90:91], v[94:95], v[90:91]
	v_pk_mul_f32 v[80:81], v[158:159], v[80:81]
	v_add_f32_e32 v64, v64, v65
	v_add_f32_e32 v82, v82, v83
	v_mul_f32_e32 v83, v80, v64
	v_sub_f32_e32 v64, v90, v91
	v_sub_f32_e32 v68, v68, v69
	v_mul_f32_e32 v69, v80, v64
	v_fma_f32 v64, v94, v66, v81
	v_mov_b32_e32 v66, v71
	v_mul_f32_e32 v81, v80, v64
	v_pk_mul_f32 v[64:65], v[96:97], v[66:67]
	v_pk_mul_f32 v[86:87], v[102:103], v[86:87]
	v_sub_f32_e32 v64, v64, v65
	v_mul_f32_e32 v71, v80, v64
	v_mov_b32_e32 v64, v97
	v_mov_b32_e32 v65, v96
	v_sub_f32_e32 v70, v100, v101
	v_pk_mul_f32 v[64:65], v[64:65], v[66:67]
	v_mul_f32_e32 v70, v80, v70
	v_sub_f32_e32 v76, v76, v77
	v_add_f32_e32 v72, v72, v73
	v_sub_f32_e32 v73, v98, v99
	v_add_f32_e32 v77, v84, v85
	v_sub_f32_e32 v78, v78, v79
	v_add_f32_e32 v74, v74, v75
	v_sub_f32_e32 v75, v88, v89
	v_add_f32_e32 v79, v86, v87
	v_mul_f32_e32 v68, v80, v68
	v_add_f32_e32 v64, v64, v65
	s_and_b64 vcc, exec, s[2:3]
	s_mov_b64 s[24:25], -1
	v_mul_f32_e32 v82, v80, v82
	v_mul_f32_e32 v76, v80, v76
	v_mul_f32_e32 v72, v80, v72
	v_mul_f32_e32 v73, v80, v73
	v_mul_f32_e32 v77, v80, v77
	v_mul_f32_e32 v78, v80, v78
	v_mul_f32_e32 v74, v80, v74
	v_mul_f32_e32 v75, v80, v75
	v_mul_f32_e32 v79, v80, v79
	v_mul_f32_e32 v80, v80, v64
	v_cvt_pk_bf16_f32 v64, v70, v76
	v_cvt_pk_bf16_f32 v65, v73, v78
	v_cvt_pk_bf16_f32 v66, v75, v68
	v_cvt_pk_bf16_f32 v67, v69, v71
	v_cvt_pk_bf16_f32 v68, v82, v72
	v_cvt_pk_bf16_f32 v69, v77, v74
	v_cvt_pk_bf16_f32 v70, v79, v83
	v_cvt_pk_bf16_f32 v71, v81, v80
	s_cbranch_vccnz .LBB0_168
	v_ashrrev_i32_e32 v161, 31, v160
	v_lshlrev_b64 v[72:73], 12, v[160:161]
	v_lshl_add_u64 v[72:73], v[156:157], 0, v[72:73]
	s_mov_b64 s[24:25], 0
	global_store_dwordx4 v[72:73], v[64:67], off nt
	global_store_dwordx4 v[72:73], v[68:71], off offset:256 nt
.LBB0_168:
	s_andn2_b64 vcc, exec, s[24:25]
	s_cbranch_vccnz .LBB0_170
	v_ashrrev_i32_e32 v72, 5, v160
	v_ashrrev_i32_e32 v73, 31, v72
	v_readlane_b32 s24, v250, 46
	s_ashr_i32 s7, s6, 31
	v_lshlrev_b64 v[72:73], 17, v[72:73]
	v_readlane_b32 s25, v250, 47
	v_lshlrev_b32_e32 v74, 4, v160
	v_and_b32_e32 v74, 0x1f0, v74
	v_lshl_add_u64 v[72:73], s[24:25], 0, v[72:73]
	s_lshl_b64 s[24:25], s[6:7], 14
	v_lshl_add_u64 v[72:73], v[72:73], 0, s[24:25]
	v_mov_b32_e32 v75, v137
	v_lshl_add_u64 v[72:73], v[72:73], 0, v[74:75]
	v_mov_b32_e32 v123, v137
	v_lshl_add_u64 v[72:73], v[72:73], 0, v[122:123]
	v_mov_b32_e32 v121, v137
	v_lshl_add_u64 v[72:73], v[72:73], 0, v[120:121]
	global_store_dwordx4 v[72:73], v[64:67], off nt
	s_nop 1
	v_add_co_u32_e32 v64, vcc, 0x2000, v72
	s_nop 1
	v_addc_co_u32_e32 v65, vcc, 0, v73, vcc
	global_store_dwordx4 v[64:65], v[68:71], off nt
.LBB0_170:
	v_add_u32_e32 v64, 0x80, v154
	v_mul_hi_i32 v65, v64, s82
	v_lshrrev_b32_e32 v66, 31, v65
	v_ashrrev_i32_e32 v65, 10, v65
	v_add_u32_e32 v65, v65, v66
	v_mul_i32_i24_e32 v65, 0x1080, v65
	v_sub_u32_e32 v65, v64, v65
	v_add_u32_e32 v66, 0xffffff90, v65
	v_cvt_f32_i32_e32 v67, v66
	v_bitop3_b32 v65, v65, s83, v176 bitop3:0x6c
	v_cvt_f32_ubyte0_e32 v65, v65
	v_mul_f32_e32 v65, v179, v65
	v_exp_f32_e32 v66, v65
	v_mul_f32_e32 v65, v143, v67
	v_fract_f32_e32 v65, v65
	v_cos_f32_e32 v68, v65
	v_sin_f32_e32 v69, v65
	v_mul_f32_e32 v65, v145, v67
	v_fract_f32_e32 v65, v65
	v_cos_f32_e32 v70, v65
	v_sin_f32_e32 v71, v65
	v_mul_f32_e32 v65, v166, v67
	v_fract_f32_e32 v65, v65
	v_cos_f32_e32 v72, v65
	v_sin_f32_e32 v73, v65
	v_mul_f32_e32 v65, v167, v67
	v_fract_f32_e32 v65, v65
	v_cos_f32_e32 v74, v65
	v_sin_f32_e32 v75, v65
	v_mul_f32_e32 v65, v168, v67
	v_fract_f32_e32 v65, v65
	v_cos_f32_e32 v76, v65
	v_sin_f32_e32 v77, v65
	v_mul_f32_e32 v65, v169, v67
	v_fract_f32_e32 v65, v65
	v_cos_f32_e32 v78, v65
	v_sin_f32_e32 v79, v65
	v_mul_f32_e32 v65, v170, v67
	v_fract_f32_e32 v65, v65
	v_mov_b32_e32 v84, v60
	v_mov_b32_e32 v85, v56
	v_mov_b32_e32 v88, v69
	v_mov_b32_e32 v89, v68
	v_mov_b32_e32 v56, v61
	v_sin_f32_e32 v81, v65
	v_pk_mul_f32 v[86:87], v[68:69], v[84:85]
	v_pk_mul_f32 v[68:69], v[88:89], v[84:85]
	v_pk_mul_f32 v[60:61], v[70:71], v[56:57]
	v_mov_b32_e32 v84, v71
	v_mov_b32_e32 v85, v70
	v_mov_b32_e32 v70, v62
	v_mov_b32_e32 v71, v58
	v_cos_f32_e32 v80, v65
	v_pk_mul_f32 v[56:57], v[84:85], v[56:57]
	v_pk_mul_f32 v[84:85], v[72:73], v[70:71]
	v_mov_b32_e32 v88, v73
	v_mov_b32_e32 v89, v72
	v_mov_b32_e32 v58, v63
	v_mov_b32_e32 v72, v75
	v_mov_b32_e32 v73, v74
	v_mul_f32_e32 v65, v171, v67
	v_pk_mul_f32 v[62:63], v[74:75], v[58:59]
	v_pk_mul_f32 v[58:59], v[72:73], v[58:59]
	v_mov_b32_e32 v72, v52
	v_mov_b32_e32 v73, v48
	v_fract_f32_e32 v65, v65
	v_pk_mul_f32 v[70:71], v[88:89], v[70:71]
	v_pk_mul_f32 v[74:75], v[76:77], v[72:73]
	v_mov_b32_e32 v88, v77
	v_mov_b32_e32 v89, v76
	v_mov_b32_e32 v48, v53
	v_mov_b32_e32 v76, v79
	v_mov_b32_e32 v77, v78
	v_cos_f32_e32 v82, v65
	v_sin_f32_e32 v83, v65
	v_pk_mul_f32 v[52:53], v[78:79], v[48:49]
	v_pk_mul_f32 v[48:49], v[76:77], v[48:49]
	v_mov_b32_e32 v76, v54
	v_mov_b32_e32 v77, v50
	v_mov_b32_e32 v159, v81
	v_mov_b32_e32 v67, v54
	v_pk_mul_f32 v[76:77], v[80:81], v[76:77]
	v_pk_mul_f32 v[66:67], v[158:159], v[66:67]
	v_add_f32_e32 v48, v48, v49
	v_add_f32_e32 v65, v68, v69
	v_mul_f32_e32 v68, v66, v48
	v_sub_f32_e32 v48, v76, v77
	v_sub_f32_e32 v52, v52, v53
	v_mul_f32_e32 v53, v66, v48
	v_fma_f32 v48, v80, v50, v67
	v_mov_b32_e32 v50, v55
	v_mul_f32_e32 v67, v66, v48
	v_pk_mul_f32 v[48:49], v[82:83], v[50:51]
	v_pk_mul_f32 v[72:73], v[88:89], v[72:73]
	v_sub_f32_e32 v48, v48, v49
	v_mul_f32_e32 v55, v66, v48
	v_mov_b32_e32 v48, v83
	v_mov_b32_e32 v49, v82
	v_sub_f32_e32 v54, v86, v87
	v_pk_mul_f32 v[48:49], v[48:49], v[50:51]
	v_mul_f32_e32 v54, v66, v54
	v_sub_f32_e32 v60, v60, v61
	v_add_f32_e32 v56, v56, v57
	v_sub_f32_e32 v57, v84, v85
	v_add_f32_e32 v61, v70, v71
	v_sub_f32_e32 v62, v62, v63
	v_add_f32_e32 v58, v58, v59
	v_sub_f32_e32 v59, v74, v75
	v_add_f32_e32 v63, v72, v73
	v_mul_f32_e32 v52, v66, v52
	v_add_f32_e32 v48, v48, v49
	s_and_b64 vcc, exec, s[2:3]
	s_mov_b64 s[24:25], -1
	v_mul_f32_e32 v65, v66, v65
	v_mul_f32_e32 v60, v66, v60
	v_mul_f32_e32 v56, v66, v56
	v_mul_f32_e32 v57, v66, v57
	v_mul_f32_e32 v61, v66, v61
	v_mul_f32_e32 v62, v66, v62
	v_mul_f32_e32 v58, v66, v58
	v_mul_f32_e32 v59, v66, v59
	v_mul_f32_e32 v63, v66, v63
	v_mul_f32_e32 v66, v66, v48
	v_cvt_pk_bf16_f32 v48, v54, v60
	v_cvt_pk_bf16_f32 v49, v57, v62
	v_cvt_pk_bf16_f32 v50, v59, v52
	v_cvt_pk_bf16_f32 v51, v53, v55
	v_cvt_pk_bf16_f32 v52, v65, v56
	v_cvt_pk_bf16_f32 v53, v61, v58
	v_cvt_pk_bf16_f32 v54, v63, v68
	v_cvt_pk_bf16_f32 v55, v67, v66
	s_cbranch_vccnz .LBB0_172
	v_ashrrev_i32_e32 v65, 31, v64
	v_lshlrev_b64 v[56:57], 12, v[64:65]
	v_lshl_add_u64 v[56:57], v[156:157], 0, v[56:57]
	s_mov_b64 s[24:25], 0
	global_store_dwordx4 v[56:57], v[48:51], off nt
	global_store_dwordx4 v[56:57], v[52:55], off offset:256 nt
.LBB0_172:
	s_andn2_b64 vcc, exec, s[24:25]
	s_cbranch_vccnz .LBB0_174
	v_ashrrev_i32_e32 v56, 5, v64
	v_ashrrev_i32_e32 v57, 31, v56
	v_readlane_b32 s24, v250, 46
	s_ashr_i32 s7, s6, 31
	v_lshlrev_b64 v[56:57], 17, v[56:57]
	v_readlane_b32 s25, v250, 47
	v_mov_b32_e32 v123, v137
	v_mov_b32_e32 v121, v137
	v_lshl_add_u64 v[56:57], s[24:25], 0, v[56:57]
	s_lshl_b64 s[24:25], s[6:7], 14
	v_lshl_add_u64 v[56:57], v[56:57], 0, s[24:25]
	v_lshl_add_u64 v[56:57], v[56:57], 0, v[136:137]
	v_lshl_add_u64 v[56:57], v[56:57], 0, v[122:123]
	v_lshl_add_u64 v[56:57], v[56:57], 0, v[120:121]
	global_store_dwordx4 v[56:57], v[48:51], off nt
	s_nop 1
	v_add_co_u32_e32 v48, vcc, 0x2000, v56
	s_nop 1
	v_addc_co_u32_e32 v49, vcc, 0, v57, vcc
	global_store_dwordx4 v[48:49], v[52:55], off nt
.LBB0_174:
	v_add_u32_e32 v48, 0x90, v154
	v_mul_hi_i32 v49, v48, s82
	v_lshrrev_b32_e32 v50, 31, v49
	v_ashrrev_i32_e32 v49, 10, v49
	v_add_u32_e32 v49, v49, v50
	v_mul_i32_i24_e32 v49, 0x1080, v49
	v_sub_u32_e32 v49, v48, v49
	v_add_u32_e32 v50, 0xffffff90, v49
	v_cvt_f32_i32_e32 v51, v50
	v_bitop3_b32 v49, v49, s83, v177 bitop3:0x6c
	v_cvt_f32_ubyte0_e32 v49, v49
	v_mul_f32_e32 v49, v179, v49
	v_exp_f32_e32 v50, v49
	v_mul_f32_e32 v49, v143, v51
	v_fract_f32_e32 v49, v49
	v_cos_f32_e32 v52, v49
	v_sin_f32_e32 v53, v49
	v_mul_f32_e32 v49, v145, v51
	v_fract_f32_e32 v49, v49
	v_cos_f32_e32 v54, v49
	v_sin_f32_e32 v55, v49
	v_mul_f32_e32 v49, v166, v51
	v_fract_f32_e32 v49, v49
	v_cos_f32_e32 v56, v49
	v_sin_f32_e32 v57, v49
	v_mul_f32_e32 v49, v167, v51
	v_fract_f32_e32 v49, v49
	v_cos_f32_e32 v58, v49
	v_sin_f32_e32 v59, v49
	v_mul_f32_e32 v49, v168, v51
	v_fract_f32_e32 v49, v49
	v_cos_f32_e32 v60, v49
	v_sin_f32_e32 v61, v49
	v_mul_f32_e32 v49, v169, v51
	v_fract_f32_e32 v49, v49
	v_cos_f32_e32 v62, v49
	v_sin_f32_e32 v63, v49
	v_mul_f32_e32 v49, v170, v51
	v_fract_f32_e32 v49, v49
	v_mov_b32_e32 v68, v44
	v_mov_b32_e32 v69, v40
	v_mov_b32_e32 v72, v53
	v_mov_b32_e32 v73, v52
	v_mov_b32_e32 v40, v45
	v_sin_f32_e32 v65, v49
	v_pk_mul_f32 v[70:71], v[52:53], v[68:69]
	v_pk_mul_f32 v[52:53], v[72:73], v[68:69]
	v_pk_mul_f32 v[44:45], v[54:55], v[40:41]
	v_mov_b32_e32 v68, v55
	v_mov_b32_e32 v69, v54
	v_mov_b32_e32 v54, v46
	v_mov_b32_e32 v55, v42
	v_cos_f32_e32 v64, v49
	v_pk_mul_f32 v[40:41], v[68:69], v[40:41]
	v_pk_mul_f32 v[68:69], v[56:57], v[54:55]
	v_mov_b32_e32 v72, v57
	v_mov_b32_e32 v73, v56
	v_mov_b32_e32 v42, v47
	v_mov_b32_e32 v56, v59
	v_mov_b32_e32 v57, v58
	v_mul_f32_e32 v49, v171, v51
	v_pk_mul_f32 v[46:47], v[58:59], v[42:43]
	v_pk_mul_f32 v[42:43], v[56:57], v[42:43]
	v_mov_b32_e32 v56, v36
	v_mov_b32_e32 v57, v32
	v_fract_f32_e32 v49, v49
	v_pk_mul_f32 v[54:55], v[72:73], v[54:55]
	v_pk_mul_f32 v[58:59], v[60:61], v[56:57]
	v_mov_b32_e32 v72, v61
	v_mov_b32_e32 v73, v60
	v_mov_b32_e32 v32, v37
	v_mov_b32_e32 v60, v63
	v_mov_b32_e32 v61, v62
	v_cos_f32_e32 v66, v49
	v_sin_f32_e32 v67, v49
	v_pk_mul_f32 v[36:37], v[62:63], v[32:33]
	v_pk_mul_f32 v[32:33], v[60:61], v[32:33]
	v_mov_b32_e32 v60, v38
	v_mov_b32_e32 v61, v34
	v_mov_b32_e32 v159, v65
	v_mov_b32_e32 v51, v38
	v_pk_mul_f32 v[60:61], v[64:65], v[60:61]
	v_pk_mul_f32 v[50:51], v[158:159], v[50:51]
	v_add_f32_e32 v32, v32, v33
	v_add_f32_e32 v49, v52, v53
	v_mul_f32_e32 v52, v50, v32
	v_sub_f32_e32 v32, v60, v61
	v_sub_f32_e32 v36, v36, v37
	v_mul_f32_e32 v37, v50, v32
	v_fma_f32 v32, v64, v34, v51
	v_mov_b32_e32 v34, v39
	v_mul_f32_e32 v51, v50, v32
	v_pk_mul_f32 v[32:33], v[66:67], v[34:35]
	v_pk_mul_f32 v[56:57], v[72:73], v[56:57]
	v_sub_f32_e32 v32, v32, v33
	v_mul_f32_e32 v39, v50, v32
	v_mov_b32_e32 v32, v67
	v_mov_b32_e32 v33, v66
	v_sub_f32_e32 v38, v70, v71
	v_pk_mul_f32 v[32:33], v[32:33], v[34:35]
	v_mul_f32_e32 v38, v50, v38
	v_sub_f32_e32 v44, v44, v45
	v_add_f32_e32 v40, v40, v41
	v_sub_f32_e32 v41, v68, v69
	v_add_f32_e32 v45, v54, v55
	v_sub_f32_e32 v46, v46, v47
	v_add_f32_e32 v42, v42, v43
	v_sub_f32_e32 v43, v58, v59
	v_add_f32_e32 v47, v56, v57
	v_mul_f32_e32 v36, v50, v36
	v_add_f32_e32 v32, v32, v33
	s_and_b64 vcc, exec, s[2:3]
	s_mov_b64 s[24:25], -1
	v_mul_f32_e32 v49, v50, v49
	v_mul_f32_e32 v44, v50, v44
	v_mul_f32_e32 v40, v50, v40
	v_mul_f32_e32 v41, v50, v41
	v_mul_f32_e32 v45, v50, v45
	v_mul_f32_e32 v46, v50, v46
	v_mul_f32_e32 v42, v50, v42
	v_mul_f32_e32 v43, v50, v43
	v_mul_f32_e32 v47, v50, v47
	v_mul_f32_e32 v50, v50, v32
	v_cvt_pk_bf16_f32 v32, v38, v44
	v_cvt_pk_bf16_f32 v33, v41, v46
	v_cvt_pk_bf16_f32 v34, v43, v36
	v_cvt_pk_bf16_f32 v35, v37, v39
	v_cvt_pk_bf16_f32 v36, v49, v40
	v_cvt_pk_bf16_f32 v37, v45, v42
	v_cvt_pk_bf16_f32 v38, v47, v52
	v_cvt_pk_bf16_f32 v39, v51, v50
	s_cbranch_vccnz .LBB0_176
	v_ashrrev_i32_e32 v49, 31, v48
	v_lshlrev_b64 v[40:41], 12, v[48:49]
	v_lshl_add_u64 v[40:41], v[156:157], 0, v[40:41]
	s_mov_b64 s[24:25], 0
	global_store_dwordx4 v[40:41], v[32:35], off nt
	global_store_dwordx4 v[40:41], v[36:39], off offset:256 nt
.LBB0_176:
	s_andn2_b64 vcc, exec, s[24:25]
	s_cbranch_vccnz .LBB0_178
	v_ashrrev_i32_e32 v40, 5, v48
	v_ashrrev_i32_e32 v41, 31, v40
	v_readlane_b32 s24, v250, 46
	s_ashr_i32 s7, s6, 31
	v_lshlrev_b64 v[40:41], 17, v[40:41]
	v_readlane_b32 s25, v250, 47
	v_lshlrev_b32_e32 v42, 4, v48
	v_and_b32_e32 v42, 0x1f0, v42
	v_lshl_add_u64 v[40:41], s[24:25], 0, v[40:41]
	s_lshl_b64 s[24:25], s[6:7], 14
	v_lshl_add_u64 v[40:41], v[40:41], 0, s[24:25]
	v_mov_b32_e32 v43, v137
	v_lshl_add_u64 v[40:41], v[40:41], 0, v[42:43]
	v_mov_b32_e32 v123, v137
	v_lshl_add_u64 v[40:41], v[40:41], 0, v[122:123]
	v_mov_b32_e32 v121, v137
	v_lshl_add_u64 v[40:41], v[40:41], 0, v[120:121]
	global_store_dwordx4 v[40:41], v[32:35], off nt
	s_nop 1
	v_add_co_u32_e32 v32, vcc, 0x2000, v40
	s_nop 1
	v_addc_co_u32_e32 v33, vcc, 0, v41, vcc
	global_store_dwordx4 v[32:33], v[36:39], off nt
.LBB0_178:
	v_add_u32_e32 v32, 0xa0, v154
	v_mul_hi_i32 v33, v32, s82
	v_lshrrev_b32_e32 v34, 31, v33
	v_ashrrev_i32_e32 v33, 10, v33
	v_add_u32_e32 v33, v33, v34
	v_mul_i32_i24_e32 v33, 0x1080, v33
	v_sub_u32_e32 v33, v32, v33
	v_add_u32_e32 v34, 0xffffff90, v33
	v_cvt_f32_i32_e32 v35, v34
	v_bitop3_b32 v33, v33, s83, v178 bitop3:0x6c
	v_cvt_f32_ubyte0_e32 v33, v33
	v_mul_f32_e32 v33, v179, v33
	v_exp_f32_e32 v34, v33
	v_mul_f32_e32 v33, v143, v35
	v_fract_f32_e32 v33, v33
	v_cos_f32_e32 v36, v33
	v_sin_f32_e32 v37, v33
	v_mul_f32_e32 v33, v145, v35
	v_fract_f32_e32 v33, v33
	v_cos_f32_e32 v38, v33
	v_sin_f32_e32 v39, v33
	v_mul_f32_e32 v33, v166, v35
	v_fract_f32_e32 v33, v33
	v_cos_f32_e32 v40, v33
	v_sin_f32_e32 v41, v33
	v_mul_f32_e32 v33, v167, v35
	v_fract_f32_e32 v33, v33
	v_cos_f32_e32 v42, v33
	v_sin_f32_e32 v43, v33
	v_mul_f32_e32 v33, v168, v35
	v_fract_f32_e32 v33, v33
	v_cos_f32_e32 v44, v33
	v_sin_f32_e32 v45, v33
	v_mul_f32_e32 v33, v169, v35
	v_fract_f32_e32 v33, v33
	v_cos_f32_e32 v46, v33
	v_sin_f32_e32 v47, v33
	v_mul_f32_e32 v33, v170, v35
	v_fract_f32_e32 v33, v33
	v_mov_b32_e32 v52, v28
	v_mov_b32_e32 v53, v24
	v_mov_b32_e32 v56, v37
	v_mov_b32_e32 v57, v36
	v_mov_b32_e32 v24, v29
	v_sin_f32_e32 v49, v33
	v_pk_mul_f32 v[54:55], v[36:37], v[52:53]
	v_pk_mul_f32 v[36:37], v[56:57], v[52:53]
	v_pk_mul_f32 v[28:29], v[38:39], v[24:25]
	v_mov_b32_e32 v52, v39
	v_mov_b32_e32 v53, v38
	v_mov_b32_e32 v38, v30
	v_mov_b32_e32 v39, v26
	v_cos_f32_e32 v48, v33
	v_pk_mul_f32 v[24:25], v[52:53], v[24:25]
	v_pk_mul_f32 v[52:53], v[40:41], v[38:39]
	v_mov_b32_e32 v56, v41
	v_mov_b32_e32 v57, v40
	v_mov_b32_e32 v26, v31
	v_mov_b32_e32 v40, v43
	v_mov_b32_e32 v41, v42
	v_mul_f32_e32 v33, v171, v35
	v_pk_mul_f32 v[30:31], v[42:43], v[26:27]
	v_pk_mul_f32 v[26:27], v[40:41], v[26:27]
	v_mov_b32_e32 v40, v20
	v_mov_b32_e32 v41, v16
	v_fract_f32_e32 v33, v33
	v_pk_mul_f32 v[38:39], v[56:57], v[38:39]
	v_pk_mul_f32 v[42:43], v[44:45], v[40:41]
	v_mov_b32_e32 v56, v45
	v_mov_b32_e32 v57, v44
	v_mov_b32_e32 v16, v21
	v_mov_b32_e32 v44, v47
	v_mov_b32_e32 v45, v46
	v_cos_f32_e32 v50, v33
	v_sin_f32_e32 v51, v33
	v_pk_mul_f32 v[20:21], v[46:47], v[16:17]
	v_pk_mul_f32 v[16:17], v[44:45], v[16:17]
	v_mov_b32_e32 v44, v22
	v_mov_b32_e32 v45, v18
	v_mov_b32_e32 v159, v49
	v_mov_b32_e32 v35, v22
	v_pk_mul_f32 v[44:45], v[48:49], v[44:45]
	v_pk_mul_f32 v[34:35], v[158:159], v[34:35]
	v_add_f32_e32 v16, v16, v17
	v_add_f32_e32 v33, v36, v37
	v_mul_f32_e32 v36, v34, v16
	v_sub_f32_e32 v16, v44, v45
	v_sub_f32_e32 v20, v20, v21
	v_mul_f32_e32 v21, v34, v16
	v_fma_f32 v16, v48, v18, v35
	v_mov_b32_e32 v18, v23
	v_mul_f32_e32 v35, v34, v16
	v_pk_mul_f32 v[16:17], v[50:51], v[18:19]
	v_pk_mul_f32 v[40:41], v[56:57], v[40:41]
	v_sub_f32_e32 v16, v16, v17
	v_mul_f32_e32 v23, v34, v16
	v_mov_b32_e32 v16, v51
	v_mov_b32_e32 v17, v50
	v_sub_f32_e32 v22, v54, v55
	v_pk_mul_f32 v[16:17], v[16:17], v[18:19]
	v_mul_f32_e32 v22, v34, v22
	v_sub_f32_e32 v28, v28, v29
	v_add_f32_e32 v24, v24, v25
	v_sub_f32_e32 v25, v52, v53
	v_add_f32_e32 v29, v38, v39
	v_sub_f32_e32 v30, v30, v31
	v_add_f32_e32 v26, v26, v27
	v_sub_f32_e32 v27, v42, v43
	v_add_f32_e32 v31, v40, v41
	v_mul_f32_e32 v20, v34, v20
	v_add_f32_e32 v16, v16, v17
	s_and_b64 vcc, exec, s[2:3]
	s_mov_b64 s[24:25], -1
	v_mul_f32_e32 v33, v34, v33
	v_mul_f32_e32 v28, v34, v28
	v_mul_f32_e32 v24, v34, v24
	v_mul_f32_e32 v25, v34, v25
	v_mul_f32_e32 v29, v34, v29
	v_mul_f32_e32 v30, v34, v30
	v_mul_f32_e32 v26, v34, v26
	v_mul_f32_e32 v27, v34, v27
	v_mul_f32_e32 v31, v34, v31
	v_mul_f32_e32 v34, v34, v16
	v_cvt_pk_bf16_f32 v16, v22, v28
	v_cvt_pk_bf16_f32 v17, v25, v30
	v_cvt_pk_bf16_f32 v18, v27, v20
	v_cvt_pk_bf16_f32 v19, v21, v23
	v_cvt_pk_bf16_f32 v20, v33, v24
	v_cvt_pk_bf16_f32 v21, v29, v26
	v_cvt_pk_bf16_f32 v22, v31, v36
	v_cvt_pk_bf16_f32 v23, v35, v34
	s_cbranch_vccnz .LBB0_180
	v_ashrrev_i32_e32 v33, 31, v32
	v_lshlrev_b64 v[24:25], 12, v[32:33]
	v_lshl_add_u64 v[24:25], v[156:157], 0, v[24:25]
	s_mov_b64 s[24:25], 0
	global_store_dwordx4 v[24:25], v[16:19], off nt
	global_store_dwordx4 v[24:25], v[20:23], off offset:256 nt
.LBB0_180:
	s_andn2_b64 vcc, exec, s[24:25]
	s_cbranch_vccnz .LBB0_182
	v_ashrrev_i32_e32 v24, 5, v32
	v_ashrrev_i32_e32 v25, 31, v24
	v_readlane_b32 s24, v250, 46
	s_ashr_i32 s7, s6, 31
	v_lshlrev_b64 v[24:25], 17, v[24:25]
	v_readlane_b32 s25, v250, 47
	v_mov_b32_e32 v123, v137
	v_mov_b32_e32 v121, v137
	v_lshl_add_u64 v[24:25], s[24:25], 0, v[24:25]
	s_lshl_b64 s[24:25], s[6:7], 14
	v_lshl_add_u64 v[24:25], v[24:25], 0, s[24:25]
	v_lshl_add_u64 v[24:25], v[24:25], 0, v[136:137]
	v_lshl_add_u64 v[24:25], v[24:25], 0, v[122:123]
	v_lshl_add_u64 v[24:25], v[24:25], 0, v[120:121]
	global_store_dwordx4 v[24:25], v[16:19], off nt
	s_nop 1
	v_add_co_u32_e32 v16, vcc, 0x2000, v24
	s_nop 1
	v_addc_co_u32_e32 v17, vcc, 0, v25, vcc
	global_store_dwordx4 v[16:17], v[20:23], off nt
.LBB0_182:
	v_add_u32_e32 v16, 0xb0, v154
	v_mul_hi_i32 v17, v16, s82
	v_lshrrev_b32_e32 v18, 31, v17
	v_ashrrev_i32_e32 v17, 10, v17
	v_add_u32_e32 v17, v17, v18
	v_mul_i32_i24_e32 v17, 0x1080, v17
	v_sub_u32_e32 v17, v16, v17
	v_add_u32_e32 v18, 0xffffff90, v17
	v_cvt_f32_i32_e32 v19, v18
	v_bitop3_b32 v17, v17, s83, v17 bitop3:0xc
	v_cvt_f32_ubyte0_e32 v17, v17
	v_mul_f32_e32 v17, v179, v17
	v_exp_f32_e32 v18, v17
	v_mul_f32_e32 v17, v143, v19
	v_fract_f32_e32 v17, v17
	v_cos_f32_e32 v20, v17
	v_sin_f32_e32 v21, v17
	v_mul_f32_e32 v17, v145, v19
	v_fract_f32_e32 v17, v17
	v_cos_f32_e32 v22, v17
	v_sin_f32_e32 v23, v17
	v_mul_f32_e32 v17, v166, v19
	v_fract_f32_e32 v17, v17
	v_cos_f32_e32 v24, v17
	v_sin_f32_e32 v25, v17
	v_mul_f32_e32 v17, v167, v19
	v_fract_f32_e32 v17, v17
	v_cos_f32_e32 v26, v17
	v_sin_f32_e32 v27, v17
	v_mul_f32_e32 v17, v168, v19
	v_fract_f32_e32 v17, v17
	v_cos_f32_e32 v28, v17
	v_sin_f32_e32 v29, v17
	v_mul_f32_e32 v17, v169, v19
	v_fract_f32_e32 v17, v17
	v_cos_f32_e32 v30, v17
	v_sin_f32_e32 v31, v17
	v_mul_f32_e32 v17, v170, v19
	v_fract_f32_e32 v17, v17
	v_mov_b32_e32 v36, v12
	v_mov_b32_e32 v37, v8
	v_mov_b32_e32 v40, v21
	v_mov_b32_e32 v41, v20
	v_mov_b32_e32 v8, v13
	v_sin_f32_e32 v33, v17
	v_pk_mul_f32 v[38:39], v[20:21], v[36:37]
	v_pk_mul_f32 v[20:21], v[40:41], v[36:37]
	v_pk_mul_f32 v[12:13], v[22:23], v[8:9]
	v_mov_b32_e32 v36, v23
	v_mov_b32_e32 v37, v22
	v_mov_b32_e32 v22, v14
	v_mov_b32_e32 v23, v10
	v_cos_f32_e32 v32, v17
	v_pk_mul_f32 v[8:9], v[36:37], v[8:9]
	v_pk_mul_f32 v[36:37], v[24:25], v[22:23]
	v_mov_b32_e32 v40, v25
	v_mov_b32_e32 v41, v24
	v_mov_b32_e32 v10, v15
	v_mov_b32_e32 v24, v27
	v_mov_b32_e32 v25, v26
	v_mul_f32_e32 v17, v171, v19
	v_pk_mul_f32 v[14:15], v[26:27], v[10:11]
	v_pk_mul_f32 v[10:11], v[24:25], v[10:11]
	v_mov_b32_e32 v24, v4
	v_mov_b32_e32 v25, v0
	v_fract_f32_e32 v17, v17
	v_pk_mul_f32 v[22:23], v[40:41], v[22:23]
	v_pk_mul_f32 v[26:27], v[28:29], v[24:25]
	v_mov_b32_e32 v40, v29
	v_mov_b32_e32 v41, v28
	v_mov_b32_e32 v0, v5
	v_mov_b32_e32 v28, v31
	v_mov_b32_e32 v29, v30
	v_cos_f32_e32 v34, v17
	v_sin_f32_e32 v35, v17
	v_pk_mul_f32 v[4:5], v[30:31], v[0:1]
	v_pk_mul_f32 v[0:1], v[28:29], v[0:1]
	v_mov_b32_e32 v28, v6
	v_mov_b32_e32 v29, v2
	v_mov_b32_e32 v159, v33
	v_mov_b32_e32 v19, v6
	v_pk_mul_f32 v[28:29], v[32:33], v[28:29]
	v_pk_mul_f32 v[18:19], v[158:159], v[18:19]
	v_add_f32_e32 v0, v0, v1
	v_add_f32_e32 v17, v20, v21
	v_mul_f32_e32 v20, v18, v0
	v_sub_f32_e32 v0, v28, v29
	v_sub_f32_e32 v4, v4, v5
	v_mul_f32_e32 v5, v18, v0
	v_fma_f32 v0, v32, v2, v19
	v_mov_b32_e32 v2, v7
	v_mul_f32_e32 v19, v18, v0
	v_pk_mul_f32 v[0:1], v[34:35], v[2:3]
	v_pk_mul_f32 v[24:25], v[40:41], v[24:25]
	v_sub_f32_e32 v0, v0, v1
	v_mul_f32_e32 v7, v18, v0
	v_mov_b32_e32 v0, v35
	v_mov_b32_e32 v1, v34
	v_sub_f32_e32 v6, v38, v39
	v_pk_mul_f32 v[0:1], v[0:1], v[2:3]
	v_mul_f32_e32 v6, v18, v6
	v_sub_f32_e32 v12, v12, v13
	v_add_f32_e32 v8, v8, v9
	v_sub_f32_e32 v9, v36, v37
	v_add_f32_e32 v13, v22, v23
	v_sub_f32_e32 v14, v14, v15
	v_add_f32_e32 v10, v10, v11
	v_sub_f32_e32 v11, v26, v27
	v_add_f32_e32 v15, v24, v25
	v_mul_f32_e32 v4, v18, v4
	v_add_f32_e32 v0, v0, v1
	s_and_b64 vcc, exec, s[2:3]
	s_mov_b64 s[2:3], -1
	v_mul_f32_e32 v17, v18, v17
	v_mul_f32_e32 v12, v18, v12
	v_mul_f32_e32 v8, v18, v8
	v_mul_f32_e32 v9, v18, v9
	v_mul_f32_e32 v13, v18, v13
	v_mul_f32_e32 v14, v18, v14
	v_mul_f32_e32 v10, v18, v10
	v_mul_f32_e32 v11, v18, v11
	v_mul_f32_e32 v15, v18, v15
	v_mul_f32_e32 v18, v18, v0
	v_cvt_pk_bf16_f32 v0, v6, v12
	v_cvt_pk_bf16_f32 v1, v9, v14
	v_cvt_pk_bf16_f32 v2, v11, v4
	v_cvt_pk_bf16_f32 v3, v5, v7
	v_cvt_pk_bf16_f32 v4, v17, v8
	v_cvt_pk_bf16_f32 v5, v13, v10
	v_cvt_pk_bf16_f32 v6, v15, v20
	v_cvt_pk_bf16_f32 v7, v19, v18
	s_cbranch_vccnz .LBB0_184
	v_ashrrev_i32_e32 v17, 31, v16
	v_lshlrev_b64 v[8:9], 12, v[16:17]
	v_lshl_add_u64 v[8:9], v[156:157], 0, v[8:9]
	s_mov_b64 s[2:3], 0
	global_store_dwordx4 v[8:9], v[0:3], off nt
	global_store_dwordx4 v[8:9], v[4:7], off offset:256 nt
.LBB0_184:
	s_andn2_b64 vcc, exec, s[2:3]
	s_cbranch_vccnz .LBB0_186
	v_ashrrev_i32_e32 v8, 5, v16
	v_ashrrev_i32_e32 v9, 31, v8
	v_readlane_b32 s2, v250, 46
	s_ashr_i32 s7, s6, 31
	v_lshlrev_b64 v[8:9], 17, v[8:9]
	v_readlane_b32 s3, v250, 47
	v_lshlrev_b32_e32 v10, 4, v16
	v_and_b32_e32 v136, 0x1f0, v10
	v_lshl_add_u64 v[8:9], s[2:3], 0, v[8:9]
	s_lshl_b64 s[2:3], s[6:7], 14
	v_lshl_add_u64 v[8:9], v[8:9], 0, s[2:3]
	v_lshl_add_u64 v[8:9], v[8:9], 0, v[136:137]
	v_mov_b32_e32 v123, v137
	v_lshl_add_u64 v[8:9], v[8:9], 0, v[122:123]
	v_mov_b32_e32 v121, v137
	v_lshl_add_u64 v[8:9], v[8:9], 0, v[120:121]
	global_store_dwordx4 v[8:9], v[0:3], off nt
	s_nop 1
	v_add_co_u32_e32 v0, vcc, 0x2000, v8
	s_nop 1
	v_addc_co_u32_e32 v1, vcc, 0, v9, vcc
	global_store_dwordx4 v[0:1], v[4:7], off nt

.LBB0_425:
	s_andn2_saveexec_b64 s[22:23], s[22:23]
	v_max_i32_e32 v136, 0x70, v158
	v_add_u32_e32 v136, 0xffffff90, v136
	s_or_b64 exec, exec, s[22:23]
	v_lshl_or_b32 v146, s18, 8, v154
	v_lshlrev_b64 v[160:161], 13, v[136:137]
	v_ashrrev_i32_e32 v147, 31, v146
	v_lshl_add_u64 v[150:151], v[150:151], 0, v[160:161]
	v_lshl_add_u64 v[150:151], v[146:147], 2, v[150:151]
	global_load_dwordx4 v[160:163], v[150:151], off
	global_load_dwordx4 v[164:167], v[150:151], off offset:16
	v_ashrrev_i32_e32 v149, 31, v148
	v_cmp_gt_i32_e32 vcc, s46, v158
	v_lshlrev_b64 v[158:159], 12, v[148:149]
	v_lshl_add_u64 v[158:159], s[96:97], 0, v[158:159]
	v_cndmask_b32_e64 v136, 1.0, 0, vcc
	v_lshl_add_u64 v[168:169], v[146:147], 1, v[158:159]
	v_readlane_b32 s76, v250, 7
	v_readlane_b32 s78, v250, 9
	v_readlane_b32 s79, v250, 10
	v_readlane_b32 s77, v250, 8
	v_readlane_b32 s80, v250, 11
	v_readlane_b32 s81, v250, 12
	v_readlane_b32 s82, v250, 13
	v_readlane_b32 s83, v250, 14
	v_readlane_b32 s84, v250, 15
	v_readlane_b32 s85, v250, 16
	v_readlane_b32 s86, v250, 17
	v_readlane_b32 s87, v250, 18
	v_readlane_b32 s88, v250, 19
	v_readlane_b32 s89, v250, 20
	v_readlane_b32 s90, v250, 21
	v_readlane_b32 s91, v250, 22
	s_waitcnt vmcnt(0)
	v_fma_f32 v124, v136, v160, v124
	v_fmac_f32_e32 v123, v136, v167
	v_fma_f32 v125, v136, v161, v125
	v_fma_f32 v126, v136, v162, v126
	v_fmac_f32_e32 v127, v136, v163
	v_fma_f32 v149, v136, v164, v120
	v_fma_f32 v158, v136, v165, v121
	v_fma_f32 v159, v136, v166, v122
	v_cvt_pk_bf16_f32 v120, v124, v125
	v_cvt_pk_bf16_f32 v121, v126, v127
	v_cvt_pk_bf16_f32 v122, v149, v158
	v_cvt_pk_bf16_f32 v123, v159, v123
	global_store_dwordx4 v[168:169], v[120:123], off nt
	global_load_dwordx4 v[158:161], v[150:151], off offset:512
	global_load_dwordx4 v[162:165], v[150:151], off offset:528
	v_or_b32_e32 v120, 16, v148
	v_mul_hi_i32 v121, v120, s43
	v_lshrrev_b32_e32 v122, 31, v121
	v_ashrrev_i32_e32 v121, 10, v121
	v_add_u32_e32 v122, v121, v122
	v_mad_i32_i24 v124, v122, s44, v120
	v_cmp_lt_i32_e32 vcc, s45, v124
	s_waitcnt vmcnt(1)
	v_fma_f32 v116, v136, v158, v116
	v_fma_f32 v117, v136, v159, v117
	v_fma_f32 v118, v136, v160, v118
	v_fmac_f32_e32 v119, v136, v161
	s_waitcnt vmcnt(0)
	v_fma_f32 v121, v136, v162, v112
	v_fma_f32 v123, v136, v163, v113
	v_fmac_f32_e32 v115, v136, v165
	v_cvt_pk_bf16_f32 v112, v116, v117
	v_cvt_pk_bf16_f32 v113, v118, v119
	v_fma_f32 v125, v136, v164, v114
	v_cvt_pk_bf16_f32 v114, v121, v123
	v_cvt_pk_bf16_f32 v115, v125, v115
	global_store_dwordx4 v[168:169], v[112:115], off offset:256 nt
	s_nop 1
	v_mov_b64_e32 v[112:113], s[78:79]
	s_and_saveexec_b64 s[18:19], vcc
	s_xor_b64 s[18:19], exec, s[18:19]
	s_mov_b32 s60, s66
	v_readlane_b32 s59, v250, 50
	s_cbranch_execz .LBB0_429
	v_ashrrev_i32_e32 v123, 31, v122
	v_readlane_b32 s76, v250, 7
	v_lshlrev_b64 v[112:113], 25, v[122:123]
	v_readlane_b32 s77, v250, 8
	v_add_u32_e32 v136, 0xffffff80, v124
	v_readlane_b32 s78, v250, 9
	v_lshl_add_u64 v[112:113], s[76:77], 0, v[112:113]
	v_readlane_b32 s79, v250, 10
	v_readlane_b32 s80, v250, 11
	v_readlane_b32 s81, v250, 12
	v_readlane_b32 s82, v250, 13
	v_readlane_b32 s83, v250, 14
	v_readlane_b32 s84, v250, 15
	v_readlane_b32 s85, v250, 16
	v_readlane_b32 s86, v250, 17
	v_readlane_b32 s87, v250, 18
	v_readlane_b32 s88, v250, 19
	v_readlane_b32 s89, v250, 20
	v_readlane_b32 s90, v250, 21
	v_readlane_b32 s91, v250, 22
.LBB0_429:
	s_andn2_saveexec_b64 s[18:19], s[18:19]
	v_max_i32_e32 v114, 0x70, v124
	v_add_u32_e32 v136, 0xffffff90, v114
	s_or_b64 exec, exec, s[18:19]
	v_lshlrev_b64 v[114:115], 13, v[136:137]
	v_lshl_add_u64 v[112:113], v[112:113], 0, v[114:115]
	v_lshl_add_u64 v[122:123], v[146:147], 2, v[112:113]
	global_load_dwordx4 v[112:115], v[122:123], off
	global_load_dwordx4 v[116:119], v[122:123], off offset:16
	v_ashrrev_i32_e32 v121, 31, v120
	v_cmp_gt_i32_e32 vcc, s46, v124
	v_lshlrev_b64 v[120:121], 12, v[120:121]
	v_lshl_add_u64 v[120:121], s[96:97], 0, v[120:121]
	v_cndmask_b32_e64 v124, 1.0, 0, vcc
	v_lshl_add_u64 v[120:121], v[146:147], 1, v[120:121]
	v_readlane_b32 s76, v250, 7
	v_readlane_b32 s78, v250, 9
	v_readlane_b32 s79, v250, 10
	v_readlane_b32 s77, v250, 8
	v_readlane_b32 s80, v250, 11
	v_readlane_b32 s81, v250, 12
	v_readlane_b32 s82, v250, 13
	v_readlane_b32 s83, v250, 14
	v_readlane_b32 s84, v250, 15
	v_readlane_b32 s85, v250, 16
	v_readlane_b32 s86, v250, 17
	v_readlane_b32 s87, v250, 18
	v_readlane_b32 s88, v250, 19
	v_readlane_b32 s89, v250, 20
	v_readlane_b32 s90, v250, 21
	v_readlane_b32 s91, v250, 22
	s_waitcnt vmcnt(1)
	v_fma_f32 v108, v124, v112, v108
	s_waitcnt vmcnt(0)
	v_fmac_f32_e32 v107, v124, v119
	v_fma_f32 v109, v124, v113, v109
	v_fma_f32 v110, v124, v114, v110
	v_fmac_f32_e32 v111, v124, v115
	v_fma_f32 v112, v124, v116, v104
	v_fma_f32 v113, v124, v117, v105
	v_fma_f32 v114, v124, v118, v106
	v_cvt_pk_bf16_f32 v104, v108, v109
	v_cvt_pk_bf16_f32 v105, v110, v111
	v_cvt_pk_bf16_f32 v106, v112, v113
	v_cvt_pk_bf16_f32 v107, v114, v107
	global_store_dwordx4 v[120:121], v[104:107], off nt
	global_load_dwordx4 v[110:113], v[122:123], off offset:512
	global_load_dwordx4 v[114:117], v[122:123], off offset:528
	v_or_b32_e32 v104, 32, v148
	v_mul_hi_i32 v105, v104, s43
	v_lshrrev_b32_e32 v106, 31, v105
	v_ashrrev_i32_e32 v105, 10, v105
	v_add_u32_e32 v106, v105, v106
	v_mad_i32_i24 v108, v106, s44, v104
	v_cmp_lt_i32_e32 vcc, s45, v108
	s_waitcnt vmcnt(1)
	v_fma_f32 v100, v124, v110, v100
	v_fma_f32 v101, v124, v111, v101
	v_fma_f32 v102, v124, v112, v102
	v_fmac_f32_e32 v103, v124, v113
	s_waitcnt vmcnt(0)
	v_fma_f32 v105, v124, v114, v96
	v_fma_f32 v107, v124, v115, v97
	v_fmac_f32_e32 v99, v124, v117
	v_cvt_pk_bf16_f32 v96, v100, v101
	v_cvt_pk_bf16_f32 v97, v102, v103
	v_fma_f32 v109, v124, v116, v98
	v_cvt_pk_bf16_f32 v98, v105, v107
	v_cvt_pk_bf16_f32 v99, v109, v99
	global_store_dwordx4 v[120:121], v[96:99], off offset:256 nt
	s_nop 1
	v_mov_b64_e32 v[96:97], s[78:79]
	s_and_saveexec_b64 s[18:19], vcc
	s_xor_b64 s[18:19], exec, s[18:19]
	s_cbranch_execz .LBB0_433
	v_ashrrev_i32_e32 v107, 31, v106
	v_readlane_b32 s76, v250, 7
	v_lshlrev_b64 v[96:97], 25, v[106:107]
	v_readlane_b32 s77, v250, 8
	v_add_u32_e32 v136, 0xffffff80, v108
	v_readlane_b32 s78, v250, 9
	v_lshl_add_u64 v[96:97], s[76:77], 0, v[96:97]
	v_readlane_b32 s79, v250, 10
	v_readlane_b32 s80, v250, 11
	v_readlane_b32 s81, v250, 12
	v_readlane_b32 s82, v250, 13
	v_readlane_b32 s83, v250, 14
	v_readlane_b32 s84, v250, 15
	v_readlane_b32 s85, v250, 16
	v_readlane_b32 s86, v250, 17
	v_readlane_b32 s87, v250, 18
	v_readlane_b32 s88, v250, 19
	v_readlane_b32 s89, v250, 20
	v_readlane_b32 s90, v250, 21
	v_readlane_b32 s91, v250, 22
.LBB0_433:
	s_andn2_saveexec_b64 s[18:19], s[18:19]
	v_max_i32_e32 v98, 0x70, v108
	v_add_u32_e32 v136, 0xffffff90, v98
	s_or_b64 exec, exec, s[18:19]
	v_lshlrev_b64 v[98:99], 13, v[136:137]
	v_lshl_add_u64 v[96:97], v[96:97], 0, v[98:99]
	v_lshl_add_u64 v[106:107], v[146:147], 2, v[96:97]
	global_load_dwordx4 v[96:99], v[106:107], off
	global_load_dwordx4 v[100:103], v[106:107], off offset:16
	v_ashrrev_i32_e32 v105, 31, v104
	v_cmp_gt_i32_e32 vcc, s46, v108
	v_lshlrev_b64 v[104:105], 12, v[104:105]
	v_lshl_add_u64 v[104:105], s[96:97], 0, v[104:105]
	v_cndmask_b32_e64 v108, 1.0, 0, vcc
	v_lshl_add_u64 v[104:105], v[146:147], 1, v[104:105]
	v_readlane_b32 s76, v250, 7
	v_readlane_b32 s78, v250, 9
	v_readlane_b32 s79, v250, 10
	v_readlane_b32 s77, v250, 8
	v_readlane_b32 s80, v250, 11
	v_readlane_b32 s81, v250, 12
	v_readlane_b32 s82, v250, 13
	v_readlane_b32 s83, v250, 14
	v_readlane_b32 s84, v250, 15
	v_readlane_b32 s85, v250, 16
	v_readlane_b32 s86, v250, 17
	v_readlane_b32 s87, v250, 18
	v_readlane_b32 s88, v250, 19
	v_readlane_b32 s89, v250, 20
	v_readlane_b32 s90, v250, 21
	v_readlane_b32 s91, v250, 22
	s_waitcnt vmcnt(1)
	v_fma_f32 v92, v108, v96, v92
	s_waitcnt vmcnt(0)
	v_fmac_f32_e32 v91, v108, v103
	v_fma_f32 v93, v108, v97, v93
	v_fma_f32 v94, v108, v98, v94
	v_fmac_f32_e32 v95, v108, v99
	v_fma_f32 v96, v108, v100, v88
	v_fma_f32 v97, v108, v101, v89
	v_fma_f32 v98, v108, v102, v90
	v_cvt_pk_bf16_f32 v88, v92, v93
	v_cvt_pk_bf16_f32 v89, v94, v95
	v_cvt_pk_bf16_f32 v90, v96, v97
	v_cvt_pk_bf16_f32 v91, v98, v91
	global_store_dwordx4 v[104:105], v[88:91], off nt
	global_load_dwordx4 v[94:97], v[106:107], off offset:512
	global_load_dwordx4 v[98:101], v[106:107], off offset:528
	v_or_b32_e32 v88, 48, v148
	v_mul_hi_i32 v89, v88, s43
	v_lshrrev_b32_e32 v90, 31, v89
	v_ashrrev_i32_e32 v89, 10, v89
	v_add_u32_e32 v90, v89, v90
	v_mad_i32_i24 v92, v90, s44, v88
	v_cmp_lt_i32_e32 vcc, s45, v92
	s_waitcnt vmcnt(1)
	v_fma_f32 v84, v108, v94, v84
	v_fma_f32 v85, v108, v95, v85
	v_fma_f32 v86, v108, v96, v86
	v_fmac_f32_e32 v87, v108, v97
	s_waitcnt vmcnt(0)
	v_fma_f32 v89, v108, v98, v80
	v_fma_f32 v91, v108, v99, v81
	v_fmac_f32_e32 v83, v108, v101
	v_cvt_pk_bf16_f32 v80, v84, v85
	v_cvt_pk_bf16_f32 v81, v86, v87
	v_fma_f32 v93, v108, v100, v82
	v_cvt_pk_bf16_f32 v82, v89, v91
	v_cvt_pk_bf16_f32 v83, v93, v83
	global_store_dwordx4 v[104:105], v[80:83], off offset:256 nt
	s_nop 1
	v_mov_b64_e32 v[80:81], s[78:79]
	s_and_saveexec_b64 s[18:19], vcc
	s_xor_b64 s[18:19], exec, s[18:19]
	s_cbranch_execz .LBB0_437
	v_ashrrev_i32_e32 v91, 31, v90
	v_readlane_b32 s76, v250, 7
	v_lshlrev_b64 v[80:81], 25, v[90:91]
	v_readlane_b32 s77, v250, 8
	v_add_u32_e32 v136, 0xffffff80, v92
	v_readlane_b32 s78, v250, 9
	v_lshl_add_u64 v[80:81], s[76:77], 0, v[80:81]
	v_readlane_b32 s79, v250, 10
	v_readlane_b32 s80, v250, 11
	v_readlane_b32 s81, v250, 12
	v_readlane_b32 s82, v250, 13
	v_readlane_b32 s83, v250, 14
	v_readlane_b32 s84, v250, 15
	v_readlane_b32 s85, v250, 16
	v_readlane_b32 s86, v250, 17
	v_readlane_b32 s87, v250, 18
	v_readlane_b32 s88, v250, 19
	v_readlane_b32 s89, v250, 20
	v_readlane_b32 s90, v250, 21
	v_readlane_b32 s91, v250, 22
.LBB0_437:
	s_andn2_saveexec_b64 s[18:19], s[18:19]
	v_max_i32_e32 v82, 0x70, v92
	v_add_u32_e32 v136, 0xffffff90, v82
	s_or_b64 exec, exec, s[18:19]
	v_lshlrev_b64 v[82:83], 13, v[136:137]
	v_lshl_add_u64 v[80:81], v[80:81], 0, v[82:83]
	v_lshl_add_u64 v[90:91], v[146:147], 2, v[80:81]
	global_load_dwordx4 v[80:83], v[90:91], off
	global_load_dwordx4 v[84:87], v[90:91], off offset:16
	v_ashrrev_i32_e32 v89, 31, v88
	v_cmp_gt_i32_e32 vcc, s46, v92
	v_lshlrev_b64 v[88:89], 12, v[88:89]
	v_lshl_add_u64 v[88:89], s[96:97], 0, v[88:89]
	v_cndmask_b32_e64 v92, 1.0, 0, vcc
	v_lshl_add_u64 v[88:89], v[146:147], 1, v[88:89]
	v_readlane_b32 s76, v250, 7
	v_readlane_b32 s78, v250, 9
	v_readlane_b32 s79, v250, 10
	v_readlane_b32 s77, v250, 8
	v_readlane_b32 s80, v250, 11
	v_readlane_b32 s81, v250, 12
	v_readlane_b32 s82, v250, 13
	v_readlane_b32 s83, v250, 14
	v_readlane_b32 s84, v250, 15
	v_readlane_b32 s85, v250, 16
	v_readlane_b32 s86, v250, 17
	v_readlane_b32 s87, v250, 18
	v_readlane_b32 s88, v250, 19
	v_readlane_b32 s89, v250, 20
	v_readlane_b32 s90, v250, 21
	v_readlane_b32 s91, v250, 22
	s_waitcnt vmcnt(1)
	v_fma_f32 v76, v92, v80, v76
	s_waitcnt vmcnt(0)
	v_fmac_f32_e32 v75, v92, v87
	v_fma_f32 v77, v92, v81, v77
	v_fma_f32 v78, v92, v82, v78
	v_fmac_f32_e32 v79, v92, v83
	v_fma_f32 v80, v92, v84, v72
	v_fma_f32 v81, v92, v85, v73
	v_fma_f32 v82, v92, v86, v74
	v_cvt_pk_bf16_f32 v72, v76, v77
	v_cvt_pk_bf16_f32 v73, v78, v79
	v_cvt_pk_bf16_f32 v74, v80, v81
	v_cvt_pk_bf16_f32 v75, v82, v75
	global_store_dwordx4 v[88:89], v[72:75], off nt
	global_load_dwordx4 v[78:81], v[90:91], off offset:512
	global_load_dwordx4 v[82:85], v[90:91], off offset:528
	v_add_u32_e32 v72, 0x80, v148
	v_mul_hi_i32 v73, v72, s43
	v_lshrrev_b32_e32 v74, 31, v73
	v_ashrrev_i32_e32 v73, 10, v73
	v_add_u32_e32 v74, v73, v74
	v_mad_i32_i24 v76, v74, s44, v72
	v_cmp_lt_i32_e32 vcc, s45, v76
	s_waitcnt vmcnt(1)
	v_fma_f32 v68, v92, v78, v68
	v_fma_f32 v69, v92, v79, v69
	v_fma_f32 v70, v92, v80, v70
	v_fmac_f32_e32 v71, v92, v81
	s_waitcnt vmcnt(0)
	v_fma_f32 v73, v92, v82, v64
	v_fma_f32 v75, v92, v83, v65
	v_fmac_f32_e32 v67, v92, v85
	v_cvt_pk_bf16_f32 v64, v68, v69
	v_cvt_pk_bf16_f32 v65, v70, v71
	v_fma_f32 v77, v92, v84, v66
	v_cvt_pk_bf16_f32 v66, v73, v75
	v_cvt_pk_bf16_f32 v67, v77, v67
	global_store_dwordx4 v[88:89], v[64:67], off offset:256 nt
	s_nop 1
	v_mov_b64_e32 v[64:65], s[78:79]
	s_and_saveexec_b64 s[18:19], vcc
	s_xor_b64 s[18:19], exec, s[18:19]
	s_cbranch_execz .LBB0_441
	v_mul_i32_i24_e32 v64, 0xffffef80, v74
	v_ashrrev_i32_e32 v75, 31, v74
	v_readlane_b32 s76, v250, 7
	v_add_u32_e32 v136, v64, v148
	v_lshlrev_b64 v[64:65], 25, v[74:75]
	v_readlane_b32 s77, v250, 8
	v_readlane_b32 s78, v250, 9
	v_readlane_b32 s79, v250, 10
	v_lshl_add_u64 v[64:65], s[76:77], 0, v[64:65]
	v_readlane_b32 s80, v250, 11
	v_readlane_b32 s81, v250, 12
	v_readlane_b32 s82, v250, 13
	v_readlane_b32 s83, v250, 14
	v_readlane_b32 s84, v250, 15
	v_readlane_b32 s85, v250, 16
	v_readlane_b32 s86, v250, 17
	v_readlane_b32 s87, v250, 18
	v_readlane_b32 s88, v250, 19
	v_readlane_b32 s89, v250, 20
	v_readlane_b32 s90, v250, 21
	v_readlane_b32 s91, v250, 22
.LBB0_441:
	s_andn2_saveexec_b64 s[18:19], s[18:19]
	v_max_i32_e32 v66, 0x70, v76
	v_add_u32_e32 v136, 0xffffff90, v66
	s_or_b64 exec, exec, s[18:19]
	v_lshlrev_b64 v[66:67], 13, v[136:137]
	v_lshl_add_u64 v[64:65], v[64:65], 0, v[66:67]
	v_lshl_add_u64 v[74:75], v[146:147], 2, v[64:65]
	global_load_dwordx4 v[64:67], v[74:75], off
	global_load_dwordx4 v[68:71], v[74:75], off offset:16
	v_ashrrev_i32_e32 v73, 31, v72
	v_cmp_gt_i32_e32 vcc, s46, v76
	v_lshlrev_b64 v[72:73], 12, v[72:73]
	v_lshl_add_u64 v[72:73], s[96:97], 0, v[72:73]
	v_cndmask_b32_e64 v76, 1.0, 0, vcc
	v_lshl_add_u64 v[72:73], v[146:147], 1, v[72:73]
	v_readlane_b32 s76, v250, 7
	v_readlane_b32 s78, v250, 9
	v_readlane_b32 s79, v250, 10
	v_readlane_b32 s77, v250, 8
	v_readlane_b32 s80, v250, 11
	v_readlane_b32 s81, v250, 12
	v_readlane_b32 s82, v250, 13
	v_readlane_b32 s83, v250, 14
	v_readlane_b32 s84, v250, 15
	v_readlane_b32 s85, v250, 16
	v_readlane_b32 s86, v250, 17
	v_readlane_b32 s87, v250, 18
	v_readlane_b32 s88, v250, 19
	v_readlane_b32 s89, v250, 20
	v_readlane_b32 s90, v250, 21
	v_readlane_b32 s91, v250, 22
	s_waitcnt vmcnt(1)
	v_fma_f32 v60, v76, v64, v60
	s_waitcnt vmcnt(0)
	v_fmac_f32_e32 v59, v76, v71
	v_fma_f32 v61, v76, v65, v61
	v_fma_f32 v62, v76, v66, v62
	v_fmac_f32_e32 v63, v76, v67
	v_fma_f32 v64, v76, v68, v56
	v_fma_f32 v65, v76, v69, v57
	v_fma_f32 v66, v76, v70, v58
	v_cvt_pk_bf16_f32 v56, v60, v61
	v_cvt_pk_bf16_f32 v57, v62, v63
	v_cvt_pk_bf16_f32 v58, v64, v65
	v_cvt_pk_bf16_f32 v59, v66, v59
	global_store_dwordx4 v[72:73], v[56:59], off nt
	global_load_dwordx4 v[62:65], v[74:75], off offset:512
	global_load_dwordx4 v[66:69], v[74:75], off offset:528
	v_add_u32_e32 v56, 0x90, v148
	v_mul_hi_i32 v57, v56, s43
	v_lshrrev_b32_e32 v58, 31, v57
	v_ashrrev_i32_e32 v57, 10, v57
	v_add_u32_e32 v58, v57, v58
	v_mad_i32_i24 v60, v58, s44, v56
	v_cmp_lt_i32_e32 vcc, s45, v60
	s_waitcnt vmcnt(1)
	v_fma_f32 v52, v76, v62, v52
	v_fma_f32 v53, v76, v63, v53
	v_fma_f32 v54, v76, v64, v54
	v_fmac_f32_e32 v55, v76, v65
	s_waitcnt vmcnt(0)
	v_fma_f32 v57, v76, v66, v48
	v_fma_f32 v59, v76, v67, v49
	v_fmac_f32_e32 v51, v76, v69
	v_cvt_pk_bf16_f32 v48, v52, v53
	v_cvt_pk_bf16_f32 v49, v54, v55
	v_fma_f32 v61, v76, v68, v50
	v_cvt_pk_bf16_f32 v50, v57, v59
	v_cvt_pk_bf16_f32 v51, v61, v51
	global_store_dwordx4 v[72:73], v[48:51], off offset:256 nt
	s_nop 1
	v_mov_b64_e32 v[48:49], s[78:79]
	s_and_saveexec_b64 s[18:19], vcc
	s_xor_b64 s[18:19], exec, s[18:19]
	s_cbranch_execz .LBB0_445
	v_ashrrev_i32_e32 v59, 31, v58
	v_readlane_b32 s76, v250, 7
	v_lshlrev_b64 v[48:49], 25, v[58:59]
	v_readlane_b32 s77, v250, 8
	v_add_u32_e32 v136, 0xffffff80, v60
	v_readlane_b32 s78, v250, 9
	v_lshl_add_u64 v[48:49], s[76:77], 0, v[48:49]
	v_readlane_b32 s79, v250, 10
	v_readlane_b32 s80, v250, 11
	v_readlane_b32 s81, v250, 12
	v_readlane_b32 s82, v250, 13
	v_readlane_b32 s83, v250, 14
	v_readlane_b32 s84, v250, 15
	v_readlane_b32 s85, v250, 16
	v_readlane_b32 s86, v250, 17
	v_readlane_b32 s87, v250, 18
	v_readlane_b32 s88, v250, 19
	v_readlane_b32 s89, v250, 20
	v_readlane_b32 s90, v250, 21
	v_readlane_b32 s91, v250, 22
.LBB0_445:
	s_andn2_saveexec_b64 s[18:19], s[18:19]
	v_max_i32_e32 v50, 0x70, v60
	v_add_u32_e32 v136, 0xffffff90, v50
	s_or_b64 exec, exec, s[18:19]
	v_lshlrev_b64 v[50:51], 13, v[136:137]
	v_lshl_add_u64 v[48:49], v[48:49], 0, v[50:51]
	v_lshl_add_u64 v[58:59], v[146:147], 2, v[48:49]
	global_load_dwordx4 v[48:51], v[58:59], off
	global_load_dwordx4 v[52:55], v[58:59], off offset:16
	v_ashrrev_i32_e32 v57, 31, v56
	v_cmp_gt_i32_e32 vcc, s46, v60
	v_lshlrev_b64 v[56:57], 12, v[56:57]
	v_lshl_add_u64 v[56:57], s[96:97], 0, v[56:57]
	v_cndmask_b32_e64 v60, 1.0, 0, vcc
	v_lshl_add_u64 v[56:57], v[146:147], 1, v[56:57]
	v_readlane_b32 s76, v250, 7
	v_readlane_b32 s78, v250, 9
	v_readlane_b32 s79, v250, 10
	v_readlane_b32 s77, v250, 8
	v_readlane_b32 s80, v250, 11
	v_readlane_b32 s81, v250, 12
	v_readlane_b32 s82, v250, 13
	v_readlane_b32 s83, v250, 14
	v_readlane_b32 s84, v250, 15
	v_readlane_b32 s85, v250, 16
	v_readlane_b32 s86, v250, 17
	v_readlane_b32 s87, v250, 18
	v_readlane_b32 s88, v250, 19
	v_readlane_b32 s89, v250, 20
	v_readlane_b32 s90, v250, 21
	v_readlane_b32 s91, v250, 22
	s_waitcnt vmcnt(1)
	v_fma_f32 v44, v60, v48, v44
	s_waitcnt vmcnt(0)
	v_fmac_f32_e32 v43, v60, v55
	v_fma_f32 v45, v60, v49, v45
	v_fma_f32 v46, v60, v50, v46
	v_fmac_f32_e32 v47, v60, v51
	v_fma_f32 v48, v60, v52, v40
	v_fma_f32 v49, v60, v53, v41
	v_fma_f32 v50, v60, v54, v42
	v_cvt_pk_bf16_f32 v40, v44, v45
	v_cvt_pk_bf16_f32 v41, v46, v47
	v_cvt_pk_bf16_f32 v42, v48, v49
	v_cvt_pk_bf16_f32 v43, v50, v43
	global_store_dwordx4 v[56:57], v[40:43], off nt
	global_load_dwordx4 v[46:49], v[58:59], off offset:512
	global_load_dwordx4 v[50:53], v[58:59], off offset:528
	v_add_u32_e32 v40, 0xa0, v148
	v_mul_hi_i32 v41, v40, s43
	v_lshrrev_b32_e32 v42, 31, v41
	v_ashrrev_i32_e32 v41, 10, v41
	v_add_u32_e32 v42, v41, v42
	v_mad_i32_i24 v44, v42, s44, v40
	v_cmp_lt_i32_e32 vcc, s45, v44
	s_waitcnt vmcnt(1)
	v_fma_f32 v36, v60, v46, v36
	v_fma_f32 v37, v60, v47, v37
	v_fma_f32 v38, v60, v48, v38
	v_fmac_f32_e32 v39, v60, v49
	s_waitcnt vmcnt(0)
	v_fma_f32 v41, v60, v50, v32
	v_fma_f32 v43, v60, v51, v33
	v_fmac_f32_e32 v35, v60, v53
	v_cvt_pk_bf16_f32 v32, v36, v37
	v_cvt_pk_bf16_f32 v33, v38, v39
	v_fma_f32 v45, v60, v52, v34
	v_cvt_pk_bf16_f32 v34, v41, v43
	v_cvt_pk_bf16_f32 v35, v45, v35
	global_store_dwordx4 v[56:57], v[32:35], off offset:256 nt
	s_nop 1
	v_mov_b64_e32 v[32:33], s[78:79]
	s_and_saveexec_b64 s[18:19], vcc
	s_xor_b64 s[18:19], exec, s[18:19]
	s_cbranch_execz .LBB0_449
	v_ashrrev_i32_e32 v43, 31, v42
	v_readlane_b32 s76, v250, 7
	v_lshlrev_b64 v[32:33], 25, v[42:43]
	v_readlane_b32 s77, v250, 8
	v_add_u32_e32 v136, 0xffffff80, v44
	v_readlane_b32 s78, v250, 9
	v_lshl_add_u64 v[32:33], s[76:77], 0, v[32:33]
	v_readlane_b32 s79, v250, 10
	v_readlane_b32 s80, v250, 11
	v_readlane_b32 s81, v250, 12
	v_readlane_b32 s82, v250, 13
	v_readlane_b32 s83, v250, 14
	v_readlane_b32 s84, v250, 15
	v_readlane_b32 s85, v250, 16
	v_readlane_b32 s86, v250, 17
	v_readlane_b32 s87, v250, 18
	v_readlane_b32 s88, v250, 19
	v_readlane_b32 s89, v250, 20
	v_readlane_b32 s90, v250, 21
	v_readlane_b32 s91, v250, 22
.LBB0_449:
	s_andn2_saveexec_b64 s[18:19], s[18:19]
	v_max_i32_e32 v34, 0x70, v44
	v_add_u32_e32 v136, 0xffffff90, v34
	s_or_b64 exec, exec, s[18:19]
	v_lshlrev_b64 v[34:35], 13, v[136:137]
	v_lshl_add_u64 v[32:33], v[32:33], 0, v[34:35]
	v_lshl_add_u64 v[42:43], v[146:147], 2, v[32:33]
	global_load_dwordx4 v[32:35], v[42:43], off
	global_load_dwordx4 v[36:39], v[42:43], off offset:16
	v_ashrrev_i32_e32 v41, 31, v40
	v_cmp_gt_i32_e32 vcc, s46, v44
	v_lshlrev_b64 v[40:41], 12, v[40:41]
	v_lshl_add_u64 v[40:41], s[96:97], 0, v[40:41]
	v_cndmask_b32_e64 v44, 1.0, 0, vcc
	v_lshl_add_u64 v[40:41], v[146:147], 1, v[40:41]
	v_readlane_b32 s76, v250, 7
	v_readlane_b32 s78, v250, 9
	v_readlane_b32 s79, v250, 10
	v_readlane_b32 s77, v250, 8
	v_readlane_b32 s80, v250, 11
	v_readlane_b32 s81, v250, 12
	v_readlane_b32 s82, v250, 13
	v_readlane_b32 s83, v250, 14
	v_readlane_b32 s84, v250, 15
	v_readlane_b32 s85, v250, 16
	v_readlane_b32 s86, v250, 17
	v_readlane_b32 s87, v250, 18
	v_readlane_b32 s88, v250, 19
	v_readlane_b32 s89, v250, 20
	v_readlane_b32 s90, v250, 21
	v_readlane_b32 s91, v250, 22
	s_waitcnt vmcnt(1)
	v_fma_f32 v28, v44, v32, v28
	s_waitcnt vmcnt(0)
	v_fmac_f32_e32 v27, v44, v39
	v_fma_f32 v29, v44, v33, v29
	v_fma_f32 v30, v44, v34, v30
	v_fmac_f32_e32 v31, v44, v35
	v_fma_f32 v32, v44, v36, v24
	v_fma_f32 v33, v44, v37, v25
	v_fma_f32 v34, v44, v38, v26
	v_cvt_pk_bf16_f32 v24, v28, v29
	v_cvt_pk_bf16_f32 v25, v30, v31
	v_cvt_pk_bf16_f32 v26, v32, v33
	v_cvt_pk_bf16_f32 v27, v34, v27
	global_store_dwordx4 v[40:41], v[24:27], off nt
	global_load_dwordx4 v[30:33], v[42:43], off offset:512
	global_load_dwordx4 v[34:37], v[42:43], off offset:528
	v_add_u32_e32 v24, 0xb0, v148
	v_mul_hi_i32 v25, v24, s43
	v_lshrrev_b32_e32 v26, 31, v25
	v_ashrrev_i32_e32 v25, 10, v25
	v_add_u32_e32 v26, v25, v26
	v_mad_i32_i24 v28, v26, s44, v24
	v_cmp_lt_i32_e32 vcc, s45, v28
	s_waitcnt vmcnt(1)
	v_fma_f32 v20, v44, v30, v20
	v_fma_f32 v21, v44, v31, v21
	v_fma_f32 v22, v44, v32, v22
	v_fmac_f32_e32 v23, v44, v33
	s_waitcnt vmcnt(0)
	v_fma_f32 v25, v44, v34, v16
	v_fma_f32 v27, v44, v35, v17
	v_fmac_f32_e32 v19, v44, v37
	v_cvt_pk_bf16_f32 v16, v20, v21
	v_cvt_pk_bf16_f32 v17, v22, v23
	v_fma_f32 v29, v44, v36, v18
	v_cvt_pk_bf16_f32 v18, v25, v27
	v_cvt_pk_bf16_f32 v19, v29, v19
	global_store_dwordx4 v[40:41], v[16:19], off offset:256 nt
	s_nop 1
	v_mov_b64_e32 v[16:17], s[78:79]
	s_and_saveexec_b64 s[18:19], vcc
	s_xor_b64 s[18:19], exec, s[18:19]
	s_cbranch_execz .LBB0_453
	v_ashrrev_i32_e32 v27, 31, v26
	v_readlane_b32 s76, v250, 7
	v_lshlrev_b64 v[16:17], 25, v[26:27]
	v_readlane_b32 s77, v250, 8
	v_add_u32_e32 v136, 0xffffff80, v28
	v_readlane_b32 s78, v250, 9
	v_lshl_add_u64 v[16:17], s[76:77], 0, v[16:17]
	v_readlane_b32 s79, v250, 10
	v_readlane_b32 s80, v250, 11
	v_readlane_b32 s81, v250, 12
	v_readlane_b32 s82, v250, 13
	v_readlane_b32 s83, v250, 14
	v_readlane_b32 s84, v250, 15
	v_readlane_b32 s85, v250, 16
	v_readlane_b32 s86, v250, 17
	v_readlane_b32 s87, v250, 18
	v_readlane_b32 s88, v250, 19
	v_readlane_b32 s89, v250, 20
	v_readlane_b32 s90, v250, 21
	v_readlane_b32 s91, v250, 22
.LBB0_453:
	s_andn2_saveexec_b64 s[18:19], s[18:19]
	v_max_i32_e32 v18, 0x70, v28
	v_add_u32_e32 v136, 0xffffff90, v18
	s_or_b64 exec, exec, s[18:19]
	v_lshlrev_b64 v[18:19], 13, v[136:137]
	v_lshl_add_u64 v[16:17], v[16:17], 0, v[18:19]
	v_lshl_add_u64 v[26:27], v[146:147], 2, v[16:17]
	global_load_dwordx4 v[16:19], v[26:27], off
	global_load_dwordx4 v[20:23], v[26:27], off offset:16
	v_ashrrev_i32_e32 v25, 31, v24
	v_cmp_gt_i32_e32 vcc, s46, v28
	v_lshlrev_b64 v[24:25], 12, v[24:25]
	v_lshl_add_u64 v[24:25], s[96:97], 0, v[24:25]
	v_cndmask_b32_e64 v28, 1.0, 0, vcc
	v_lshl_add_u64 v[24:25], v[146:147], 1, v[24:25]
	s_andn2_b64 vcc, exec, s[0:1]
	s_mov_b64 s[0:1], -1
	s_waitcnt vmcnt(1)
	v_fma_f32 v12, v28, v16, v12
	s_waitcnt vmcnt(0)
	v_fmac_f32_e32 v11, v28, v23
	v_fma_f32 v13, v28, v17, v13
	v_fma_f32 v14, v28, v18, v14
	v_fmac_f32_e32 v15, v28, v19
	v_fma_f32 v16, v28, v20, v8
	v_fma_f32 v17, v28, v21, v9
	v_fma_f32 v18, v28, v22, v10
	v_cvt_pk_bf16_f32 v8, v12, v13
	v_cvt_pk_bf16_f32 v9, v14, v15
	v_cvt_pk_bf16_f32 v10, v16, v17
	v_cvt_pk_bf16_f32 v11, v18, v11
	global_store_dwordx4 v[24:25], v[8:11], off nt
	global_load_dwordx4 v[8:11], v[26:27], off offset:512
	s_nop 0
	global_load_dwordx4 v[12:15], v[26:27], off offset:528
	s_waitcnt vmcnt(1)
	v_fma_f32 v4, v28, v8, v4
	s_waitcnt vmcnt(0)
	v_fmac_f32_e32 v3, v28, v15
	v_fma_f32 v5, v28, v9, v5
	v_fma_f32 v6, v28, v10, v6
	v_fmac_f32_e32 v7, v28, v11
	v_fma_f32 v8, v28, v12, v0
	v_fma_f32 v9, v28, v13, v1
	v_fma_f32 v10, v28, v14, v2
	v_cvt_pk_bf16_f32 v0, v4, v5
	v_cvt_pk_bf16_f32 v1, v6, v7
	v_cvt_pk_bf16_f32 v2, v8, v9
	v_cvt_pk_bf16_f32 v3, v10, v3
	global_store_dwordx4 v[24:25], v[0:3], off offset:256 nt
	s_cbranch_vccnz .LBB0_412
	s_andn2_b64 vcc, exec, s[4:5]
	s_cbranch_vccnz .LBB0_411
	s_barrier
	s_branch .LBB0_411

.LBB0_473:
	v_lshl_or_b32 v138, s10, 8, v134
	s_ashr_i32 s10, s12, 31
	s_lshr_b32 s10, s10, 24
	s_add_i32 s10, s12, s10
	s_ashr_i32 s36, s10, 8
	s_ashr_i32 s37, s36, 31
	s_lshl_b64 s[36:37], s[36:37], 22
	s_add_u32 s36, s41, s36
	v_lshl_add_u32 v140, s8, 8, v133
	s_addc_u32 s37, s42, s37
	v_ashrrev_i32_e32 v139, 31, v138
	v_ashrrev_i32_e32 v141, 31, v140
	v_lshl_add_u64 v[138:139], v[138:139], 2, s[36:37]
	v_lshlrev_b64 v[142:143], 13, v[140:141]
	v_lshl_add_u64 v[142:143], v[138:139], 0, v[142:143]
	global_store_dwordx4 v[142:143], v[32:35], off nt
	global_store_dwordx4 v[142:143], v[36:39], off offset:64 nt
	global_store_dwordx4 v[142:143], v[64:67], off offset:512 nt
	global_store_dwordx4 v[142:143], v[68:71], off offset:576 nt
	v_or_b32_e32 v32, 16, v140
	v_ashrrev_i32_e32 v33, 31, v32
	v_lshlrev_b64 v[32:33], 13, v[32:33]
	v_lshl_add_u64 v[32:33], v[138:139], 0, v[32:33]
	global_store_dwordx4 v[32:33], v[16:19], off nt
	global_store_dwordx4 v[32:33], v[20:23], off offset:64 nt
	global_store_dwordx4 v[32:33], v[48:51], off offset:512 nt
	global_store_dwordx4 v[32:33], v[52:55], off offset:576 nt
	v_or_b32_e32 v16, 32, v140
	v_ashrrev_i32_e32 v17, 31, v16
	v_lshlrev_b64 v[16:17], 13, v[16:17]
	v_lshl_add_u64 v[16:17], v[138:139], 0, v[16:17]
	global_store_dwordx4 v[16:17], v[8:11], off nt
	global_store_dwordx4 v[16:17], v[12:15], off offset:64 nt
	global_store_dwordx4 v[16:17], v[40:43], off offset:512 nt
	global_store_dwordx4 v[16:17], v[44:47], off offset:576 nt
	v_or_b32_e32 v8, 48, v140
	v_ashrrev_i32_e32 v9, 31, v8
	v_lshlrev_b64 v[8:9], 13, v[8:9]
	v_lshl_add_u64 v[8:9], v[138:139], 0, v[8:9]
	s_mov_b32 s8, 0x100000
	global_store_dwordx4 v[8:9], v[0:3], off nt
	global_store_dwordx4 v[8:9], v[4:7], off offset:64 nt
	global_store_dwordx4 v[8:9], v[24:27], off offset:512 nt
	global_store_dwordx4 v[8:9], v[28:31], off offset:576 nt
	v_add_co_u32_e32 v2, vcc, s8, v142
	s_mov_b64 s[36:37], 0x100000
	s_nop 0
	v_addc_co_u32_e32 v3, vcc, 0, v143, vcc
	s_mov_b32 s8, 0x120000
	v_lshl_add_u64 v[0:1], v[142:143], 0, s[36:37]
	global_store_dwordx4 v[2:3], v[96:99], off nt
	global_store_dwordx4 v[0:1], v[100:103], off offset:64 nt
	global_store_dwordx4 v[0:1], v[120:123], off offset:512 nt
	global_store_dwordx4 v[0:1], v[124:127], off offset:576 nt
	v_add_co_u32_e32 v2, vcc, s8, v142
	s_mov_b64 s[36:37], 0x120000
	s_nop 0
	v_addc_co_u32_e32 v3, vcc, 0, v143, vcc
	v_lshl_add_u64 v[0:1], v[142:143], 0, s[36:37]
	global_store_dwordx4 v[2:3], v[80:83], off nt
	global_store_dwordx4 v[0:1], v[84:87], off offset:64 nt
	global_store_dwordx4 v[0:1], v[112:115], off offset:512 nt
	global_store_dwordx4 v[0:1], v[116:119], off offset:576 nt
	v_add_co_u32_e32 v2, vcc, s56, v142
	s_mov_b64 s[36:37], 0x140000
	s_nop 0
	v_addc_co_u32_e32 v3, vcc, 0, v143, vcc
	v_lshl_add_u64 v[0:1], v[142:143], 0, s[36:37]
	global_store_dwordx4 v[2:3], v[72:75], off nt
	global_store_dwordx4 v[0:1], v[76:79], off offset:64 nt
	global_store_dwordx4 v[0:1], v[104:107], off offset:512 nt
	global_store_dwordx4 v[0:1], v[108:111], off offset:576 nt
	v_add_co_u32_e32 v2, vcc, 0x160000, v142
	s_mov_b32 s60, s66
	s_nop 0
	v_addc_co_u32_e32 v3, vcc, 0, v143, vcc
	s_and_b64 vcc, exec, s[0:1]
	s_mov_b64 s[0:1], -1
	v_readlane_b32 s59, v250, 50
	v_lshl_add_u64 v[0:1], v[142:143], 0, s[22:23]
	global_store_dwordx4 v[2:3], v[56:59], off nt
	global_store_dwordx4 v[0:1], v[60:63], off offset:64 nt
	global_store_dwordx4 v[0:1], v[88:91], off offset:512 nt
	global_store_dwordx4 v[0:1], v[92:95], off offset:576 nt
	s_cbranch_vccnz .LBB0_464
	s_andn2_b64 vcc, exec, s[4:5]
	s_cbranch_vccnz .LBB0_463
	s_barrier
	s_branch .LBB0_463

.LBB0_705:
	s_or_b64 exec, exec, s[30:31]
	v_mul_f32_e32 v149, 0xbfb8aa3b, v72
	v_mul_f32_e32 v150, 0xbfb8aa3b, v73
	v_mul_f32_e32 v151, 0xbfb8aa3b, v74
	v_mul_f32_e32 v152, 0xbfb8aa3b, v75
	v_mul_f32_e32 v153, 0xbfb8aa3b, v64
	v_mul_f32_e32 v169, 0xbfb8aa3b, v65
	v_mul_f32_e32 v170, 0xbfb8aa3b, v66
	v_mul_f32_e32 v171, 0xbfb8aa3b, v67
	v_exp_f32_e32 v149, v149
	v_exp_f32_e32 v150, v150
	v_exp_f32_e32 v151, v151
	v_exp_f32_e32 v152, v152
	v_exp_f32_e32 v153, v153
	v_exp_f32_e32 v169, v169
	v_exp_f32_e32 v170, v170
	v_exp_f32_e32 v171, v171
	v_add_f32_e32 v149, 1.0, v149
	v_add_f32_e32 v150, 1.0, v150
	v_add_f32_e32 v151, 1.0, v151
	v_add_f32_e32 v152, 1.0, v152
	v_add_f32_e32 v153, 1.0, v153
	v_add_f32_e32 v169, 1.0, v169
	v_add_f32_e32 v170, 1.0, v170
	v_add_f32_e32 v171, 1.0, v171
	v_rcp_f32_e32 v149, v149
	v_rcp_f32_e32 v150, v150
	v_rcp_f32_e32 v151, v151
	v_rcp_f32_e32 v152, v152
	v_rcp_f32_e32 v153, v153
	v_rcp_f32_e32 v169, v169
	v_rcp_f32_e32 v170, v170
	v_rcp_f32_e32 v171, v171
	v_lshlrev_b32_e32 v143, 7, v128
	v_mul_f32_e32 v149, v72, v149
	v_mul_f32_e32 v150, v73, v150
	v_mul_f32_e32 v151, v74, v151
	v_mul_f32_e32 v152, v75, v152
	v_mul_f32_e32 v153, v64, v153
	v_mul_f32_e32 v169, v65, v169
	v_mul_f32_e32 v170, v66, v170
	v_mul_f32_e32 v171, v67, v171
	v_and_b32_e32 v143, 0x180, v143
	v_mul_f32_e32 v149, v149, v36
	v_mul_f32_e32 v150, v150, v37
	v_mul_f32_e32 v151, v151, v38
	v_mul_f32_e32 v152, v152, v39
	v_mul_f32_e32 v153, v153, v32
	v_mul_f32_e32 v169, v169, v33
	v_mul_f32_e32 v170, v170, v34
	v_mul_f32_e32 v171, v171, v35
	v_or_b32_e32 v143, v143, v137
	s_waitcnt vmcnt(0)
	v_mul_f32_e32 v149, v149, v130
	v_mul_f32_e32 v150, v150, v130
	v_mul_f32_e32 v151, v151, v130
	v_mul_f32_e32 v152, v152, v130
	v_mul_f32_e32 v153, v153, v130
	v_mul_f32_e32 v169, v169, v130
	v_mul_f32_e32 v170, v170, v130
	v_mul_f32_e32 v130, v171, v130
	v_cvt_pk_bf16_f32 v150, v149, v150
	v_cvt_pk_bf16_f32 v151, v151, v152
	v_cvt_pk_bf16_f32 v152, v153, v169
	v_cvt_pk_bf16_f32 v153, v170, v130
	v_lshlrev_b32_e32 v130, 1, v143
	ds_read_b32 v143, v133
	v_ashrrev_i32_e32 v149, 31, v148
	v_lshlrev_b64 v[170:171], 10, v[148:149]
	v_lshl_add_u64 v[170:171], s[14:15], 0, v[170:171]
	v_lshl_add_u64 v[170:171], v[170:171], 0, v[130:131]
	s_waitcnt lgkmcnt(0)
	v_lshlrev_b32_e32 v149, 2, v143
	global_store_dwordx4 v[170:171], v[150:153], off nt
	s_nop 1
	v_add_u32_e32 v151, 0, v149
	v_add_u32_e32 v149, 0x20100, v151
	ds_read_b32 v149, v149
	v_add_u32_e32 v151, 0x20200, v151
	ds_read_b32 v151, v151
	v_or_b32_e32 v150, 16, v148
	s_waitcnt lgkmcnt(1)
	v_sub_u32_e32 v149, v150, v149
	s_waitcnt lgkmcnt(0)
	v_cmp_lt_i32_e32 vcc, v149, v151
	s_and_saveexec_b64 s[30:31], vcc
	s_cbranch_execz .LBB0_707
	v_mul_lo_u32 v135, v143, s79
	v_add_u32_e32 v152, v149, v135
	v_ashrrev_i32_e32 v153, 31, v152
	v_lshl_add_u64 v[152:153], v[152:153], 2, s[16:17]
	global_load_dword v135, v[152:153], off
.LBB0_707:
	s_or_b64 exec, exec, s[30:31]
	v_mul_f32_e32 v170, 0xbfb8aa3b, v58
	v_mul_f32_e32 v149, 0xbfb8aa3b, v61
	v_exp_f32_e32 v170, v170
	v_mul_f32_e32 v143, 0xbfb8aa3b, v60
	v_exp_f32_e32 v149, v149
	v_mul_f32_e32 v151, 0xbfb8aa3b, v62
	v_mul_f32_e32 v152, 0xbfb8aa3b, v63
	v_mul_f32_e32 v153, 0xbfb8aa3b, v56
	v_mul_f32_e32 v169, 0xbfb8aa3b, v57
	v_mul_f32_e32 v171, 0xbfb8aa3b, v59
	v_exp_f32_e32 v143, v143
	v_exp_f32_e32 v151, v151
	v_exp_f32_e32 v152, v152
	v_exp_f32_e32 v153, v153
	v_exp_f32_e32 v169, v169
	v_exp_f32_e32 v171, v171
	v_add_f32_e32 v170, 1.0, v170
	v_add_f32_e32 v149, 1.0, v149
	v_rcp_f32_e32 v170, v170
	v_add_f32_e32 v143, 1.0, v143
	v_rcp_f32_e32 v149, v149
	v_add_f32_e32 v151, 1.0, v151
	v_add_f32_e32 v152, 1.0, v152
	v_add_f32_e32 v153, 1.0, v153
	v_add_f32_e32 v169, 1.0, v169
	v_add_f32_e32 v171, 1.0, v171
	v_rcp_f32_e32 v143, v143
	v_rcp_f32_e32 v151, v151
	v_rcp_f32_e32 v152, v152
	v_rcp_f32_e32 v153, v153
	v_rcp_f32_e32 v169, v169
	v_rcp_f32_e32 v171, v171
	v_mul_f32_e32 v170, v58, v170
	v_mul_f32_e32 v149, v61, v149
	v_mul_f32_e32 v170, v170, v26
	v_mul_f32_e32 v143, v60, v143
	v_mul_f32_e32 v149, v149, v29
	v_mul_f32_e32 v151, v62, v151
	v_mul_f32_e32 v152, v63, v152
	v_mul_f32_e32 v153, v56, v153
	v_mul_f32_e32 v169, v57, v169
	s_waitcnt vmcnt(0)
	v_mul_f32_e32 v173, v170, v135
	v_mul_f32_e32 v170, v59, v171
	v_mul_f32_e32 v143, v143, v28
	v_mul_f32_e32 v149, v149, v135
	v_mul_f32_e32 v151, v151, v30
	v_mul_f32_e32 v152, v152, v31
	v_mul_f32_e32 v153, v153, v24
	v_mul_f32_e32 v169, v169, v25
	v_mul_f32_e32 v170, v170, v27
	v_mul_f32_e32 v143, v143, v135
	v_mul_f32_e32 v151, v151, v135
	v_mul_f32_e32 v152, v152, v135
	v_mul_f32_e32 v153, v153, v135
	v_mul_f32_e32 v169, v169, v135
	v_mul_f32_e32 v135, v170, v135
	v_cvt_pk_bf16_f32 v170, v143, v149
	v_cvt_pk_bf16_f32 v171, v151, v152
	v_cvt_pk_bf16_f32 v172, v153, v169
	v_cvt_pk_bf16_f32 v173, v173, v135
	ds_read_b32 v149, v133
	v_ashrrev_i32_e32 v151, 31, v150
	v_lshlrev_b64 v[150:151], 10, v[150:151]
	v_lshl_add_u64 v[150:151], s[14:15], 0, v[150:151]
	v_lshl_add_u64 v[150:151], v[150:151], 0, v[130:131]
	s_waitcnt lgkmcnt(0)
	v_lshlrev_b32_e32 v135, 2, v149
	v_add_u32_e32 v135, 0, v135
	v_add_u32_e32 v143, 0x20100, v135
	v_add_u32_e32 v135, 0x20200, v135
	ds_read_b32 v143, v143
	ds_read_b32 v135, v135
	global_store_dwordx4 v[150:151], v[170:173], off nt
	v_or_b32_e32 v150, 32, v148
	s_waitcnt lgkmcnt(1)
	v_sub_u32_e32 v151, v150, v143
	s_waitcnt lgkmcnt(0)
	v_cmp_lt_i32_e32 vcc, v151, v135
	v_mov_b32_e32 v135, 0
	v_mov_b32_e32 v143, 0
	s_and_saveexec_b64 s[30:31], vcc
	s_cbranch_execz .LBB0_709
	v_mul_lo_u32 v143, v149, s79
	v_add_u32_e32 v152, v151, v143
	v_ashrrev_i32_e32 v153, 31, v152
	v_lshl_add_u64 v[152:153], v[152:153], 2, s[16:17]
	global_load_dword v143, v[152:153], off
.LBB0_709:
	s_or_b64 exec, exec, s[30:31]
	v_mul_f32_e32 v170, 0xbfb8aa3b, v49
	v_exp_f32_e32 v170, v170
	v_mul_f32_e32 v149, 0xbfb8aa3b, v52
	v_mul_f32_e32 v151, 0xbfb8aa3b, v53
	v_mul_f32_e32 v152, 0xbfb8aa3b, v54
	v_add_f32_e32 v170, 1.0, v170
	v_rcp_f32_e32 v170, v170
	v_mul_f32_e32 v153, 0xbfb8aa3b, v55
	v_mul_f32_e32 v169, 0xbfb8aa3b, v48
	v_mul_f32_e32 v171, 0xbfb8aa3b, v50
	v_mul_f32_e32 v172, 0xbfb8aa3b, v51
	v_exp_f32_e32 v149, v149
	v_exp_f32_e32 v151, v151
	v_exp_f32_e32 v152, v152
	v_exp_f32_e32 v153, v153
	v_exp_f32_e32 v169, v169
	v_exp_f32_e32 v171, v171
	v_exp_f32_e32 v172, v172
	v_mul_f32_e32 v170, v49, v170
	v_mul_f32_e32 v170, v170, v17
	v_add_f32_e32 v149, 1.0, v149
	v_add_f32_e32 v151, 1.0, v151
	v_add_f32_e32 v152, 1.0, v152
	v_add_f32_e32 v153, 1.0, v153
	v_add_f32_e32 v169, 1.0, v169
	v_add_f32_e32 v171, 1.0, v171
	s_waitcnt vmcnt(0)
	v_mul_f32_e32 v173, v170, v143
	v_add_f32_e32 v170, 1.0, v172
	v_rcp_f32_e32 v149, v149
	v_rcp_f32_e32 v151, v151
	v_rcp_f32_e32 v152, v152
	v_rcp_f32_e32 v153, v153
	v_rcp_f32_e32 v169, v169
	v_rcp_f32_e32 v171, v171
	v_rcp_f32_e32 v170, v170
	v_mul_f32_e32 v149, v52, v149
	v_mul_f32_e32 v151, v53, v151
	v_mul_f32_e32 v152, v54, v152
	v_mul_f32_e32 v153, v55, v153
	v_mul_f32_e32 v169, v48, v169
	v_mul_f32_e32 v171, v50, v171
	v_mul_f32_e32 v170, v51, v170
	v_mul_f32_e32 v149, v149, v20
	v_mul_f32_e32 v151, v151, v21
	v_mul_f32_e32 v152, v152, v22
	v_mul_f32_e32 v153, v153, v23
	v_mul_f32_e32 v169, v169, v16
	v_mul_f32_e32 v171, v171, v18
	v_mul_f32_e32 v170, v170, v19
	v_mul_f32_e32 v149, v149, v143
	v_mul_f32_e32 v151, v151, v143
	v_mul_f32_e32 v152, v152, v143
	v_mul_f32_e32 v153, v153, v143
	v_mul_f32_e32 v169, v169, v143
	v_mul_f32_e32 v174, v171, v143
	v_mul_f32_e32 v143, v170, v143
	v_cvt_pk_bf16_f32 v170, v149, v151
	v_cvt_pk_bf16_f32 v171, v152, v153
	v_cvt_pk_bf16_f32 v172, v169, v173
	v_cvt_pk_bf16_f32 v173, v174, v143
	ds_read_b32 v143, v133
	v_ashrrev_i32_e32 v151, 31, v150
	v_lshlrev_b64 v[150:151], 10, v[150:151]
	v_lshl_add_u64 v[150:151], s[14:15], 0, v[150:151]
	v_lshl_add_u64 v[150:151], v[150:151], 0, v[130:131]
	s_waitcnt lgkmcnt(0)
	v_lshlrev_b32_e32 v149, 2, v143
	v_add_u32_e32 v149, 0, v149
	v_add_u32_e32 v152, 0x20100, v149
	v_add_u32_e32 v149, 0x20200, v149
	ds_read_b32 v152, v152
	ds_read_b32 v153, v149
	global_store_dwordx4 v[150:151], v[170:173], off nt
	v_or_b32_e32 v150, 48, v148
	s_waitcnt lgkmcnt(1)
	v_sub_u32_e32 v149, v150, v152
	s_waitcnt lgkmcnt(0)
	v_cmp_lt_i32_e32 vcc, v149, v153
	s_and_saveexec_b64 s[30:31], vcc
	s_cbranch_execz .LBB0_711
	v_mul_lo_u32 v135, v143, s79
	v_add_u32_e32 v152, v149, v135
	v_ashrrev_i32_e32 v153, 31, v152
	v_lshl_add_u64 v[152:153], v[152:153], 2, s[16:17]
	global_load_dword v135, v[152:153], off
.LBB0_711:
	s_or_b64 exec, exec, s[30:31]
	v_mul_f32_e32 v170, 0xbfb8aa3b, v42
	v_mul_f32_e32 v149, 0xbfb8aa3b, v45
	v_exp_f32_e32 v170, v170
	v_mul_f32_e32 v143, 0xbfb8aa3b, v44
	v_exp_f32_e32 v149, v149
	v_mul_f32_e32 v151, 0xbfb8aa3b, v46
	v_mul_f32_e32 v152, 0xbfb8aa3b, v47
	v_mul_f32_e32 v153, 0xbfb8aa3b, v40
	v_mul_f32_e32 v169, 0xbfb8aa3b, v41
	v_mul_f32_e32 v171, 0xbfb8aa3b, v43
	v_exp_f32_e32 v143, v143
	v_exp_f32_e32 v151, v151
	v_exp_f32_e32 v152, v152
	v_exp_f32_e32 v153, v153
	v_exp_f32_e32 v169, v169
	v_exp_f32_e32 v171, v171
	v_add_f32_e32 v170, 1.0, v170
	v_add_f32_e32 v149, 1.0, v149
	v_rcp_f32_e32 v170, v170
	v_add_f32_e32 v143, 1.0, v143
	v_rcp_f32_e32 v149, v149
	v_add_f32_e32 v151, 1.0, v151
	v_add_f32_e32 v152, 1.0, v152
	v_add_f32_e32 v153, 1.0, v153
	v_add_f32_e32 v169, 1.0, v169
	v_add_f32_e32 v171, 1.0, v171
	v_rcp_f32_e32 v143, v143
	v_rcp_f32_e32 v151, v151
	v_rcp_f32_e32 v152, v152
	v_rcp_f32_e32 v153, v153
	v_rcp_f32_e32 v169, v169
	v_rcp_f32_e32 v171, v171
	v_mul_f32_e32 v170, v42, v170
	v_mul_f32_e32 v149, v45, v149
	v_mul_f32_e32 v170, v170, v10
	v_mul_f32_e32 v143, v44, v143
	v_mul_f32_e32 v149, v149, v13
	v_mul_f32_e32 v151, v46, v151
	v_mul_f32_e32 v152, v47, v152
	v_mul_f32_e32 v153, v40, v153
	v_mul_f32_e32 v169, v41, v169
	s_waitcnt vmcnt(0)
	v_mul_f32_e32 v173, v170, v135
	v_mul_f32_e32 v170, v43, v171
	v_mul_f32_e32 v143, v143, v12
	v_mul_f32_e32 v149, v149, v135
	v_mul_f32_e32 v151, v151, v14
	v_mul_f32_e32 v152, v152, v15
	v_mul_f32_e32 v153, v153, v8
	v_mul_f32_e32 v169, v169, v9
	v_mul_f32_e32 v170, v170, v11
	v_mul_f32_e32 v143, v143, v135
	v_mul_f32_e32 v151, v151, v135
	v_mul_f32_e32 v152, v152, v135
	v_mul_f32_e32 v153, v153, v135
	v_mul_f32_e32 v169, v169, v135
	v_mul_f32_e32 v135, v170, v135
	v_cvt_pk_bf16_f32 v170, v143, v149
	v_cvt_pk_bf16_f32 v171, v151, v152
	v_cvt_pk_bf16_f32 v172, v153, v169
	v_cvt_pk_bf16_f32 v173, v173, v135
	ds_read_b32 v149, v133
	v_ashrrev_i32_e32 v151, 31, v150
	v_lshlrev_b64 v[150:151], 10, v[150:151]
	v_lshl_add_u64 v[150:151], s[14:15], 0, v[150:151]
	v_lshl_add_u64 v[150:151], v[150:151], 0, v[130:131]
	s_waitcnt lgkmcnt(0)
	v_lshlrev_b32_e32 v135, 2, v149
	v_add_u32_e32 v135, 0, v135
	v_add_u32_e32 v143, 0x20100, v135
	v_add_u32_e32 v135, 0x20200, v135
	ds_read_b32 v143, v143
	ds_read_b32 v135, v135
	global_store_dwordx4 v[150:151], v[170:173], off nt
	v_add_u32_e32 v150, 0x80, v148
	s_waitcnt lgkmcnt(1)
	v_sub_u32_e32 v151, v150, v143
	s_waitcnt lgkmcnt(0)
	v_cmp_lt_i32_e32 vcc, v151, v135
	v_mov_b32_e32 v135, 0
	v_mov_b32_e32 v143, 0
	s_and_saveexec_b64 s[30:31], vcc
	s_cbranch_execz .LBB0_713
	v_mul_lo_u32 v143, v149, s79
	v_add_u32_e32 v152, v151, v143
	v_ashrrev_i32_e32 v153, 31, v152
	v_lshl_add_u64 v[152:153], v[152:153], 2, s[16:17]
	global_load_dword v143, v[152:153], off
.LBB0_713:
	s_or_b64 exec, exec, s[30:31]
	v_mul_f32_e32 v170, 0xbfb8aa3b, v1
	v_exp_f32_e32 v170, v170
	v_mul_f32_e32 v149, 0xbfb8aa3b, v4
	v_mul_f32_e32 v151, 0xbfb8aa3b, v5
	v_mul_f32_e32 v152, 0xbfb8aa3b, v6
	v_add_f32_e32 v170, 1.0, v170
	v_rcp_f32_e32 v170, v170
	v_mul_f32_e32 v153, 0xbfb8aa3b, v7
	v_mul_f32_e32 v169, 0xbfb8aa3b, v0
	v_mul_f32_e32 v171, 0xbfb8aa3b, v2
	v_mul_f32_e32 v172, 0xbfb8aa3b, v3
	v_exp_f32_e32 v149, v149
	v_exp_f32_e32 v151, v151
	v_exp_f32_e32 v152, v152
	v_exp_f32_e32 v153, v153
	v_exp_f32_e32 v169, v169
	v_exp_f32_e32 v171, v171
	v_exp_f32_e32 v172, v172
	v_mul_f32_e32 v170, v1, v170
	v_mul_f32_e32 v170, v170, v101
	v_add_f32_e32 v149, 1.0, v149
	v_add_f32_e32 v151, 1.0, v151
	v_add_f32_e32 v152, 1.0, v152
	v_add_f32_e32 v153, 1.0, v153
	v_add_f32_e32 v169, 1.0, v169
	v_add_f32_e32 v171, 1.0, v171
	s_waitcnt vmcnt(0)
	v_mul_f32_e32 v173, v170, v143
	v_add_f32_e32 v170, 1.0, v172
	v_rcp_f32_e32 v149, v149
	v_rcp_f32_e32 v151, v151
	v_rcp_f32_e32 v152, v152
	v_rcp_f32_e32 v153, v153
	v_rcp_f32_e32 v169, v169
	v_rcp_f32_e32 v171, v171
	v_rcp_f32_e32 v170, v170
	v_mul_f32_e32 v149, v4, v149
	v_mul_f32_e32 v151, v5, v151
	v_mul_f32_e32 v152, v6, v152
	v_mul_f32_e32 v153, v7, v153
	v_mul_f32_e32 v169, v0, v169
	v_mul_f32_e32 v171, v2, v171
	v_mul_f32_e32 v170, v3, v170
	v_mul_f32_e32 v149, v149, v96
	v_mul_f32_e32 v151, v151, v97
	v_mul_f32_e32 v152, v152, v98
	v_mul_f32_e32 v153, v153, v99
	v_mul_f32_e32 v169, v169, v100
	v_mul_f32_e32 v171, v171, v102
	v_mul_f32_e32 v170, v170, v103
	v_mul_f32_e32 v149, v149, v143
	v_mul_f32_e32 v151, v151, v143
	v_mul_f32_e32 v152, v152, v143
	v_mul_f32_e32 v153, v153, v143
	v_mul_f32_e32 v169, v169, v143
	v_mul_f32_e32 v174, v171, v143
	v_mul_f32_e32 v143, v170, v143
	v_cvt_pk_bf16_f32 v170, v149, v151
	v_cvt_pk_bf16_f32 v171, v152, v153
	v_cvt_pk_bf16_f32 v172, v169, v173
	v_cvt_pk_bf16_f32 v173, v174, v143
	ds_read_b32 v143, v133
	v_ashrrev_i32_e32 v151, 31, v150
	v_lshlrev_b64 v[150:151], 10, v[150:151]
	v_lshl_add_u64 v[150:151], s[14:15], 0, v[150:151]
	v_lshl_add_u64 v[150:151], v[150:151], 0, v[130:131]
	s_waitcnt lgkmcnt(0)
	v_lshlrev_b32_e32 v149, 2, v143
	v_add_u32_e32 v149, 0, v149
	v_add_u32_e32 v152, 0x20100, v149
	v_add_u32_e32 v149, 0x20200, v149
	ds_read_b32 v152, v152
	ds_read_b32 v153, v149
	global_store_dwordx4 v[150:151], v[170:173], off nt
	v_add_u32_e32 v150, 0x90, v148
	s_waitcnt lgkmcnt(1)
	v_sub_u32_e32 v149, v150, v152
	s_waitcnt lgkmcnt(0)
	v_cmp_lt_i32_e32 vcc, v149, v153
	s_and_saveexec_b64 s[30:31], vcc
	s_cbranch_execz .LBB0_715
	v_mul_lo_u32 v135, v143, s79
	v_add_u32_e32 v152, v149, v135
	v_ashrrev_i32_e32 v153, 31, v152
	v_lshl_add_u64 v[152:153], v[152:153], 2, s[16:17]
	global_load_dword v135, v[152:153], off
.LBB0_715:
	s_or_b64 exec, exec, s[30:31]
	v_mul_f32_e32 v170, 0xbfb8aa3b, v78
	v_mul_f32_e32 v149, 0xbfb8aa3b, v69
	v_exp_f32_e32 v170, v170
	v_mul_f32_e32 v143, 0xbfb8aa3b, v68
	v_exp_f32_e32 v149, v149
	v_mul_f32_e32 v151, 0xbfb8aa3b, v70
	v_mul_f32_e32 v152, 0xbfb8aa3b, v71
	v_mul_f32_e32 v153, 0xbfb8aa3b, v76
	v_mul_f32_e32 v169, 0xbfb8aa3b, v77
	v_mul_f32_e32 v171, 0xbfb8aa3b, v79
	v_exp_f32_e32 v143, v143
	v_exp_f32_e32 v151, v151
	v_exp_f32_e32 v152, v152
	v_exp_f32_e32 v153, v153
	v_exp_f32_e32 v169, v169
	v_exp_f32_e32 v171, v171
	v_add_f32_e32 v170, 1.0, v170
	v_add_f32_e32 v149, 1.0, v149
	v_rcp_f32_e32 v170, v170
	v_add_f32_e32 v143, 1.0, v143
	v_rcp_f32_e32 v149, v149
	v_add_f32_e32 v151, 1.0, v151
	v_add_f32_e32 v152, 1.0, v152
	v_add_f32_e32 v153, 1.0, v153
	v_add_f32_e32 v169, 1.0, v169
	v_add_f32_e32 v171, 1.0, v171
	v_rcp_f32_e32 v143, v143
	v_rcp_f32_e32 v151, v151
	v_rcp_f32_e32 v152, v152
	v_rcp_f32_e32 v153, v153
	v_rcp_f32_e32 v169, v169
	v_rcp_f32_e32 v171, v171
	v_mul_f32_e32 v170, v78, v170
	v_mul_f32_e32 v149, v69, v149
	v_mul_f32_e32 v170, v170, v110
	v_mul_f32_e32 v143, v68, v143
	v_mul_f32_e32 v149, v149, v105
	v_mul_f32_e32 v151, v70, v151
	v_mul_f32_e32 v152, v71, v152
	v_mul_f32_e32 v153, v76, v153
	v_mul_f32_e32 v169, v77, v169
	s_waitcnt vmcnt(0)
	v_mul_f32_e32 v173, v170, v135
	v_mul_f32_e32 v170, v79, v171
	v_mul_f32_e32 v143, v143, v104
	v_mul_f32_e32 v149, v149, v135
	v_mul_f32_e32 v151, v151, v106
	v_mul_f32_e32 v152, v152, v107
	v_mul_f32_e32 v153, v153, v108
	v_mul_f32_e32 v169, v169, v109
	v_mul_f32_e32 v170, v170, v111
	v_mul_f32_e32 v143, v143, v135
	v_mul_f32_e32 v151, v151, v135
	v_mul_f32_e32 v152, v152, v135
	v_mul_f32_e32 v153, v153, v135
	v_mul_f32_e32 v169, v169, v135
	v_mul_f32_e32 v135, v170, v135
	v_cvt_pk_bf16_f32 v170, v143, v149
	v_cvt_pk_bf16_f32 v171, v151, v152
	v_cvt_pk_bf16_f32 v172, v153, v169
	v_cvt_pk_bf16_f32 v173, v173, v135
	ds_read_b32 v149, v133
	v_ashrrev_i32_e32 v151, 31, v150
	v_lshlrev_b64 v[150:151], 10, v[150:151]
	v_lshl_add_u64 v[150:151], s[14:15], 0, v[150:151]
	v_lshl_add_u64 v[150:151], v[150:151], 0, v[130:131]
	s_waitcnt lgkmcnt(0)
	v_lshlrev_b32_e32 v135, 2, v149
	v_add_u32_e32 v135, 0, v135
	v_add_u32_e32 v143, 0x20100, v135
	v_add_u32_e32 v135, 0x20200, v135
	ds_read_b32 v143, v143
	ds_read_b32 v135, v135
	global_store_dwordx4 v[150:151], v[170:173], off nt
	v_add_u32_e32 v150, 0xa0, v148
	s_waitcnt lgkmcnt(1)
	v_sub_u32_e32 v151, v150, v143
	s_waitcnt lgkmcnt(0)
	v_cmp_lt_i32_e32 vcc, v151, v135
	v_mov_b32_e32 v135, 0
	v_mov_b32_e32 v143, 0
	s_and_saveexec_b64 s[30:31], vcc
	s_cbranch_execz .LBB0_717
	v_mul_lo_u32 v143, v149, s79
	v_add_u32_e32 v152, v151, v143
	v_ashrrev_i32_e32 v153, 31, v152
	v_lshl_add_u64 v[152:153], v[152:153], 2, s[16:17]
	global_load_dword v143, v[152:153], off
.LBB0_717:
	s_or_b64 exec, exec, s[30:31]
	v_mul_f32_e32 v170, 0xbfb8aa3b, v85
	v_exp_f32_e32 v170, v170
	v_mul_f32_e32 v149, 0xbfb8aa3b, v80
	v_mul_f32_e32 v151, 0xbfb8aa3b, v81
	v_mul_f32_e32 v152, 0xbfb8aa3b, v82
	v_add_f32_e32 v170, 1.0, v170
	v_rcp_f32_e32 v170, v170
	v_mul_f32_e32 v153, 0xbfb8aa3b, v83
	v_mul_f32_e32 v169, 0xbfb8aa3b, v84
	v_mul_f32_e32 v171, 0xbfb8aa3b, v86
	v_mul_f32_e32 v172, 0xbfb8aa3b, v87
	v_exp_f32_e32 v149, v149
	v_exp_f32_e32 v151, v151
	v_exp_f32_e32 v152, v152
	v_exp_f32_e32 v153, v153
	v_exp_f32_e32 v169, v169
	v_exp_f32_e32 v171, v171
	v_exp_f32_e32 v172, v172
	v_mul_f32_e32 v170, v85, v170
	v_mul_f32_e32 v170, v170, v117
	v_add_f32_e32 v149, 1.0, v149
	v_add_f32_e32 v151, 1.0, v151
	v_add_f32_e32 v152, 1.0, v152
	v_add_f32_e32 v153, 1.0, v153
	v_add_f32_e32 v169, 1.0, v169
	v_add_f32_e32 v171, 1.0, v171
	s_waitcnt vmcnt(0)
	v_mul_f32_e32 v173, v170, v143
	v_add_f32_e32 v170, 1.0, v172
	v_rcp_f32_e32 v149, v149
	v_rcp_f32_e32 v151, v151
	v_rcp_f32_e32 v152, v152
	v_rcp_f32_e32 v153, v153
	v_rcp_f32_e32 v169, v169
	v_rcp_f32_e32 v171, v171
	v_rcp_f32_e32 v170, v170
	v_mul_f32_e32 v149, v80, v149
	v_mul_f32_e32 v151, v81, v151
	v_mul_f32_e32 v152, v82, v152
	v_mul_f32_e32 v153, v83, v153
	v_mul_f32_e32 v169, v84, v169
	v_mul_f32_e32 v171, v86, v171
	v_mul_f32_e32 v170, v87, v170
	v_mul_f32_e32 v149, v149, v112
	v_mul_f32_e32 v151, v151, v113
	v_mul_f32_e32 v152, v152, v114
	v_mul_f32_e32 v153, v153, v115
	v_mul_f32_e32 v169, v169, v116
	v_mul_f32_e32 v171, v171, v118
	v_mul_f32_e32 v170, v170, v119
	v_mul_f32_e32 v149, v149, v143
	v_mul_f32_e32 v151, v151, v143
	v_mul_f32_e32 v152, v152, v143
	v_mul_f32_e32 v153, v153, v143
	v_mul_f32_e32 v169, v169, v143
	v_mul_f32_e32 v174, v171, v143
	v_mul_f32_e32 v143, v170, v143
	v_cvt_pk_bf16_f32 v170, v149, v151
	v_cvt_pk_bf16_f32 v171, v152, v153
	v_cvt_pk_bf16_f32 v172, v169, v173
	v_cvt_pk_bf16_f32 v173, v174, v143
	ds_read_b32 v133, v133
	v_ashrrev_i32_e32 v151, 31, v150
	v_lshlrev_b64 v[150:151], 10, v[150:151]
	v_add_u32_e32 v148, 0xb0, v148
	v_lshl_add_u64 v[150:151], s[14:15], 0, v[150:151]
	s_waitcnt lgkmcnt(0)
	v_lshlrev_b32_e32 v143, 2, v133
	v_add_u32_e32 v143, 0, v143
	v_add_u32_e32 v149, 0x20100, v143
	v_add_u32_e32 v143, 0x20200, v143
	ds_read_b32 v149, v149
	ds_read_b32 v152, v143
	v_lshl_add_u64 v[150:151], v[150:151], 0, v[130:131]
	global_store_dwordx4 v[150:151], v[170:173], off nt
	s_waitcnt lgkmcnt(1)
	v_sub_u32_e32 v143, v148, v149
	s_waitcnt lgkmcnt(0)
	v_cmp_lt_i32_e32 vcc, v143, v152
	s_and_saveexec_b64 s[30:31], vcc
	s_cbranch_execz .LBB0_719
	v_mul_lo_u32 v133, v133, s79
	v_add_u32_e32 v150, v143, v133
	v_ashrrev_i32_e32 v151, 31, v150
	v_lshl_add_u64 v[150:151], v[150:151], 2, s[16:17]
	global_load_dword v135, v[150:151], off
.LBB0_719:
	s_or_b64 exec, exec, s[30:31]
	v_mul_f32_e32 v150, 0xbfb8aa3b, v91
	v_exp_f32_e32 v150, v150
	v_mul_f32_e32 v151, 0xbfb8aa3b, v92
	v_exp_f32_e32 v151, v151
	v_mul_f32_e32 v152, 0xbfb8aa3b, v93
	v_add_f32_e32 v150, 1.0, v150
	v_rcp_f32_e32 v150, v150
	v_add_f32_e32 v151, 1.0, v151
	v_exp_f32_e32 v152, v152
	v_rcp_f32_e32 v151, v151
	v_mul_f32_e32 v150, v91, v150
	v_mul_f32_e32 v150, v150, v123
	s_waitcnt vmcnt(0)
	v_mul_f32_e32 v153, v150, v135
	v_add_f32_e32 v150, 1.0, v152
	v_mul_f32_e32 v151, v92, v151
	v_mul_f32_e32 v149, 0xbfb8aa3b, v90
	v_rcp_f32_e32 v150, v150
	v_mul_f32_e32 v151, v151, v124
	v_mul_f32_e32 v133, 0xbfb8aa3b, v88
	v_mul_f32_e32 v143, 0xbfb8aa3b, v89
	v_exp_f32_e32 v149, v149
	v_mul_f32_e32 v152, v151, v135
	v_mul_f32_e32 v151, 0xbfb8aa3b, v94
	v_mul_f32_e32 v169, 0xbfb8aa3b, v95
	v_exp_f32_e32 v133, v133
	v_exp_f32_e32 v143, v143
	v_exp_f32_e32 v151, v151
	v_exp_f32_e32 v169, v169
	v_mul_f32_e32 v150, v93, v150
	v_add_f32_e32 v149, 1.0, v149
	v_mul_f32_e32 v150, v150, v125
	v_add_f32_e32 v133, 1.0, v133
	v_add_f32_e32 v143, 1.0, v143
	v_rcp_f32_e32 v149, v149
	v_add_f32_e32 v151, 1.0, v151
	v_mul_f32_e32 v170, v150, v135
	v_add_f32_e32 v150, 1.0, v169
	v_rcp_f32_e32 v133, v133
	v_rcp_f32_e32 v143, v143
	v_rcp_f32_e32 v151, v151
	v_rcp_f32_e32 v150, v150
	v_mul_f32_e32 v149, v90, v149
	v_mul_f32_e32 v133, v88, v133
	v_mul_f32_e32 v143, v89, v143
	v_mul_f32_e32 v149, v149, v122
	v_mul_f32_e32 v151, v94, v151
	v_mul_f32_e32 v150, v95, v150
	v_mul_f32_e32 v133, v133, v120
	v_mul_f32_e32 v143, v143, v121
	v_mul_f32_e32 v149, v149, v135
	v_mul_f32_e32 v151, v151, v126
	v_mul_f32_e32 v150, v150, v127
	v_mul_f32_e32 v133, v133, v135
	v_mul_f32_e32 v143, v143, v135
	v_mul_f32_e32 v169, v151, v135
	v_mul_f32_e32 v135, v150, v135
	v_cvt_pk_bf16_f32 v150, v133, v143
	v_cvt_pk_bf16_f32 v151, v149, v153
	v_ashrrev_i32_e32 v149, 31, v148
	v_lshlrev_b64 v[148:149], 10, v[148:149]
	v_lshl_add_u64 v[148:149], s[14:15], 0, v[148:149]
	v_lshl_add_u64 v[148:149], v[148:149], 0, v[130:131]
	s_and_b64 vcc, exec, s[2:3]
	v_cvt_pk_bf16_f32 v152, v152, v170
	v_cvt_pk_bf16_f32 v153, v169, v135
	global_store_dwordx4 v[148:149], v[150:153], off nt
	s_cbranch_vccnz .LBB0_722
	s_andn2_b64 vcc, exec, s[12:13]
	s_cbranch_vccnz .LBB0_665
	s_barrier
	s_branch .LBB0_665

.LBB0_843:
	v_lshl_add_u32 v152, v136, 8, v156
	v_lshlrev_b32_e32 v136, 8, v142
	v_and_b32_e32 v136, 0x700, v136
	v_ashrrev_i32_e32 v153, 31, v152
	v_readlane_b32 s28, v250, 48
	v_or_b32_e32 v136, v136, v158
	v_lshlrev_b64 v[142:143], 12, v[152:153]
	v_readlane_b32 s29, v250, 49
	v_lshlrev_b32_e32 v136, 1, v136
	v_cvt_pk_bf16_f32 v124, v124, v125
	v_cvt_pk_bf16_f32 v125, v126, v127
	v_cvt_pk_bf16_f32 v126, v120, v121
	v_cvt_pk_bf16_f32 v127, v122, v123
	s_nop 0
	v_lshl_add_u64 v[142:143], s[28:29], 0, v[142:143]
	v_lshl_add_u64 v[142:143], v[142:143], 0, v[136:137]
	global_store_dwordx4 v[142:143], v[124:127], off nt
	v_cvt_pk_bf16_f32 v112, v112, v113
	v_cvt_pk_bf16_f32 v113, v114, v115
	v_cvt_pk_bf16_f32 v114, v104, v105
	v_or_b32_e32 v104, 16, v152
	v_ashrrev_i32_e32 v105, 31, v104
	v_lshlrev_b64 v[104:105], 12, v[104:105]
	v_lshl_add_u64 v[104:105], s[28:29], 0, v[104:105]
	v_cvt_pk_bf16_f32 v115, v106, v107
	global_store_dwordx4 v[142:143], v[112:115], off offset:256 nt
	s_nop 1
	v_lshl_add_u64 v[112:113], v[104:105], 0, v[136:137]
	v_cvt_pk_bf16_f32 v104, v116, v117
	v_cvt_pk_bf16_f32 v105, v118, v119
	v_cvt_pk_bf16_f32 v106, v108, v109
	v_cvt_pk_bf16_f32 v107, v110, v111
	global_store_dwordx4 v[112:113], v[104:107], off nt
	v_cvt_pk_bf16_f32 v96, v96, v97
	v_cvt_pk_bf16_f32 v97, v98, v99
	v_cvt_pk_bf16_f32 v98, v88, v89
	v_or_b32_e32 v88, 32, v152
	v_ashrrev_i32_e32 v89, 31, v88
	v_lshlrev_b64 v[88:89], 12, v[88:89]
	v_lshl_add_u64 v[88:89], s[28:29], 0, v[88:89]
	v_cvt_pk_bf16_f32 v99, v90, v91
	global_store_dwordx4 v[112:113], v[96:99], off offset:256 nt
	s_nop 1
	v_lshl_add_u64 v[96:97], v[88:89], 0, v[136:137]
	v_cvt_pk_bf16_f32 v88, v100, v101
	v_cvt_pk_bf16_f32 v89, v102, v103
	v_cvt_pk_bf16_f32 v90, v92, v93
	v_cvt_pk_bf16_f32 v91, v94, v95
	global_store_dwordx4 v[96:97], v[88:91], off nt
	v_cvt_pk_bf16_f32 v84, v84, v85
	v_cvt_pk_bf16_f32 v85, v86, v87
	v_cvt_pk_bf16_f32 v86, v76, v77
	v_or_b32_e32 v76, 48, v152
	v_ashrrev_i32_e32 v77, 31, v76
	v_lshlrev_b64 v[76:77], 12, v[76:77]
	v_lshl_add_u64 v[76:77], s[28:29], 0, v[76:77]
	v_cvt_pk_bf16_f32 v87, v78, v79
	global_store_dwordx4 v[96:97], v[84:87], off offset:256 nt
	s_mov_b64 s[28:29], 0x80000
	s_nop 0
	v_lshl_add_u64 v[84:85], v[76:77], 0, v[136:137]
	v_cvt_pk_bf16_f32 v76, v80, v81
	v_cvt_pk_bf16_f32 v77, v82, v83
	v_cvt_pk_bf16_f32 v78, v72, v73
	v_cvt_pk_bf16_f32 v79, v74, v75
	global_store_dwordx4 v[84:85], v[76:79], off nt
	v_cvt_pk_bf16_f32 v68, v68, v69
	v_cvt_pk_bf16_f32 v69, v70, v71
	v_cvt_pk_bf16_f32 v70, v64, v65
	v_lshl_add_u64 v[64:65], v[142:143], 0, s[28:29]
	s_mov_b32 s28, 0x80000
	v_cvt_pk_bf16_f32 v71, v66, v67
	global_store_dwordx4 v[84:85], v[68:71], off offset:256 nt
	v_cvt_pk_bf16_f32 v60, v60, v61
	v_cvt_pk_bf16_f32 v61, v62, v63
	v_cvt_pk_bf16_f32 v62, v56, v57
	v_add_co_u32_e32 v56, vcc, s28, v142
	v_cvt_pk_bf16_f32 v63, v58, v59
	s_mov_b64 s[28:29], 0x90000
	s_nop 0
	v_addc_co_u32_e32 v57, vcc, 0, v143, vcc
	global_store_dwordx4 v[56:57], v[60:63], off nt
	v_cvt_pk_bf16_f32 v48, v48, v49
	v_cvt_pk_bf16_f32 v49, v50, v51
	v_cvt_pk_bf16_f32 v50, v40, v41
	v_cvt_pk_bf16_f32 v51, v42, v43
	global_store_dwordx4 v[64:65], v[48:51], off offset:256 nt
	v_cvt_pk_bf16_f32 v40, v52, v53
	v_cvt_pk_bf16_f32 v41, v54, v55
	v_cvt_pk_bf16_f32 v42, v44, v45
	v_cvt_pk_bf16_f32 v43, v46, v47
	s_nop 1
	v_lshl_add_u64 v[48:49], v[142:143], 0, s[28:29]
	s_mov_b32 s28, 0x90000
	v_add_co_u32_e32 v44, vcc, s28, v142
	s_mov_b64 s[28:29], 0xa0000
	s_nop 0
	v_addc_co_u32_e32 v45, vcc, 0, v143, vcc
	global_store_dwordx4 v[44:45], v[40:43], off nt
	v_cvt_pk_bf16_f32 v32, v32, v33
	v_cvt_pk_bf16_f32 v33, v34, v35
	v_cvt_pk_bf16_f32 v34, v24, v25
	v_cvt_pk_bf16_f32 v35, v26, v27
	global_store_dwordx4 v[48:49], v[32:35], off offset:256 nt
	v_cvt_pk_bf16_f32 v24, v36, v37
	v_cvt_pk_bf16_f32 v25, v38, v39
	v_cvt_pk_bf16_f32 v26, v28, v29
	v_add_co_u32_e32 v28, vcc, s56, v142
	s_nop 0
	v_lshl_add_u64 v[32:33], v[142:143], 0, s[28:29]
	v_addc_co_u32_e32 v29, vcc, 0, v143, vcc
	v_cvt_pk_bf16_f32 v27, v30, v31
	global_store_dwordx4 v[28:29], v[24:27], off nt
	v_cvt_pk_bf16_f32 v16, v16, v17
	v_cvt_pk_bf16_f32 v17, v18, v19
	v_cvt_pk_bf16_f32 v18, v8, v9
	v_cvt_pk_bf16_f32 v19, v10, v11
	global_store_dwordx4 v[32:33], v[16:19], off offset:256 nt
	v_cvt_pk_bf16_f32 v8, v20, v21
	v_cvt_pk_bf16_f32 v9, v22, v23
	v_cvt_pk_bf16_f32 v10, v12, v13
	v_add_co_u32_e32 v12, vcc, s57, v142
	s_nop 0
	v_lshl_add_u64 v[16:17], v[142:143], 0, s[24:25]
	v_addc_co_u32_e32 v13, vcc, 0, v143, vcc
	s_andn2_b64 vcc, exec, s[26:27]
	s_mov_b64 s[26:27], -1
	v_cvt_pk_bf16_f32 v11, v14, v15
	global_store_dwordx4 v[12:13], v[8:11], off nt
	v_cvt_pk_bf16_f32 v4, v4, v5
	v_cvt_pk_bf16_f32 v5, v6, v7
	v_cvt_pk_bf16_f32 v6, v0, v1
	v_cvt_pk_bf16_f32 v7, v2, v3
	global_store_dwordx4 v[16:17], v[4:7], off offset:256 nt
	s_cbranch_vccnz .LBB0_814
	s_andn2_b64 vcc, exec, s[12:13]
	s_cbranch_vccnz .LBB0_813
	s_barrier
	s_branch .LBB0_813

.LBB0_1007:
	s_ashr_i32 s25, s61, 31
	s_lshr_b32 s25, s25, 29
	s_add_i32 s25, s61, s25
	s_ashr_i32 s25, s25, 3
	s_lshl_b32 s23, s61, 8
	s_mul_i32 s34, s25, 0x4200000
	v_readlane_b32 s16, v250, 46
	s_mul_hi_i32 s35, s25, 0x4200000
	v_readlane_b32 s17, v250, 47
	s_add_u32 s34, s16, s34
	s_addc_u32 s35, s17, s35
	s_lshl_b32 s25, s25, 11
	s_sub_i32 s23, s23, s25
	v_lshl_add_u32 v152, s30, 8, v146
	v_or_b32_e32 v144, s23, v148
	v_ashrrev_i32_e32 v145, 31, v144
	v_ashrrev_i32_e32 v153, 31, v152
	v_lshl_add_u64 v[154:155], v[144:145], 1, s[34:35]
	v_lshlrev_b64 v[144:145], 12, v[152:153]
	v_lshl_add_u64 v[144:145], v[154:155], 0, v[144:145]
	v_pk_add_f32 v[126:127], v[126:127], 0 op_sel_hi:[1,0]
	v_pk_add_f32 v[124:125], v[124:125], 0 op_sel_hi:[1,0]
	v_pk_add_f32 v[156:157], v[122:123], 0 op_sel_hi:[1,0]
	v_pk_add_f32 v[122:123], v[120:121], 0 op_sel_hi:[1,0]
	v_cvt_pk_bf16_f32 v120, v124, v125
	v_cvt_pk_bf16_f32 v121, v126, v127
	v_pk_add_f32 v[116:117], v[116:117], 0 op_sel_hi:[1,0]
	v_cvt_pk_bf16_f32 v122, v122, v123
	v_cvt_pk_bf16_f32 v123, v156, v157
	global_store_dwordx4 v[144:145], v[120:123], off nt
	v_pk_add_f32 v[118:119], v[118:119], 0 op_sel_hi:[1,0]
	v_pk_add_f32 v[112:113], v[112:113], 0 op_sel_hi:[1,0]
	v_pk_add_f32 v[120:121], v[110:111], 0 op_sel_hi:[1,0]
	v_pk_add_f32 v[110:111], v[108:109], 0 op_sel_hi:[1,0]
	v_cvt_pk_bf16_f32 v108, v116, v117
	v_cvt_pk_bf16_f32 v109, v118, v119
	v_pk_add_f32 v[100:101], v[100:101], 0 op_sel_hi:[1,0]
	v_cvt_pk_bf16_f32 v110, v110, v111
	v_cvt_pk_bf16_f32 v111, v120, v121
	global_store_dwordx4 v[144:145], v[108:111], off offset:256 nt
	v_pk_add_f32 v[102:103], v[102:103], 0 op_sel_hi:[1,0]
	v_pk_add_f32 v[96:97], v[96:97], 0 op_sel_hi:[1,0]
	v_or_b32_e32 v108, 16, v152
	v_ashrrev_i32_e32 v109, 31, v108
	v_lshlrev_b64 v[108:109], 12, v[108:109]
	v_lshl_add_u64 v[108:109], v[154:155], 0, v[108:109]
	v_pk_add_f32 v[110:111], v[114:115], 0 op_sel_hi:[1,0]
	v_pk_add_f32 v[114:115], v[106:107], 0 op_sel_hi:[1,0]
	v_pk_add_f32 v[106:107], v[104:105], 0 op_sel_hi:[1,0]
	v_cvt_pk_bf16_f32 v104, v112, v113
	v_cvt_pk_bf16_f32 v105, v110, v111
	v_pk_add_f32 v[84:85], v[84:85], 0 op_sel_hi:[1,0]
	v_cvt_pk_bf16_f32 v106, v106, v107
	v_cvt_pk_bf16_f32 v107, v114, v115
	global_store_dwordx4 v[108:109], v[104:107], off nt
	v_pk_add_f32 v[86:87], v[86:87], 0 op_sel_hi:[1,0]
	v_pk_add_f32 v[80:81], v[80:81], 0 op_sel_hi:[1,0]
	v_pk_add_f32 v[104:105], v[94:95], 0 op_sel_hi:[1,0]
	v_pk_add_f32 v[94:95], v[92:93], 0 op_sel_hi:[1,0]
	v_cvt_pk_bf16_f32 v92, v100, v101
	v_cvt_pk_bf16_f32 v93, v102, v103
	v_pk_add_f32 v[70:71], v[70:71], 0 op_sel_hi:[1,0]
	v_cvt_pk_bf16_f32 v94, v94, v95
	v_cvt_pk_bf16_f32 v95, v104, v105
	global_store_dwordx4 v[108:109], v[92:95], off offset:256 nt
	v_pk_add_f32 v[68:69], v[68:69], 0 op_sel_hi:[1,0]
	v_pk_add_f32 v[60:61], v[60:61], 0 op_sel_hi:[1,0]
	v_or_b32_e32 v92, 32, v152
	v_ashrrev_i32_e32 v93, 31, v92
	v_lshlrev_b64 v[92:93], 12, v[92:93]
	v_lshl_add_u64 v[92:93], v[154:155], 0, v[92:93]
	v_pk_add_f32 v[94:95], v[98:99], 0 op_sel_hi:[1,0]
	v_pk_add_f32 v[98:99], v[90:91], 0 op_sel_hi:[1,0]
	v_pk_add_f32 v[90:91], v[88:89], 0 op_sel_hi:[1,0]
	v_cvt_pk_bf16_f32 v88, v96, v97
	v_cvt_pk_bf16_f32 v89, v94, v95
	v_pk_add_f32 v[62:63], v[62:63], 0 op_sel_hi:[1,0]
	v_cvt_pk_bf16_f32 v90, v90, v91
	v_cvt_pk_bf16_f32 v91, v98, v99
	global_store_dwordx4 v[92:93], v[88:91], off nt
	v_pk_add_f32 v[54:55], v[54:55], 0 op_sel_hi:[1,0]
	v_pk_add_f32 v[52:53], v[52:53], 0 op_sel_hi:[1,0]
	v_pk_add_f32 v[88:89], v[78:79], 0 op_sel_hi:[1,0]
	v_pk_add_f32 v[78:79], v[76:77], 0 op_sel_hi:[1,0]
	v_cvt_pk_bf16_f32 v76, v84, v85
	v_cvt_pk_bf16_f32 v77, v86, v87
	v_pk_add_f32 v[48:49], v[48:49], 0 op_sel_hi:[1,0]
	v_cvt_pk_bf16_f32 v78, v78, v79
	v_cvt_pk_bf16_f32 v79, v88, v89
	global_store_dwordx4 v[92:93], v[76:79], off offset:256 nt
	v_pk_add_f32 v[38:39], v[38:39], 0 op_sel_hi:[1,0]
	v_pk_add_f32 v[36:37], v[36:37], 0 op_sel_hi:[1,0]
	v_or_b32_e32 v76, 48, v152
	v_ashrrev_i32_e32 v77, 31, v76
	v_lshlrev_b64 v[76:77], 12, v[76:77]
	v_lshl_add_u64 v[76:77], v[154:155], 0, v[76:77]
	v_pk_add_f32 v[78:79], v[82:83], 0 op_sel_hi:[1,0]
	v_pk_add_f32 v[82:83], v[74:75], 0 op_sel_hi:[1,0]
	v_pk_add_f32 v[74:75], v[72:73], 0 op_sel_hi:[1,0]
	v_cvt_pk_bf16_f32 v72, v80, v81
	v_cvt_pk_bf16_f32 v73, v78, v79
	v_pk_add_f32 v[32:33], v[32:33], 0 op_sel_hi:[1,0]
	v_cvt_pk_bf16_f32 v74, v74, v75
	v_cvt_pk_bf16_f32 v75, v82, v83
	global_store_dwordx4 v[76:77], v[72:75], off nt
	v_pk_add_f32 v[22:23], v[22:23], 0 op_sel_hi:[1,0]
	v_pk_add_f32 v[20:21], v[20:21], 0 op_sel_hi:[1,0]
	v_pk_add_f32 v[72:73], v[66:67], 0 op_sel_hi:[1,0]
	v_pk_add_f32 v[66:67], v[64:65], 0 op_sel_hi:[1,0]
	v_cvt_pk_bf16_f32 v64, v68, v69
	v_cvt_pk_bf16_f32 v65, v70, v71
	v_pk_add_f32 v[16:17], v[16:17], 0 op_sel_hi:[1,0]
	v_cvt_pk_bf16_f32 v66, v66, v67
	v_cvt_pk_bf16_f32 v67, v72, v73
	global_store_dwordx4 v[76:77], v[64:67], off offset:256 nt
	v_readlane_b32 s67, v250, 53
	v_pk_add_f32 v[6:7], v[6:7], 0 op_sel_hi:[1,0]
	v_pk_add_f32 v[66:67], v[58:59], 0 op_sel_hi:[1,0]
	v_pk_add_f32 v[58:59], v[56:57], 0 op_sel_hi:[1,0]
	v_cvt_pk_bf16_f32 v56, v60, v61
	v_add_co_u32_e32 v60, vcc, s57, v144
	v_cvt_pk_bf16_f32 v57, v62, v63
	v_cvt_pk_bf16_f32 v58, v58, v59
	v_cvt_pk_bf16_f32 v59, v66, v67
	v_lshl_add_u64 v[64:65], v[144:145], 0, s[4:5]
	s_nop 0
	v_addc_co_u32_e32 v61, vcc, 0, v145, vcc
	global_store_dwordx4 v[60:61], v[56:59], off nt
	v_pk_add_f32 v[4:5], v[4:5], 0 op_sel_hi:[1,0]
	s_nop 0
	v_pk_add_f32 v[56:57], v[46:47], 0 op_sel_hi:[1,0]
	v_pk_add_f32 v[46:47], v[44:45], 0 op_sel_hi:[1,0]
	v_cvt_pk_bf16_f32 v44, v52, v53
	v_cvt_pk_bf16_f32 v45, v54, v55
	s_nop 0
	v_cvt_pk_bf16_f32 v46, v46, v47
	v_cvt_pk_bf16_f32 v47, v56, v57
	global_store_dwordx4 v[64:65], v[44:47], off offset:256 nt
	s_nop 1
	v_pk_add_f32 v[46:47], v[50:51], 0 op_sel_hi:[1,0]
	v_pk_add_f32 v[50:51], v[42:43], 0 op_sel_hi:[1,0]
	v_pk_add_f32 v[42:43], v[40:41], 0 op_sel_hi:[1,0]
	v_cvt_pk_bf16_f32 v40, v48, v49
	v_cvt_pk_bf16_f32 v41, v46, v47
	v_add_co_u32_e32 v46, vcc, s58, v144
	v_cvt_pk_bf16_f32 v42, v42, v43
	v_cvt_pk_bf16_f32 v43, v50, v51
	v_lshl_add_u64 v[44:45], v[144:145], 0, s[12:13]
	s_nop 0
	v_addc_co_u32_e32 v47, vcc, 0, v145, vcc
	global_store_dwordx4 v[46:47], v[40:43], off nt
	s_nop 1
	v_pk_add_f32 v[40:41], v[30:31], 0 op_sel_hi:[1,0]
	v_pk_add_f32 v[30:31], v[28:29], 0 op_sel_hi:[1,0]
	v_cvt_pk_bf16_f32 v28, v36, v37
	v_cvt_pk_bf16_f32 v29, v38, v39
	s_nop 0
	v_cvt_pk_bf16_f32 v30, v30, v31
	v_cvt_pk_bf16_f32 v31, v40, v41
	global_store_dwordx4 v[44:45], v[28:31], off offset:256 nt
	s_nop 1
	v_pk_add_f32 v[30:31], v[34:35], 0 op_sel_hi:[1,0]
	v_pk_add_f32 v[34:35], v[26:27], 0 op_sel_hi:[1,0]
	v_pk_add_f32 v[26:27], v[24:25], 0 op_sel_hi:[1,0]
	v_cvt_pk_bf16_f32 v24, v32, v33
	v_cvt_pk_bf16_f32 v25, v30, v31
	v_add_co_u32_e32 v30, vcc, s59, v144
	v_cvt_pk_bf16_f32 v26, v26, v27
	v_cvt_pk_bf16_f32 v27, v34, v35
	v_lshl_add_u64 v[28:29], v[144:145], 0, s[14:15]
	s_nop 0
	v_addc_co_u32_e32 v31, vcc, 0, v145, vcc
	global_store_dwordx4 v[30:31], v[24:27], off nt
	s_nop 1
	v_pk_add_f32 v[24:25], v[14:15], 0 op_sel_hi:[1,0]
	v_pk_add_f32 v[14:15], v[12:13], 0 op_sel_hi:[1,0]
	v_cvt_pk_bf16_f32 v12, v20, v21
	v_cvt_pk_bf16_f32 v13, v22, v23
	s_nop 0
	v_cvt_pk_bf16_f32 v14, v14, v15
	v_cvt_pk_bf16_f32 v15, v24, v25
	global_store_dwordx4 v[28:29], v[12:15], off offset:256 nt
	s_nop 1
	v_pk_add_f32 v[14:15], v[18:19], 0 op_sel_hi:[1,0]
	v_pk_add_f32 v[18:19], v[10:11], 0 op_sel_hi:[1,0]
	v_pk_add_f32 v[10:11], v[8:9], 0 op_sel_hi:[1,0]
	v_cvt_pk_bf16_f32 v8, v16, v17
	v_cvt_pk_bf16_f32 v9, v14, v15
	v_add_co_u32_e32 v14, vcc, s60, v144
	v_lshl_add_u64 v[12:13], v[144:145], 0, s[18:19]
	s_nop 0
	v_addc_co_u32_e32 v15, vcc, 0, v145, vcc
	v_cvt_pk_bf16_f32 v10, v10, v11
	v_cvt_pk_bf16_f32 v11, v18, v19
	global_store_dwordx4 v[14:15], v[8:11], off nt
	s_andn2_b64 vcc, exec, s[2:3]
	s_mov_b64 s[2:3], -1
	v_pk_add_f32 v[8:9], v[2:3], 0 op_sel_hi:[1,0]
	v_pk_add_f32 v[2:3], v[0:1], 0 op_sel_hi:[1,0]
	v_cvt_pk_bf16_f32 v0, v4, v5
	v_cvt_pk_bf16_f32 v1, v6, v7
	s_nop 0
	v_cvt_pk_bf16_f32 v2, v2, v3
	v_cvt_pk_bf16_f32 v3, v8, v9
	global_store_dwordx4 v[12:13], v[0:3], off offset:256 nt
	s_cbranch_vccnz .LBB0_1000
	s_andn2_b64 vcc, exec, s[6:7]
	s_cbranch_vccnz .LBB0_999
	s_barrier
	s_branch .LBB0_999

.LBB0_1332:
	v_lshl_add_u32 v146, s30, 8, v148
	v_lshl_or_b32 v144, s58, 8, v150
	v_ashrrev_i32_e32 v147, 31, v146
	v_ashrrev_i32_e32 v145, 31, v144
	v_lshlrev_b64 v[154:155], 12, v[146:147]
	v_lshl_add_u64 v[154:155], s[96:97], 0, v[154:155]
	v_lshlrev_b64 v[158:159], 1, v[144:145]
	v_lshl_add_u64 v[144:145], v[154:155], 0, v[158:159]
	global_load_dwordx4 v[154:157], v[144:145], off
	s_waitcnt vmcnt(0)
	v_lshlrev_b32_e32 v147, 16, v154
	v_and_b32_e32 v154, 0xffff0000, v154
	v_lshlrev_b32_e32 v160, 16, v155
	v_and_b32_e32 v155, 0xffff0000, v155
	v_lshlrev_b32_e32 v162, 16, v157
	v_and_b32_e32 v157, 0xffff0000, v157
	v_lshlrev_b32_e32 v161, 16, v156
	v_and_b32_e32 v156, 0xffff0000, v156
	v_add_f32_e32 v124, v124, v147
	v_add_f32_e32 v125, v125, v154
	v_add_f32_e32 v126, v126, v160
	v_add_f32_e32 v127, v127, v155
	v_add_f32_e32 v123, v123, v157
	v_add_f32_e32 v147, v120, v161
	v_add_f32_e32 v154, v121, v156
	v_add_f32_e32 v155, v122, v162
	v_cvt_pk_bf16_f32 v120, v124, v125
	v_cvt_pk_bf16_f32 v121, v126, v127
	v_cvt_pk_bf16_f32 v122, v147, v154
	v_cvt_pk_bf16_f32 v123, v155, v123
	global_load_dwordx4 v[124:127], v[144:145], off offset:256
	v_or_b32_e32 v154, 16, v146
	v_ashrrev_i32_e32 v155, 31, v154
	v_lshlrev_b64 v[154:155], 12, v[154:155]
	v_lshl_add_u64 v[154:155], s[96:97], 0, v[154:155]
	global_store_dwordx4 v[144:145], v[120:123], off nt
	v_lshl_add_u64 v[154:155], v[154:155], 0, v[158:159]
	s_waitcnt vmcnt(1)
	v_lshlrev_b32_e32 v120, 16, v124
	v_and_b32_e32 v121, 0xffff0000, v124
	v_lshlrev_b32_e32 v122, 16, v125
	v_and_b32_e32 v123, 0xffff0000, v125
	v_lshlrev_b32_e32 v124, 16, v126
	v_and_b32_e32 v125, 0xffff0000, v126
	v_lshlrev_b32_e32 v126, 16, v127
	v_and_b32_e32 v127, 0xffff0000, v127
	v_add_f32_e32 v116, v116, v120
	v_add_f32_e32 v117, v117, v121
	v_add_f32_e32 v118, v118, v122
	v_add_f32_e32 v119, v119, v123
	v_add_f32_e32 v111, v111, v127
	v_add_f32_e32 v120, v108, v124
	v_add_f32_e32 v121, v109, v125
	v_add_f32_e32 v122, v110, v126
	v_cvt_pk_bf16_f32 v108, v116, v117
	v_cvt_pk_bf16_f32 v109, v118, v119
	v_cvt_pk_bf16_f32 v110, v120, v121
	v_cvt_pk_bf16_f32 v111, v122, v111
	global_load_dwordx4 v[116:119], v[154:155], off
	s_nop 0
	global_store_dwordx4 v[144:145], v[108:111], off offset:256 nt
	s_waitcnt vmcnt(1)
	s_nop 0
	v_lshlrev_b32_e32 v108, 16, v116
	v_and_b32_e32 v109, 0xffff0000, v116
	v_lshlrev_b32_e32 v110, 16, v117
	v_and_b32_e32 v111, 0xffff0000, v117
	v_lshlrev_b32_e32 v116, 16, v118
	v_and_b32_e32 v117, 0xffff0000, v118
	v_lshlrev_b32_e32 v118, 16, v119
	v_and_b32_e32 v119, 0xffff0000, v119
	v_add_f32_e32 v108, v112, v108
	v_add_f32_e32 v109, v113, v109
	v_add_f32_e32 v110, v114, v110
	v_add_f32_e32 v111, v115, v111
	v_add_f32_e32 v107, v107, v119
	v_add_f32_e32 v112, v104, v116
	v_add_f32_e32 v113, v105, v117
	v_add_f32_e32 v114, v106, v118
	v_cvt_pk_bf16_f32 v104, v108, v109
	v_cvt_pk_bf16_f32 v105, v110, v111
	v_cvt_pk_bf16_f32 v106, v112, v113
	v_cvt_pk_bf16_f32 v107, v114, v107
	global_load_dwordx4 v[108:111], v[154:155], off offset:256
	v_or_b32_e32 v112, 32, v146
	v_ashrrev_i32_e32 v113, 31, v112
	v_lshlrev_b64 v[112:113], 12, v[112:113]
	v_lshl_add_u64 v[112:113], s[96:97], 0, v[112:113]
	global_store_dwordx4 v[154:155], v[104:107], off nt
	v_lshl_add_u64 v[112:113], v[112:113], 0, v[158:159]
	s_waitcnt vmcnt(1)
	v_lshlrev_b32_e32 v104, 16, v108
	v_and_b32_e32 v105, 0xffff0000, v108
	v_lshlrev_b32_e32 v106, 16, v109
	v_and_b32_e32 v107, 0xffff0000, v109
	v_lshlrev_b32_e32 v108, 16, v110
	v_and_b32_e32 v109, 0xffff0000, v110
	v_lshlrev_b32_e32 v110, 16, v111
	v_and_b32_e32 v111, 0xffff0000, v111
	v_add_f32_e32 v100, v100, v104
	v_add_f32_e32 v101, v101, v105
	v_add_f32_e32 v102, v102, v106
	v_add_f32_e32 v103, v103, v107
	v_add_f32_e32 v95, v95, v111
	v_add_f32_e32 v104, v92, v108
	v_add_f32_e32 v105, v93, v109
	v_add_f32_e32 v106, v94, v110
	v_cvt_pk_bf16_f32 v92, v100, v101
	v_cvt_pk_bf16_f32 v93, v102, v103
	v_cvt_pk_bf16_f32 v94, v104, v105
	v_cvt_pk_bf16_f32 v95, v106, v95
	global_load_dwordx4 v[100:103], v[112:113], off
	s_nop 0
	global_store_dwordx4 v[154:155], v[92:95], off offset:256 nt
	s_waitcnt vmcnt(1)
	s_nop 0
	v_lshlrev_b32_e32 v92, 16, v100
	v_and_b32_e32 v93, 0xffff0000, v100
	v_lshlrev_b32_e32 v94, 16, v101
	v_and_b32_e32 v95, 0xffff0000, v101
	v_lshlrev_b32_e32 v100, 16, v102
	v_and_b32_e32 v101, 0xffff0000, v102
	v_lshlrev_b32_e32 v102, 16, v103
	v_and_b32_e32 v103, 0xffff0000, v103
	v_add_f32_e32 v92, v96, v92
	v_add_f32_e32 v93, v97, v93
	v_add_f32_e32 v94, v98, v94
	v_add_f32_e32 v95, v99, v95
	v_add_f32_e32 v91, v91, v103
	v_add_f32_e32 v96, v88, v100
	v_add_f32_e32 v97, v89, v101
	v_add_f32_e32 v98, v90, v102
	v_cvt_pk_bf16_f32 v88, v92, v93
	v_cvt_pk_bf16_f32 v89, v94, v95
	v_cvt_pk_bf16_f32 v90, v96, v97
	v_cvt_pk_bf16_f32 v91, v98, v91
	global_load_dwordx4 v[92:95], v[112:113], off offset:256
	v_or_b32_e32 v96, 48, v146
	v_ashrrev_i32_e32 v97, 31, v96
	v_lshlrev_b64 v[96:97], 12, v[96:97]
	v_lshl_add_u64 v[96:97], s[96:97], 0, v[96:97]
	global_store_dwordx4 v[112:113], v[88:91], off nt
	v_lshl_add_u64 v[96:97], v[96:97], 0, v[158:159]
	s_waitcnt vmcnt(1)
	v_lshlrev_b32_e32 v88, 16, v92
	v_and_b32_e32 v89, 0xffff0000, v92
	v_lshlrev_b32_e32 v90, 16, v93
	v_and_b32_e32 v91, 0xffff0000, v93
	v_lshlrev_b32_e32 v92, 16, v94
	v_and_b32_e32 v93, 0xffff0000, v94
	v_lshlrev_b32_e32 v94, 16, v95
	v_and_b32_e32 v95, 0xffff0000, v95
	v_add_f32_e32 v84, v84, v88
	v_add_f32_e32 v85, v85, v89
	v_add_f32_e32 v86, v86, v90
	v_add_f32_e32 v87, v87, v91
	v_add_f32_e32 v79, v79, v95
	v_add_f32_e32 v88, v76, v92
	v_add_f32_e32 v89, v77, v93
	v_add_f32_e32 v90, v78, v94
	v_cvt_pk_bf16_f32 v76, v84, v85
	v_cvt_pk_bf16_f32 v77, v86, v87
	v_cvt_pk_bf16_f32 v78, v88, v89
	v_cvt_pk_bf16_f32 v79, v90, v79
	global_load_dwordx4 v[84:87], v[96:97], off
	s_nop 0
	global_store_dwordx4 v[112:113], v[76:79], off offset:256 nt
	s_waitcnt vmcnt(1)
	s_nop 0
	v_lshlrev_b32_e32 v76, 16, v84
	v_and_b32_e32 v77, 0xffff0000, v84
	v_lshlrev_b32_e32 v78, 16, v85
	v_and_b32_e32 v79, 0xffff0000, v85
	v_lshlrev_b32_e32 v84, 16, v86
	v_and_b32_e32 v85, 0xffff0000, v86
	v_lshlrev_b32_e32 v86, 16, v87
	v_and_b32_e32 v87, 0xffff0000, v87
	v_add_f32_e32 v76, v80, v76
	v_add_f32_e32 v77, v81, v77
	v_add_f32_e32 v78, v82, v78
	v_add_f32_e32 v79, v83, v79
	v_add_f32_e32 v75, v75, v87
	v_add_f32_e32 v80, v72, v84
	v_add_f32_e32 v81, v73, v85
	v_add_f32_e32 v82, v74, v86
	v_cvt_pk_bf16_f32 v72, v76, v77
	v_cvt_pk_bf16_f32 v73, v78, v79
	v_cvt_pk_bf16_f32 v74, v80, v81
	v_cvt_pk_bf16_f32 v75, v82, v75
	global_load_dwordx4 v[76:79], v[96:97], off offset:256
	v_add_co_u32_e32 v80, vcc, s52, v144
	global_store_dwordx4 v[96:97], v[72:75], off nt
	s_nop 0
	v_addc_co_u32_e32 v81, vcc, 0, v145, vcc
	s_waitcnt vmcnt(1)
	v_lshlrev_b32_e32 v72, 16, v76
	v_and_b32_e32 v73, 0xffff0000, v76
	v_lshlrev_b32_e32 v74, 16, v77
	v_and_b32_e32 v75, 0xffff0000, v77
	v_lshlrev_b32_e32 v76, 16, v78
	v_and_b32_e32 v77, 0xffff0000, v78
	v_lshlrev_b32_e32 v78, 16, v79
	v_and_b32_e32 v79, 0xffff0000, v79
	v_add_f32_e32 v68, v68, v72
	v_add_f32_e32 v69, v69, v73
	v_add_f32_e32 v70, v70, v74
	v_add_f32_e32 v71, v71, v75
	v_add_f32_e32 v67, v67, v79
	v_add_f32_e32 v72, v64, v76
	v_add_f32_e32 v73, v65, v77
	v_add_f32_e32 v74, v66, v78
	v_cvt_pk_bf16_f32 v64, v68, v69
	v_cvt_pk_bf16_f32 v65, v70, v71
	v_cvt_pk_bf16_f32 v66, v72, v73
	v_cvt_pk_bf16_f32 v67, v74, v67
	global_load_dwordx4 v[68:71], v[80:81], off
	v_lshl_add_u64 v[72:73], v[144:145], 0, s[6:7]
	global_store_dwordx4 v[96:97], v[64:67], off offset:256 nt
	s_waitcnt vmcnt(1)
	s_nop 0
	v_lshlrev_b32_e32 v64, 16, v68
	v_and_b32_e32 v65, 0xffff0000, v68
	v_lshlrev_b32_e32 v66, 16, v69
	v_and_b32_e32 v67, 0xffff0000, v69
	v_lshlrev_b32_e32 v68, 16, v70
	v_and_b32_e32 v69, 0xffff0000, v70
	v_lshlrev_b32_e32 v70, 16, v71
	v_and_b32_e32 v71, 0xffff0000, v71
	v_add_f32_e32 v60, v60, v64
	v_add_f32_e32 v61, v61, v65
	v_add_f32_e32 v62, v62, v66
	v_add_f32_e32 v63, v63, v67
	v_add_f32_e32 v59, v59, v71
	v_add_f32_e32 v64, v56, v68
	v_add_f32_e32 v65, v57, v69
	v_add_f32_e32 v66, v58, v70
	v_cvt_pk_bf16_f32 v56, v60, v61
	v_cvt_pk_bf16_f32 v57, v62, v63
	v_cvt_pk_bf16_f32 v58, v64, v65
	v_cvt_pk_bf16_f32 v59, v66, v59
	global_load_dwordx4 v[60:63], v[72:73], off offset:256
	v_add_co_u32_e32 v64, vcc, s53, v144
	global_store_dwordx4 v[80:81], v[56:59], off nt
	s_nop 0
	v_addc_co_u32_e32 v65, vcc, 0, v145, vcc
	s_waitcnt vmcnt(1)
	v_lshlrev_b32_e32 v56, 16, v60
	v_and_b32_e32 v57, 0xffff0000, v60
	v_lshlrev_b32_e32 v58, 16, v61
	v_and_b32_e32 v59, 0xffff0000, v61
	v_lshlrev_b32_e32 v60, 16, v62
	v_and_b32_e32 v61, 0xffff0000, v62
	v_lshlrev_b32_e32 v62, 16, v63
	v_and_b32_e32 v63, 0xffff0000, v63
	v_add_f32_e32 v52, v52, v56
	v_add_f32_e32 v53, v53, v57
	v_add_f32_e32 v54, v54, v58
	v_add_f32_e32 v55, v55, v59
	v_add_f32_e32 v51, v51, v63
	v_add_f32_e32 v56, v48, v60
	v_add_f32_e32 v57, v49, v61
	v_add_f32_e32 v58, v50, v62
	v_cvt_pk_bf16_f32 v48, v52, v53
	v_cvt_pk_bf16_f32 v49, v54, v55
	v_cvt_pk_bf16_f32 v50, v56, v57
	v_cvt_pk_bf16_f32 v51, v58, v51
	global_load_dwordx4 v[52:55], v[64:65], off
	v_lshl_add_u64 v[56:57], v[144:145], 0, s[14:15]
	global_store_dwordx4 v[72:73], v[48:51], off offset:256 nt
	s_waitcnt vmcnt(1)
	s_nop 0
	v_lshlrev_b32_e32 v48, 16, v52
	v_and_b32_e32 v49, 0xffff0000, v52
	v_lshlrev_b32_e32 v50, 16, v53
	v_and_b32_e32 v51, 0xffff0000, v53
	v_lshlrev_b32_e32 v52, 16, v54
	v_and_b32_e32 v53, 0xffff0000, v54
	v_lshlrev_b32_e32 v54, 16, v55
	v_and_b32_e32 v55, 0xffff0000, v55
	v_add_f32_e32 v44, v44, v48
	v_add_f32_e32 v45, v45, v49
	v_add_f32_e32 v46, v46, v50
	v_add_f32_e32 v47, v47, v51
	v_add_f32_e32 v43, v43, v55
	v_add_f32_e32 v48, v40, v52
	v_add_f32_e32 v49, v41, v53
	v_add_f32_e32 v50, v42, v54
	v_cvt_pk_bf16_f32 v40, v44, v45
	v_cvt_pk_bf16_f32 v41, v46, v47
	v_cvt_pk_bf16_f32 v42, v48, v49
	v_cvt_pk_bf16_f32 v43, v50, v43
	global_load_dwordx4 v[44:47], v[56:57], off offset:256
	v_add_co_u32_e32 v48, vcc, s54, v144
	global_store_dwordx4 v[64:65], v[40:43], off nt
	s_nop 0
	v_addc_co_u32_e32 v49, vcc, 0, v145, vcc
	s_waitcnt vmcnt(1)
	v_lshlrev_b32_e32 v40, 16, v44
	v_and_b32_e32 v41, 0xffff0000, v44
	v_lshlrev_b32_e32 v42, 16, v45
	v_and_b32_e32 v43, 0xffff0000, v45
	v_lshlrev_b32_e32 v44, 16, v46
	v_and_b32_e32 v45, 0xffff0000, v46
	v_lshlrev_b32_e32 v46, 16, v47
	v_and_b32_e32 v47, 0xffff0000, v47
	v_add_f32_e32 v36, v36, v40
	v_add_f32_e32 v37, v37, v41
	v_add_f32_e32 v38, v38, v42
	v_add_f32_e32 v39, v39, v43
	v_add_f32_e32 v35, v35, v47
	v_add_f32_e32 v40, v32, v44
	v_add_f32_e32 v41, v33, v45
	v_add_f32_e32 v42, v34, v46
	v_cvt_pk_bf16_f32 v32, v36, v37
	v_cvt_pk_bf16_f32 v33, v38, v39
	v_cvt_pk_bf16_f32 v34, v40, v41
	v_cvt_pk_bf16_f32 v35, v42, v35
	global_load_dwordx4 v[36:39], v[48:49], off
	v_lshl_add_u64 v[40:41], v[144:145], 0, s[16:17]
	global_store_dwordx4 v[56:57], v[32:35], off offset:256 nt
	s_waitcnt vmcnt(1)
	s_nop 0
	v_lshlrev_b32_e32 v32, 16, v36
	v_and_b32_e32 v33, 0xffff0000, v36
	v_lshlrev_b32_e32 v34, 16, v37
	v_and_b32_e32 v35, 0xffff0000, v37
	v_lshlrev_b32_e32 v36, 16, v38
	v_and_b32_e32 v37, 0xffff0000, v38
	v_lshlrev_b32_e32 v38, 16, v39
	v_and_b32_e32 v39, 0xffff0000, v39
	v_add_f32_e32 v28, v28, v32
	v_add_f32_e32 v29, v29, v33
	v_add_f32_e32 v30, v30, v34
	v_add_f32_e32 v31, v31, v35
	v_add_f32_e32 v27, v27, v39
	v_add_f32_e32 v32, v24, v36
	v_add_f32_e32 v33, v25, v37
	v_add_f32_e32 v34, v26, v38
	v_cvt_pk_bf16_f32 v24, v28, v29
	v_cvt_pk_bf16_f32 v25, v30, v31
	v_cvt_pk_bf16_f32 v26, v32, v33
	v_cvt_pk_bf16_f32 v27, v34, v27
	global_load_dwordx4 v[28:31], v[40:41], off offset:256
	v_add_co_u32_e32 v32, vcc, s55, v144
	global_store_dwordx4 v[48:49], v[24:27], off nt
	s_nop 0
	v_addc_co_u32_e32 v33, vcc, 0, v145, vcc
	s_andn2_b64 vcc, exec, s[2:3]
	s_mov_b64 s[2:3], -1
	s_waitcnt vmcnt(1)
	v_lshlrev_b32_e32 v24, 16, v28
	v_and_b32_e32 v25, 0xffff0000, v28
	v_lshlrev_b32_e32 v26, 16, v29
	v_and_b32_e32 v27, 0xffff0000, v29
	v_lshlrev_b32_e32 v28, 16, v30
	v_and_b32_e32 v29, 0xffff0000, v30
	v_lshlrev_b32_e32 v30, 16, v31
	v_and_b32_e32 v31, 0xffff0000, v31
	v_add_f32_e32 v20, v20, v24
	v_add_f32_e32 v21, v21, v25
	v_add_f32_e32 v22, v22, v26
	v_add_f32_e32 v23, v23, v27
	v_add_f32_e32 v19, v19, v31
	v_add_f32_e32 v24, v16, v28
	v_add_f32_e32 v25, v17, v29
	v_add_f32_e32 v26, v18, v30
	v_cvt_pk_bf16_f32 v16, v20, v21
	v_cvt_pk_bf16_f32 v17, v22, v23
	v_cvt_pk_bf16_f32 v18, v24, v25
	v_cvt_pk_bf16_f32 v19, v26, v19
	global_load_dwordx4 v[20:23], v[32:33], off
	v_lshl_add_u64 v[24:25], v[144:145], 0, s[18:19]
	global_store_dwordx4 v[40:41], v[16:19], off offset:256 nt
	s_waitcnt vmcnt(1)
	s_nop 0
	v_lshlrev_b32_e32 v16, 16, v20
	v_and_b32_e32 v17, 0xffff0000, v20
	v_lshlrev_b32_e32 v18, 16, v21
	v_and_b32_e32 v19, 0xffff0000, v21
	v_lshlrev_b32_e32 v20, 16, v22
	v_and_b32_e32 v21, 0xffff0000, v22
	v_lshlrev_b32_e32 v22, 16, v23
	v_and_b32_e32 v23, 0xffff0000, v23
	v_add_f32_e32 v12, v12, v16
	v_add_f32_e32 v13, v13, v17
	v_add_f32_e32 v14, v14, v18
	v_add_f32_e32 v15, v15, v19
	v_add_f32_e32 v11, v11, v23
	v_add_f32_e32 v16, v8, v20
	v_add_f32_e32 v17, v9, v21
	v_add_f32_e32 v18, v10, v22
	v_cvt_pk_bf16_f32 v8, v12, v13
	v_cvt_pk_bf16_f32 v9, v14, v15
	v_cvt_pk_bf16_f32 v10, v16, v17
	v_cvt_pk_bf16_f32 v11, v18, v11
	global_load_dwordx4 v[12:15], v[24:25], off offset:256
	s_nop 0
	global_store_dwordx4 v[32:33], v[8:11], off nt
	s_waitcnt vmcnt(1)
	s_nop 0
	v_lshlrev_b32_e32 v8, 16, v12
	v_and_b32_e32 v9, 0xffff0000, v12
	v_lshlrev_b32_e32 v10, 16, v13
	v_and_b32_e32 v11, 0xffff0000, v13
	v_lshlrev_b32_e32 v12, 16, v14
	v_and_b32_e32 v13, 0xffff0000, v14
	v_lshlrev_b32_e32 v14, 16, v15
	v_and_b32_e32 v15, 0xffff0000, v15
	v_add_f32_e32 v3, v3, v15
	v_add_f32_e32 v4, v4, v8
	v_add_f32_e32 v5, v5, v9
	v_add_f32_e32 v6, v6, v10
	v_add_f32_e32 v7, v7, v11
	v_add_f32_e32 v8, v0, v12
	v_add_f32_e32 v9, v1, v13
	v_add_f32_e32 v10, v2, v14
	v_cvt_pk_bf16_f32 v0, v4, v5
	v_cvt_pk_bf16_f32 v1, v6, v7
	v_cvt_pk_bf16_f32 v2, v8, v9
	v_cvt_pk_bf16_f32 v3, v10, v3
	global_store_dwordx4 v[24:25], v[0:3], off offset:256 nt
	s_cbranch_vccnz .LBB0_1321
	s_andn2_b64 vcc, exec, s[8:9]
	s_cbranch_vccnz .LBB0_1320
	s_barrier
	s_branch .LBB0_1320

.LBB0_1350:
	v_lshl_or_b32 v138, s12, 8, v134
	s_ashr_i32 s12, s14, 31
	s_lshr_b32 s12, s12, 24
	s_add_i32 s12, s14, s12
	s_ashr_i32 s52, s12, 8
	s_ashr_i32 s53, s52, 31
	s_lshl_b64 s[52:53], s[52:53], 22
	s_add_u32 s52, s43, s52
	v_lshl_add_u32 v140, s10, 8, v133
	s_addc_u32 s53, s44, s53
	v_ashrrev_i32_e32 v139, 31, v138
	v_ashrrev_i32_e32 v141, 31, v140
	v_lshl_add_u64 v[138:139], v[138:139], 2, s[52:53]
	v_lshlrev_b64 v[142:143], 13, v[140:141]
	v_lshl_add_u64 v[142:143], v[138:139], 0, v[142:143]
	global_store_dwordx4 v[142:143], v[32:35], off nt
	global_store_dwordx4 v[142:143], v[36:39], off offset:64 nt
	global_store_dwordx4 v[142:143], v[56:59], off offset:512 nt
	global_store_dwordx4 v[142:143], v[64:67], off offset:576 nt
	v_or_b32_e32 v32, 16, v140
	v_ashrrev_i32_e32 v33, 31, v32
	v_lshlrev_b64 v[32:33], 13, v[32:33]
	v_lshl_add_u64 v[32:33], v[138:139], 0, v[32:33]
	global_store_dwordx4 v[32:33], v[16:19], off nt
	global_store_dwordx4 v[32:33], v[20:23], off offset:64 nt
	global_store_dwordx4 v[32:33], v[48:51], off offset:512 nt
	global_store_dwordx4 v[32:33], v[52:55], off offset:576 nt
	v_or_b32_e32 v16, 32, v140
	v_ashrrev_i32_e32 v17, 31, v16
	v_lshlrev_b64 v[16:17], 13, v[16:17]
	v_lshl_add_u64 v[16:17], v[138:139], 0, v[16:17]
	global_store_dwordx4 v[16:17], v[8:11], off nt
	global_store_dwordx4 v[16:17], v[12:15], off offset:64 nt
	global_store_dwordx4 v[16:17], v[40:43], off offset:512 nt
	global_store_dwordx4 v[16:17], v[44:47], off offset:576 nt
	v_or_b32_e32 v8, 48, v140
	v_ashrrev_i32_e32 v9, 31, v8
	v_lshlrev_b64 v[8:9], 13, v[8:9]
	v_lshl_add_u64 v[8:9], v[138:139], 0, v[8:9]
	global_store_dwordx4 v[8:9], v[0:3], off nt
	global_store_dwordx4 v[8:9], v[4:7], off offset:64 nt
	global_store_dwordx4 v[8:9], v[24:27], off offset:512 nt
	global_store_dwordx4 v[8:9], v[28:31], off offset:576 nt
	v_add_co_u32_e32 v2, vcc, s60, v142
	v_lshl_add_u64 v[0:1], v[142:143], 0, s[24:25]
	s_nop 0
	v_addc_co_u32_e32 v3, vcc, 0, v143, vcc
	global_store_dwordx4 v[2:3], v[92:95], off nt
	global_store_dwordx4 v[0:1], v[100:103], off offset:64 nt
	global_store_dwordx4 v[0:1], v[120:123], off offset:512 nt
	global_store_dwordx4 v[0:1], v[124:127], off offset:576 nt
	v_add_co_u32_e32 v2, vcc, s61, v142
	v_lshl_add_u64 v[0:1], v[142:143], 0, s[26:27]
	s_nop 0
	v_addc_co_u32_e32 v3, vcc, 0, v143, vcc
	global_store_dwordx4 v[2:3], v[80:83], off nt
	global_store_dwordx4 v[0:1], v[84:87], off offset:64 nt
	global_store_dwordx4 v[0:1], v[112:115], off offset:512 nt
	global_store_dwordx4 v[0:1], v[116:119], off offset:576 nt
	v_add_co_u32_e32 v2, vcc, s62, v142
	v_lshl_add_u64 v[0:1], v[142:143], 0, s[28:29]
	s_nop 0
	v_addc_co_u32_e32 v3, vcc, 0, v143, vcc
	global_store_dwordx4 v[2:3], v[72:75], off nt
	global_store_dwordx4 v[0:1], v[76:79], off offset:64 nt
	global_store_dwordx4 v[0:1], v[104:107], off offset:512 nt
	global_store_dwordx4 v[0:1], v[108:111], off offset:576 nt
	v_add_co_u32_e32 v2, vcc, 0x160000, v142
	v_readlane_b32 s67, v250, 53
	s_nop 0
	v_addc_co_u32_e32 v3, vcc, 0, v143, vcc
	s_and_b64 vcc, exec, s[2:3]
	s_mov_b64 s[2:3], -1
	v_lshl_add_u64 v[0:1], v[142:143], 0, s[30:31]
	global_store_dwordx4 v[2:3], v[60:63], off nt
	global_store_dwordx4 v[0:1], v[68:71], off offset:64 nt
	global_store_dwordx4 v[0:1], v[88:91], off offset:512 nt
	global_store_dwordx4 v[0:1], v[96:99], off offset:576 nt
	s_cbranch_vccnz .LBB0_1341
	s_andn2_b64 vcc, exec, s[6:7]
	s_cbranch_vccnz .LBB0_1340
	s_barrier
	s_branch .LBB0_1340

.LBB0_1581:
	s_or_b64 exec, exec, s[36:37]
	v_mul_f32_e32 v168, 0xbfb8aa3b, v64
	v_exp_f32_e32 v168, v168
	v_mul_f32_e32 v169, 0xbfb8aa3b, v65
	v_exp_f32_e32 v169, v169
	v_mul_f32_e32 v150, 0xbfb8aa3b, v73
	v_add_f32_e32 v168, 1.0, v168
	v_rcp_f32_e32 v168, v168
	v_add_f32_e32 v169, 1.0, v169
	v_rcp_f32_e32 v169, v169
	v_exp_f32_e32 v150, v150
	v_mul_f32_e32 v168, v64, v168
	v_lshlrev_b32_e32 v143, 7, v128
	v_mul_f32_e32 v168, v168, v32
	v_and_b32_e32 v143, 0x180, v143
	s_waitcnt vmcnt(0)
	v_mul_f32_e32 v170, v168, v130
	v_mul_f32_e32 v168, v65, v169
	v_mul_f32_e32 v169, 0xbfb8aa3b, v66
	v_mul_f32_e32 v149, 0xbfb8aa3b, v72
	v_or_b32_e32 v167, v143, v137
	v_add_f32_e32 v143, 1.0, v150
	v_mul_f32_e32 v150, 0xbfb8aa3b, v74
	v_mul_f32_e32 v151, 0xbfb8aa3b, v75
	v_exp_f32_e32 v169, v169
	v_mul_f32_e32 v171, 0xbfb8aa3b, v67
	v_exp_f32_e32 v149, v149
	v_exp_f32_e32 v150, v150
	v_exp_f32_e32 v151, v151
	v_exp_f32_e32 v171, v171
	v_mul_f32_e32 v168, v168, v33
	v_add_f32_e32 v169, 1.0, v169
	v_add_f32_e32 v149, 1.0, v149
	v_rcp_f32_e32 v143, v143
	v_add_f32_e32 v150, 1.0, v150
	v_add_f32_e32 v151, 1.0, v151
	v_rcp_f32_e32 v169, v169
	v_mul_f32_e32 v172, v168, v130
	v_add_f32_e32 v168, 1.0, v171
	v_rcp_f32_e32 v149, v149
	v_rcp_f32_e32 v150, v150
	v_rcp_f32_e32 v151, v151
	v_rcp_f32_e32 v168, v168
	v_mul_f32_e32 v143, v73, v143
	v_mul_f32_e32 v169, v66, v169
	v_mul_f32_e32 v149, v72, v149
	v_mul_f32_e32 v143, v143, v37
	v_mul_f32_e32 v150, v74, v150
	v_mul_f32_e32 v151, v75, v151
	v_mul_f32_e32 v169, v169, v34
	v_mul_f32_e32 v168, v67, v168
	v_mul_f32_e32 v149, v149, v36
	v_mul_f32_e32 v143, v143, v130
	v_mul_f32_e32 v150, v150, v38
	v_mul_f32_e32 v151, v151, v39
	v_mul_f32_e32 v171, v169, v130
	v_mul_f32_e32 v168, v168, v35
	v_mul_f32_e32 v149, v149, v130
	v_mul_f32_e32 v150, v150, v130
	v_mul_f32_e32 v151, v151, v130
	v_mul_f32_e32 v130, v168, v130
	v_cvt_pk_bf16_f32 v168, v149, v143
	v_cvt_pk_bf16_f32 v169, v150, v151
	v_cvt_pk_bf16_f32 v170, v170, v172
	v_cvt_pk_bf16_f32 v171, v171, v130
	ds_read_b32 v143, v133
	v_ashrrev_i32_e32 v149, 31, v148
	v_lshlrev_b64 v[150:151], 10, v[148:149]
	v_lshlrev_b32_e32 v130, 1, v167
	v_lshl_add_u64 v[150:151], s[16:17], 0, v[150:151]
	s_waitcnt lgkmcnt(0)
	v_lshlrev_b32_e32 v149, 2, v143
	v_add_u32_e32 v149, 0, v149
	v_add_u32_e32 v167, 0x20100, v149
	v_add_u32_e32 v149, 0x20200, v149
	ds_read_b32 v167, v167
	ds_read_b32 v172, v149
	v_lshl_add_u64 v[150:151], v[150:151], 0, v[130:131]
	global_store_dwordx4 v[150:151], v[168:171], off nt
	v_or_b32_e32 v150, 16, v148
	s_waitcnt lgkmcnt(1)
	v_sub_u32_e32 v149, v150, v167
	s_waitcnt lgkmcnt(0)
	v_cmp_lt_i32_e32 vcc, v149, v172
	s_and_saveexec_b64 s[36:37], vcc
	s_cbranch_execz .LBB0_1583
	v_mul_lo_u32 v135, v143, s66
	v_add_u32_e32 v168, v149, v135
	v_ashrrev_i32_e32 v169, 31, v168
	v_lshl_add_u64 v[168:169], v[168:169], 2, s[18:19]
	global_load_dword v135, v[168:169], off
.LBB0_1583:
	s_or_b64 exec, exec, s[36:37]
	v_mul_f32_e32 v168, 0xbfb8aa3b, v56
	v_exp_f32_e32 v168, v168
	v_mul_f32_e32 v169, 0xbfb8aa3b, v57
	v_exp_f32_e32 v169, v169
	v_mul_f32_e32 v149, 0xbfb8aa3b, v61
	v_add_f32_e32 v168, 1.0, v168
	v_rcp_f32_e32 v168, v168
	v_add_f32_e32 v169, 1.0, v169
	v_rcp_f32_e32 v169, v169
	v_mul_f32_e32 v143, 0xbfb8aa3b, v60
	v_mul_f32_e32 v168, v56, v168
	v_mul_f32_e32 v168, v168, v24
	s_waitcnt vmcnt(0)
	v_mul_f32_e32 v170, v168, v135
	v_mul_f32_e32 v168, v57, v169
	v_mul_f32_e32 v169, 0xbfb8aa3b, v58
	v_exp_f32_e32 v149, v149
	v_mul_f32_e32 v151, 0xbfb8aa3b, v62
	v_mul_f32_e32 v167, 0xbfb8aa3b, v63
	v_exp_f32_e32 v169, v169
	v_mul_f32_e32 v171, 0xbfb8aa3b, v59
	v_exp_f32_e32 v143, v143
	v_exp_f32_e32 v151, v151
	v_exp_f32_e32 v167, v167
	v_exp_f32_e32 v171, v171
	v_add_f32_e32 v149, 1.0, v149
	v_mul_f32_e32 v168, v168, v25
	v_add_f32_e32 v169, 1.0, v169
	v_add_f32_e32 v143, 1.0, v143
	v_rcp_f32_e32 v149, v149
	v_add_f32_e32 v151, 1.0, v151
	v_add_f32_e32 v167, 1.0, v167
	v_rcp_f32_e32 v169, v169
	v_mul_f32_e32 v172, v168, v135
	v_add_f32_e32 v168, 1.0, v171
	v_rcp_f32_e32 v143, v143
	v_rcp_f32_e32 v151, v151
	v_rcp_f32_e32 v167, v167
	v_rcp_f32_e32 v168, v168
	v_mul_f32_e32 v149, v61, v149
	v_mul_f32_e32 v169, v58, v169
	v_mul_f32_e32 v143, v60, v143
	v_mul_f32_e32 v149, v149, v29
	v_mul_f32_e32 v151, v62, v151
	v_mul_f32_e32 v167, v63, v167
	v_mul_f32_e32 v169, v169, v26
	v_mul_f32_e32 v168, v59, v168
	v_mul_f32_e32 v143, v143, v28
	v_mul_f32_e32 v149, v149, v135
	v_mul_f32_e32 v151, v151, v30
	v_mul_f32_e32 v167, v167, v31
	v_mul_f32_e32 v171, v169, v135
	v_mul_f32_e32 v168, v168, v27
	v_mul_f32_e32 v143, v143, v135
	v_mul_f32_e32 v151, v151, v135
	v_mul_f32_e32 v167, v167, v135
	v_mul_f32_e32 v135, v168, v135
	v_cvt_pk_bf16_f32 v168, v143, v149
	v_cvt_pk_bf16_f32 v169, v151, v167
	v_cvt_pk_bf16_f32 v170, v170, v172
	v_cvt_pk_bf16_f32 v171, v171, v135
	ds_read_b32 v149, v133
	v_ashrrev_i32_e32 v151, 31, v150
	v_lshlrev_b64 v[150:151], 10, v[150:151]
	v_lshl_add_u64 v[150:151], s[16:17], 0, v[150:151]
	v_lshl_add_u64 v[150:151], v[150:151], 0, v[130:131]
	s_waitcnt lgkmcnt(0)
	v_lshlrev_b32_e32 v135, 2, v149
	v_add_u32_e32 v135, 0, v135
	v_add_u32_e32 v143, 0x20100, v135
	v_add_u32_e32 v135, 0x20200, v135
	ds_read_b32 v143, v143
	ds_read_b32 v135, v135
	global_store_dwordx4 v[150:151], v[168:171], off nt
	v_or_b32_e32 v150, 32, v148
	s_waitcnt lgkmcnt(1)
	v_sub_u32_e32 v151, v150, v143
	s_waitcnt lgkmcnt(0)
	v_cmp_lt_i32_e32 vcc, v151, v135
	v_mov_b32_e32 v135, 0
	v_mov_b32_e32 v143, 0
	s_and_saveexec_b64 s[36:37], vcc
	s_cbranch_execz .LBB0_1585
	v_mul_lo_u32 v143, v149, s66
	v_add_u32_e32 v168, v151, v143
	v_ashrrev_i32_e32 v169, 31, v168
	v_lshl_add_u64 v[168:169], v[168:169], 2, s[18:19]
	global_load_dword v143, v[168:169], off
.LBB0_1585:
	s_or_b64 exec, exec, s[36:37]
	v_mul_f32_e32 v168, 0xbfb8aa3b, v55
	v_exp_f32_e32 v168, v168
	v_mul_f32_e32 v169, 0xbfb8aa3b, v48
	v_exp_f32_e32 v169, v169
	v_mul_f32_e32 v170, 0xbfb8aa3b, v49
	v_add_f32_e32 v168, 1.0, v168
	v_rcp_f32_e32 v168, v168
	v_add_f32_e32 v169, 1.0, v169
	v_exp_f32_e32 v170, v170
	v_rcp_f32_e32 v169, v169
	v_mul_f32_e32 v168, v55, v168
	v_mul_f32_e32 v168, v168, v23
	s_waitcnt vmcnt(0)
	v_mul_f32_e32 v171, v168, v143
	v_add_f32_e32 v168, 1.0, v170
	v_mul_f32_e32 v169, v48, v169
	v_rcp_f32_e32 v168, v168
	v_mul_f32_e32 v169, v169, v16
	v_mul_f32_e32 v149, 0xbfb8aa3b, v52
	v_mul_f32_e32 v151, 0xbfb8aa3b, v53
	v_mul_f32_e32 v167, 0xbfb8aa3b, v54
	v_mul_f32_e32 v170, v169, v143
	v_mul_f32_e32 v169, 0xbfb8aa3b, v50
	v_mul_f32_e32 v172, 0xbfb8aa3b, v51
	v_exp_f32_e32 v149, v149
	v_exp_f32_e32 v151, v151
	v_exp_f32_e32 v167, v167
	v_exp_f32_e32 v169, v169
	v_exp_f32_e32 v172, v172
	v_mul_f32_e32 v168, v49, v168
	v_mul_f32_e32 v168, v168, v17
	v_add_f32_e32 v149, 1.0, v149
	v_add_f32_e32 v151, 1.0, v151
	v_add_f32_e32 v167, 1.0, v167
	v_add_f32_e32 v169, 1.0, v169
	v_mul_f32_e32 v173, v168, v143
	v_add_f32_e32 v168, 1.0, v172
	v_rcp_f32_e32 v149, v149
	v_rcp_f32_e32 v151, v151
	v_rcp_f32_e32 v167, v167
	v_rcp_f32_e32 v169, v169
	v_rcp_f32_e32 v168, v168
	v_mul_f32_e32 v149, v52, v149
	v_mul_f32_e32 v151, v53, v151
	v_mul_f32_e32 v167, v54, v167
	v_mul_f32_e32 v169, v50, v169
	v_mul_f32_e32 v168, v51, v168
	v_mul_f32_e32 v149, v149, v20
	v_mul_f32_e32 v151, v151, v21
	v_mul_f32_e32 v167, v167, v22
	v_mul_f32_e32 v169, v169, v18
	v_mul_f32_e32 v168, v168, v19
	v_mul_f32_e32 v149, v149, v143
	v_mul_f32_e32 v151, v151, v143
	v_mul_f32_e32 v167, v167, v143
	v_mul_f32_e32 v172, v169, v143
	v_mul_f32_e32 v143, v168, v143
	v_cvt_pk_bf16_f32 v168, v149, v151
	v_cvt_pk_bf16_f32 v169, v167, v171
	v_cvt_pk_bf16_f32 v170, v170, v173
	v_cvt_pk_bf16_f32 v171, v172, v143
	ds_read_b32 v143, v133
	v_ashrrev_i32_e32 v151, 31, v150
	v_lshlrev_b64 v[150:151], 10, v[150:151]
	v_lshl_add_u64 v[150:151], s[16:17], 0, v[150:151]
	v_lshl_add_u64 v[150:151], v[150:151], 0, v[130:131]
	s_waitcnt lgkmcnt(0)
	v_lshlrev_b32_e32 v149, 2, v143
	v_add_u32_e32 v149, 0, v149
	v_add_u32_e32 v167, 0x20100, v149
	v_add_u32_e32 v149, 0x20200, v149
	ds_read_b32 v167, v167
	ds_read_b32 v172, v149
	global_store_dwordx4 v[150:151], v[168:171], off nt
	v_or_b32_e32 v150, 48, v148
	s_waitcnt lgkmcnt(1)
	v_sub_u32_e32 v149, v150, v167
	s_waitcnt lgkmcnt(0)
	v_cmp_lt_i32_e32 vcc, v149, v172
	s_and_saveexec_b64 s[36:37], vcc
	s_cbranch_execz .LBB0_1587
	v_mul_lo_u32 v135, v143, s66
	v_add_u32_e32 v168, v149, v135
	v_ashrrev_i32_e32 v169, 31, v168
	v_lshl_add_u64 v[168:169], v[168:169], 2, s[18:19]
	global_load_dword v135, v[168:169], off
.LBB0_1587:
	s_or_b64 exec, exec, s[36:37]
	v_mul_f32_e32 v168, 0xbfb8aa3b, v40
	v_exp_f32_e32 v168, v168
	v_mul_f32_e32 v169, 0xbfb8aa3b, v41
	v_exp_f32_e32 v169, v169
	v_mul_f32_e32 v149, 0xbfb8aa3b, v45
	v_add_f32_e32 v168, 1.0, v168
	v_rcp_f32_e32 v168, v168
	v_add_f32_e32 v169, 1.0, v169
	v_rcp_f32_e32 v169, v169
	v_mul_f32_e32 v143, 0xbfb8aa3b, v44
	v_mul_f32_e32 v168, v40, v168
	v_mul_f32_e32 v168, v168, v8
	s_waitcnt vmcnt(0)
	v_mul_f32_e32 v170, v168, v135
	v_mul_f32_e32 v168, v41, v169
	v_mul_f32_e32 v169, 0xbfb8aa3b, v42
	v_exp_f32_e32 v149, v149
	v_mul_f32_e32 v151, 0xbfb8aa3b, v46
	v_mul_f32_e32 v167, 0xbfb8aa3b, v47
	v_exp_f32_e32 v169, v169
	v_mul_f32_e32 v171, 0xbfb8aa3b, v43
	v_exp_f32_e32 v143, v143
	v_exp_f32_e32 v151, v151
	v_exp_f32_e32 v167, v167
	v_exp_f32_e32 v171, v171
	v_add_f32_e32 v149, 1.0, v149
	v_mul_f32_e32 v168, v168, v9
	v_add_f32_e32 v169, 1.0, v169
	v_add_f32_e32 v143, 1.0, v143
	v_rcp_f32_e32 v149, v149
	v_add_f32_e32 v151, 1.0, v151
	v_add_f32_e32 v167, 1.0, v167
	v_rcp_f32_e32 v169, v169
	v_mul_f32_e32 v172, v168, v135
	v_add_f32_e32 v168, 1.0, v171
	v_rcp_f32_e32 v143, v143
	v_rcp_f32_e32 v151, v151
	v_rcp_f32_e32 v167, v167
	v_rcp_f32_e32 v168, v168
	v_mul_f32_e32 v149, v45, v149
	v_mul_f32_e32 v169, v42, v169
	v_mul_f32_e32 v143, v44, v143
	v_mul_f32_e32 v149, v149, v13
	v_mul_f32_e32 v151, v46, v151
	v_mul_f32_e32 v167, v47, v167
	v_mul_f32_e32 v169, v169, v10
	v_mul_f32_e32 v168, v43, v168
	v_mul_f32_e32 v143, v143, v12
	v_mul_f32_e32 v149, v149, v135
	v_mul_f32_e32 v151, v151, v14
	v_mul_f32_e32 v167, v167, v15
	v_mul_f32_e32 v171, v169, v135
	v_mul_f32_e32 v168, v168, v11
	v_mul_f32_e32 v143, v143, v135
	v_mul_f32_e32 v151, v151, v135
	v_mul_f32_e32 v167, v167, v135
	v_mul_f32_e32 v135, v168, v135
	v_cvt_pk_bf16_f32 v168, v143, v149
	v_cvt_pk_bf16_f32 v169, v151, v167
	v_cvt_pk_bf16_f32 v170, v170, v172
	v_cvt_pk_bf16_f32 v171, v171, v135
	ds_read_b32 v149, v133
	v_ashrrev_i32_e32 v151, 31, v150
	v_lshlrev_b64 v[150:151], 10, v[150:151]
	v_lshl_add_u64 v[150:151], s[16:17], 0, v[150:151]
	v_lshl_add_u64 v[150:151], v[150:151], 0, v[130:131]
	s_waitcnt lgkmcnt(0)
	v_lshlrev_b32_e32 v135, 2, v149
	v_add_u32_e32 v135, 0, v135
	v_add_u32_e32 v143, 0x20100, v135
	v_add_u32_e32 v135, 0x20200, v135
	ds_read_b32 v143, v143
	ds_read_b32 v135, v135
	global_store_dwordx4 v[150:151], v[168:171], off nt
	v_add_u32_e32 v150, 0x80, v148
	s_waitcnt lgkmcnt(1)
	v_sub_u32_e32 v151, v150, v143
	s_waitcnt lgkmcnt(0)
	v_cmp_lt_i32_e32 vcc, v151, v135
	v_mov_b32_e32 v135, 0
	v_mov_b32_e32 v143, 0
	s_and_saveexec_b64 s[36:37], vcc
	s_cbranch_execz .LBB0_1589
	v_mul_lo_u32 v143, v149, s66
	v_add_u32_e32 v168, v151, v143
	v_ashrrev_i32_e32 v169, 31, v168
	v_lshl_add_u64 v[168:169], v[168:169], 2, s[18:19]
	global_load_dword v143, v[168:169], off
.LBB0_1589:
	s_or_b64 exec, exec, s[36:37]
	v_mul_f32_e32 v168, 0xbfb8aa3b, v7
	v_exp_f32_e32 v168, v168
	v_mul_f32_e32 v169, 0xbfb8aa3b, v0
	v_exp_f32_e32 v169, v169
	v_mul_f32_e32 v170, 0xbfb8aa3b, v1
	v_add_f32_e32 v168, 1.0, v168
	v_rcp_f32_e32 v168, v168
	v_add_f32_e32 v169, 1.0, v169
	v_exp_f32_e32 v170, v170
	v_rcp_f32_e32 v169, v169
	v_mul_f32_e32 v168, v7, v168
	v_mul_f32_e32 v168, v168, v99
	s_waitcnt vmcnt(0)
	v_mul_f32_e32 v171, v168, v143
	v_add_f32_e32 v168, 1.0, v170
	v_mul_f32_e32 v169, v0, v169
	v_rcp_f32_e32 v168, v168
	v_mul_f32_e32 v169, v169, v100
	v_mul_f32_e32 v149, 0xbfb8aa3b, v4
	v_mul_f32_e32 v151, 0xbfb8aa3b, v5
	v_mul_f32_e32 v167, 0xbfb8aa3b, v6
	v_mul_f32_e32 v170, v169, v143
	v_mul_f32_e32 v169, 0xbfb8aa3b, v2
	v_mul_f32_e32 v172, 0xbfb8aa3b, v3
	v_exp_f32_e32 v149, v149
	v_exp_f32_e32 v151, v151
	v_exp_f32_e32 v167, v167
	v_exp_f32_e32 v169, v169
	v_exp_f32_e32 v172, v172
	v_mul_f32_e32 v168, v1, v168
	v_mul_f32_e32 v168, v168, v101
	v_add_f32_e32 v149, 1.0, v149
	v_add_f32_e32 v151, 1.0, v151
	v_add_f32_e32 v167, 1.0, v167
	v_add_f32_e32 v169, 1.0, v169
	v_mul_f32_e32 v173, v168, v143
	v_add_f32_e32 v168, 1.0, v172
	v_rcp_f32_e32 v149, v149
	v_rcp_f32_e32 v151, v151
	v_rcp_f32_e32 v167, v167
	v_rcp_f32_e32 v169, v169
	v_rcp_f32_e32 v168, v168
	v_mul_f32_e32 v149, v4, v149
	v_mul_f32_e32 v151, v5, v151
	v_mul_f32_e32 v167, v6, v167
	v_mul_f32_e32 v169, v2, v169
	v_mul_f32_e32 v168, v3, v168
	v_mul_f32_e32 v149, v149, v96
	v_mul_f32_e32 v151, v151, v97
	v_mul_f32_e32 v167, v167, v98
	v_mul_f32_e32 v169, v169, v102
	v_mul_f32_e32 v168, v168, v103
	v_mul_f32_e32 v149, v149, v143
	v_mul_f32_e32 v151, v151, v143
	v_mul_f32_e32 v167, v167, v143
	v_mul_f32_e32 v172, v169, v143
	v_mul_f32_e32 v143, v168, v143
	v_cvt_pk_bf16_f32 v168, v149, v151
	v_cvt_pk_bf16_f32 v169, v167, v171
	v_cvt_pk_bf16_f32 v170, v170, v173
	v_cvt_pk_bf16_f32 v171, v172, v143
	ds_read_b32 v143, v133
	v_ashrrev_i32_e32 v151, 31, v150
	v_lshlrev_b64 v[150:151], 10, v[150:151]
	v_lshl_add_u64 v[150:151], s[16:17], 0, v[150:151]
	v_lshl_add_u64 v[150:151], v[150:151], 0, v[130:131]
	s_waitcnt lgkmcnt(0)
	v_lshlrev_b32_e32 v149, 2, v143
	v_add_u32_e32 v149, 0, v149
	v_add_u32_e32 v167, 0x20100, v149
	v_add_u32_e32 v149, 0x20200, v149
	ds_read_b32 v167, v167
	ds_read_b32 v172, v149
	global_store_dwordx4 v[150:151], v[168:171], off nt
	v_add_u32_e32 v150, 0x90, v148
	s_waitcnt lgkmcnt(1)
	v_sub_u32_e32 v149, v150, v167
	s_waitcnt lgkmcnt(0)
	v_cmp_lt_i32_e32 vcc, v149, v172
	s_and_saveexec_b64 s[36:37], vcc
	s_cbranch_execz .LBB0_1591
	v_mul_lo_u32 v135, v143, s66
	v_add_u32_e32 v168, v149, v135
	v_ashrrev_i32_e32 v169, 31, v168
	v_lshl_add_u64 v[168:169], v[168:169], 2, s[18:19]
	global_load_dword v135, v[168:169], off
.LBB0_1591:
	s_or_b64 exec, exec, s[36:37]
	v_mul_f32_e32 v168, 0xbfb8aa3b, v76
	v_exp_f32_e32 v168, v168
	v_mul_f32_e32 v169, 0xbfb8aa3b, v77
	v_exp_f32_e32 v169, v169
	v_mul_f32_e32 v149, 0xbfb8aa3b, v69
	v_add_f32_e32 v168, 1.0, v168
	v_rcp_f32_e32 v168, v168
	v_add_f32_e32 v169, 1.0, v169
	v_rcp_f32_e32 v169, v169
	v_mul_f32_e32 v143, 0xbfb8aa3b, v68
	v_mul_f32_e32 v168, v76, v168
	v_mul_f32_e32 v168, v168, v108
	s_waitcnt vmcnt(0)
	v_mul_f32_e32 v170, v168, v135
	v_mul_f32_e32 v168, v77, v169
	v_mul_f32_e32 v169, 0xbfb8aa3b, v78
	v_exp_f32_e32 v149, v149
	v_mul_f32_e32 v151, 0xbfb8aa3b, v70
	v_mul_f32_e32 v167, 0xbfb8aa3b, v71
	v_exp_f32_e32 v169, v169
	v_mul_f32_e32 v171, 0xbfb8aa3b, v79
	v_exp_f32_e32 v143, v143
	v_exp_f32_e32 v151, v151
	v_exp_f32_e32 v167, v167
	v_exp_f32_e32 v171, v171
	v_add_f32_e32 v149, 1.0, v149
	v_mul_f32_e32 v168, v168, v109
	v_add_f32_e32 v169, 1.0, v169
	v_add_f32_e32 v143, 1.0, v143
	v_rcp_f32_e32 v149, v149
	v_add_f32_e32 v151, 1.0, v151
	v_add_f32_e32 v167, 1.0, v167
	v_rcp_f32_e32 v169, v169
	v_mul_f32_e32 v172, v168, v135
	v_add_f32_e32 v168, 1.0, v171
	v_rcp_f32_e32 v143, v143
	v_rcp_f32_e32 v151, v151
	v_rcp_f32_e32 v167, v167
	v_rcp_f32_e32 v168, v168
	v_mul_f32_e32 v149, v69, v149
	v_mul_f32_e32 v169, v78, v169
	v_mul_f32_e32 v143, v68, v143
	v_mul_f32_e32 v149, v149, v105
	v_mul_f32_e32 v151, v70, v151
	v_mul_f32_e32 v167, v71, v167
	v_mul_f32_e32 v169, v169, v110
	v_mul_f32_e32 v168, v79, v168
	v_mul_f32_e32 v143, v143, v104
	v_mul_f32_e32 v149, v149, v135
	v_mul_f32_e32 v151, v151, v106
	v_mul_f32_e32 v167, v167, v107
	v_mul_f32_e32 v171, v169, v135
	v_mul_f32_e32 v168, v168, v111
	v_mul_f32_e32 v143, v143, v135
	v_mul_f32_e32 v151, v151, v135
	v_mul_f32_e32 v167, v167, v135
	v_mul_f32_e32 v135, v168, v135
	v_cvt_pk_bf16_f32 v168, v143, v149
	v_cvt_pk_bf16_f32 v169, v151, v167
	v_cvt_pk_bf16_f32 v170, v170, v172
	v_cvt_pk_bf16_f32 v171, v171, v135
	ds_read_b32 v149, v133
	v_ashrrev_i32_e32 v151, 31, v150
	v_lshlrev_b64 v[150:151], 10, v[150:151]
	v_lshl_add_u64 v[150:151], s[16:17], 0, v[150:151]
	v_lshl_add_u64 v[150:151], v[150:151], 0, v[130:131]
	s_waitcnt lgkmcnt(0)
	v_lshlrev_b32_e32 v135, 2, v149
	v_add_u32_e32 v135, 0, v135
	v_add_u32_e32 v143, 0x20100, v135
	v_add_u32_e32 v135, 0x20200, v135
	ds_read_b32 v143, v143
	ds_read_b32 v135, v135
	global_store_dwordx4 v[150:151], v[168:171], off nt
	v_add_u32_e32 v150, 0xa0, v148
	s_waitcnt lgkmcnt(1)
	v_sub_u32_e32 v151, v150, v143
	s_waitcnt lgkmcnt(0)
	v_cmp_lt_i32_e32 vcc, v151, v135
	v_mov_b32_e32 v135, 0
	v_mov_b32_e32 v143, 0
	s_and_saveexec_b64 s[36:37], vcc
	s_cbranch_execz .LBB0_1593
	v_mul_lo_u32 v143, v149, s66
	v_add_u32_e32 v168, v151, v143
	v_ashrrev_i32_e32 v169, 31, v168
	v_lshl_add_u64 v[168:169], v[168:169], 2, s[18:19]
	global_load_dword v143, v[168:169], off
.LBB0_1593:
	s_or_b64 exec, exec, s[36:37]
	v_mul_f32_e32 v168, 0xbfb8aa3b, v83
	v_exp_f32_e32 v168, v168
	v_mul_f32_e32 v169, 0xbfb8aa3b, v84
	v_exp_f32_e32 v169, v169
	v_mul_f32_e32 v170, 0xbfb8aa3b, v85
	v_add_f32_e32 v168, 1.0, v168
	v_rcp_f32_e32 v168, v168
	v_add_f32_e32 v169, 1.0, v169
	v_exp_f32_e32 v170, v170
	v_rcp_f32_e32 v169, v169
	v_mul_f32_e32 v168, v83, v168
	v_mul_f32_e32 v168, v168, v115
	s_waitcnt vmcnt(0)
	v_mul_f32_e32 v171, v168, v143
	v_add_f32_e32 v168, 1.0, v170
	v_mul_f32_e32 v169, v84, v169
	v_rcp_f32_e32 v168, v168
	v_mul_f32_e32 v169, v169, v116
	v_mul_f32_e32 v149, 0xbfb8aa3b, v80
	v_mul_f32_e32 v151, 0xbfb8aa3b, v81
	v_mul_f32_e32 v167, 0xbfb8aa3b, v82
	v_mul_f32_e32 v170, v169, v143
	v_mul_f32_e32 v169, 0xbfb8aa3b, v86
	v_mul_f32_e32 v172, 0xbfb8aa3b, v87
	v_exp_f32_e32 v149, v149
	v_exp_f32_e32 v151, v151
	v_exp_f32_e32 v167, v167
	v_exp_f32_e32 v169, v169
	v_exp_f32_e32 v172, v172
	v_mul_f32_e32 v168, v85, v168
	v_mul_f32_e32 v168, v168, v117
	v_add_f32_e32 v149, 1.0, v149
	v_add_f32_e32 v151, 1.0, v151
	v_add_f32_e32 v167, 1.0, v167
	v_add_f32_e32 v169, 1.0, v169
	v_mul_f32_e32 v173, v168, v143
	v_add_f32_e32 v168, 1.0, v172
	v_rcp_f32_e32 v149, v149
	v_rcp_f32_e32 v151, v151
	v_rcp_f32_e32 v167, v167
	v_rcp_f32_e32 v169, v169
	v_rcp_f32_e32 v168, v168
	v_mul_f32_e32 v149, v80, v149
	v_mul_f32_e32 v151, v81, v151
	v_mul_f32_e32 v167, v82, v167
	v_mul_f32_e32 v169, v86, v169
	v_mul_f32_e32 v168, v87, v168
	v_mul_f32_e32 v149, v149, v112
	v_mul_f32_e32 v151, v151, v113
	v_mul_f32_e32 v167, v167, v114
	v_mul_f32_e32 v169, v169, v118
	v_mul_f32_e32 v168, v168, v119
	v_mul_f32_e32 v149, v149, v143
	v_mul_f32_e32 v151, v151, v143
	v_mul_f32_e32 v167, v167, v143
	v_mul_f32_e32 v172, v169, v143
	v_mul_f32_e32 v143, v168, v143
	v_cvt_pk_bf16_f32 v168, v149, v151
	v_cvt_pk_bf16_f32 v169, v167, v171
	v_cvt_pk_bf16_f32 v170, v170, v173
	v_cvt_pk_bf16_f32 v171, v172, v143
	ds_read_b32 v133, v133
	v_ashrrev_i32_e32 v151, 31, v150
	v_lshlrev_b64 v[150:151], 10, v[150:151]
	v_add_u32_e32 v148, 0xb0, v148
	v_lshl_add_u64 v[150:151], s[16:17], 0, v[150:151]
	s_waitcnt lgkmcnt(0)
	v_lshlrev_b32_e32 v143, 2, v133
	v_add_u32_e32 v143, 0, v143
	v_add_u32_e32 v149, 0x20100, v143
	v_add_u32_e32 v143, 0x20200, v143
	ds_read_b32 v149, v149
	ds_read_b32 v167, v143
	v_lshl_add_u64 v[150:151], v[150:151], 0, v[130:131]
	global_store_dwordx4 v[150:151], v[168:171], off nt
	s_waitcnt lgkmcnt(1)
	v_sub_u32_e32 v143, v148, v149
	s_waitcnt lgkmcnt(0)
	v_cmp_lt_i32_e32 vcc, v143, v167
	s_and_saveexec_b64 s[36:37], vcc
	s_cbranch_execz .LBB0_1595
	v_mul_lo_u32 v133, v133, s66
	v_add_u32_e32 v150, v143, v133
	v_ashrrev_i32_e32 v151, 31, v150
	v_lshl_add_u64 v[150:151], v[150:151], 2, s[18:19]
	global_load_dword v135, v[150:151], off
.LBB0_1595:
	s_or_b64 exec, exec, s[36:37]
	v_mul_f32_e32 v168, 0xbfb8aa3b, v94
	v_mul_f32_e32 v149, 0xbfb8aa3b, v90
	v_exp_f32_e32 v168, v168
	v_mul_f32_e32 v133, 0xbfb8aa3b, v88
	v_mul_f32_e32 v143, 0xbfb8aa3b, v89
	v_exp_f32_e32 v149, v149
	v_mul_f32_e32 v150, 0xbfb8aa3b, v91
	v_mul_f32_e32 v151, 0xbfb8aa3b, v92
	v_mul_f32_e32 v167, 0xbfb8aa3b, v93
	v_mul_f32_e32 v169, 0xbfb8aa3b, v95
	v_exp_f32_e32 v133, v133
	v_exp_f32_e32 v143, v143
	v_exp_f32_e32 v150, v150
	v_exp_f32_e32 v151, v151
	v_exp_f32_e32 v167, v167
	v_exp_f32_e32 v169, v169
	v_add_f32_e32 v168, 1.0, v168
	v_add_f32_e32 v149, 1.0, v149
	v_rcp_f32_e32 v168, v168
	v_add_f32_e32 v133, 1.0, v133
	v_add_f32_e32 v143, 1.0, v143
	v_rcp_f32_e32 v149, v149
	v_add_f32_e32 v150, 1.0, v150
	v_add_f32_e32 v151, 1.0, v151
	v_add_f32_e32 v167, 1.0, v167
	v_add_f32_e32 v169, 1.0, v169
	v_rcp_f32_e32 v133, v133
	v_rcp_f32_e32 v143, v143
	v_rcp_f32_e32 v150, v150
	v_rcp_f32_e32 v151, v151
	v_rcp_f32_e32 v167, v167
	v_rcp_f32_e32 v169, v169
	v_mul_f32_e32 v168, v94, v168
	v_mul_f32_e32 v149, v90, v149
	v_mul_f32_e32 v168, v168, v126
	v_mul_f32_e32 v133, v88, v133
	v_mul_f32_e32 v143, v89, v143
	v_mul_f32_e32 v149, v149, v122
	v_mul_f32_e32 v150, v91, v150
	v_mul_f32_e32 v151, v92, v151
	v_mul_f32_e32 v167, v93, v167
	s_waitcnt vmcnt(0)
	v_mul_f32_e32 v171, v168, v135
	v_mul_f32_e32 v168, v95, v169
	v_mul_f32_e32 v133, v133, v120
	v_mul_f32_e32 v143, v143, v121
	v_mul_f32_e32 v149, v149, v135
	v_mul_f32_e32 v150, v150, v123
	v_mul_f32_e32 v151, v151, v124
	v_mul_f32_e32 v167, v167, v125
	v_mul_f32_e32 v168, v168, v127
	v_mul_f32_e32 v133, v133, v135
	v_mul_f32_e32 v143, v143, v135
	v_mul_f32_e32 v150, v150, v135
	v_mul_f32_e32 v151, v151, v135
	v_mul_f32_e32 v167, v167, v135
	v_mul_f32_e32 v135, v168, v135
	v_cvt_pk_bf16_f32 v168, v133, v143
	v_cvt_pk_bf16_f32 v169, v149, v150
	v_ashrrev_i32_e32 v149, 31, v148
	v_lshlrev_b64 v[148:149], 10, v[148:149]
	v_lshl_add_u64 v[148:149], s[16:17], 0, v[148:149]
	v_lshl_add_u64 v[148:149], v[148:149], 0, v[130:131]
	s_and_b64 vcc, exec, s[4:5]
	v_cvt_pk_bf16_f32 v170, v151, v167
	v_cvt_pk_bf16_f32 v171, v171, v135
	global_store_dwordx4 v[148:149], v[168:171], off nt
	s_cbranch_vccnz .LBB0_1598
	s_andn2_b64 vcc, exec, s[14:15]
	s_cbranch_vccnz .LBB0_1541
	s_barrier
	s_branch .LBB0_1541

.LBB0_1717:
	v_lshl_add_u32 v152, v136, 8, v156
	v_lshlrev_b32_e32 v136, 8, v142
	v_and_b32_e32 v136, 0x700, v136
	v_ashrrev_i32_e32 v153, 31, v152
	v_readlane_b32 s36, v250, 48
	v_or_b32_e32 v136, v136, v158
	v_lshlrev_b64 v[142:143], 12, v[152:153]
	v_readlane_b32 s37, v250, 49
	v_lshlrev_b32_e32 v136, 1, v136
	v_cvt_pk_bf16_f32 v124, v124, v125
	v_cvt_pk_bf16_f32 v125, v126, v127
	v_cvt_pk_bf16_f32 v126, v120, v121
	v_cvt_pk_bf16_f32 v127, v122, v123
	s_nop 0
	v_lshl_add_u64 v[142:143], s[36:37], 0, v[142:143]
	v_lshl_add_u64 v[142:143], v[142:143], 0, v[136:137]
	global_store_dwordx4 v[142:143], v[124:127], off nt
	v_cvt_pk_bf16_f32 v112, v112, v113
	v_cvt_pk_bf16_f32 v113, v114, v115
	v_cvt_pk_bf16_f32 v114, v104, v105
	v_or_b32_e32 v104, 16, v152
	v_ashrrev_i32_e32 v105, 31, v104
	v_lshlrev_b64 v[104:105], 12, v[104:105]
	v_lshl_add_u64 v[104:105], s[36:37], 0, v[104:105]
	v_cvt_pk_bf16_f32 v115, v106, v107
	global_store_dwordx4 v[142:143], v[112:115], off offset:256 nt
	s_nop 1
	v_lshl_add_u64 v[112:113], v[104:105], 0, v[136:137]
	v_cvt_pk_bf16_f32 v104, v116, v117
	v_cvt_pk_bf16_f32 v105, v118, v119
	v_cvt_pk_bf16_f32 v106, v108, v109
	v_cvt_pk_bf16_f32 v107, v110, v111
	global_store_dwordx4 v[112:113], v[104:107], off nt
	v_cvt_pk_bf16_f32 v96, v96, v97
	v_cvt_pk_bf16_f32 v97, v98, v99
	v_cvt_pk_bf16_f32 v98, v88, v89
	v_or_b32_e32 v88, 32, v152
	v_ashrrev_i32_e32 v89, 31, v88
	v_lshlrev_b64 v[88:89], 12, v[88:89]
	v_lshl_add_u64 v[88:89], s[36:37], 0, v[88:89]
	v_cvt_pk_bf16_f32 v99, v90, v91
	global_store_dwordx4 v[112:113], v[96:99], off offset:256 nt
	s_nop 1
	v_lshl_add_u64 v[96:97], v[88:89], 0, v[136:137]
	v_cvt_pk_bf16_f32 v88, v100, v101
	v_cvt_pk_bf16_f32 v89, v102, v103
	v_cvt_pk_bf16_f32 v90, v92, v93
	v_cvt_pk_bf16_f32 v91, v94, v95
	global_store_dwordx4 v[96:97], v[88:91], off nt
	v_cvt_pk_bf16_f32 v84, v84, v85
	v_cvt_pk_bf16_f32 v85, v86, v87
	v_cvt_pk_bf16_f32 v86, v76, v77
	v_or_b32_e32 v76, 48, v152
	v_ashrrev_i32_e32 v77, 31, v76
	v_lshlrev_b64 v[76:77], 12, v[76:77]
	v_lshl_add_u64 v[76:77], s[36:37], 0, v[76:77]
	v_cvt_pk_bf16_f32 v87, v78, v79
	global_store_dwordx4 v[96:97], v[84:87], off offset:256 nt
	s_nop 1
	v_lshl_add_u64 v[84:85], v[76:77], 0, v[136:137]
	v_cvt_pk_bf16_f32 v76, v80, v81
	v_cvt_pk_bf16_f32 v77, v82, v83
	v_cvt_pk_bf16_f32 v78, v72, v73
	v_cvt_pk_bf16_f32 v79, v74, v75
	global_store_dwordx4 v[84:85], v[76:79], off nt
	v_cvt_pk_bf16_f32 v68, v68, v69
	v_cvt_pk_bf16_f32 v69, v70, v71
	v_cvt_pk_bf16_f32 v70, v64, v65
	v_cvt_pk_bf16_f32 v71, v66, v67
	global_store_dwordx4 v[84:85], v[68:71], off offset:256 nt
	v_cvt_pk_bf16_f32 v60, v60, v61
	v_cvt_pk_bf16_f32 v61, v62, v63
	v_cvt_pk_bf16_f32 v62, v56, v57
	v_add_co_u32_e32 v56, vcc, s58, v142
	v_lshl_add_u64 v[64:65], v[142:143], 0, s[24:25]
	s_nop 0
	v_addc_co_u32_e32 v57, vcc, 0, v143, vcc
	v_cvt_pk_bf16_f32 v63, v58, v59
	global_store_dwordx4 v[56:57], v[60:63], off nt
	v_cvt_pk_bf16_f32 v48, v48, v49
	v_cvt_pk_bf16_f32 v49, v50, v51
	v_cvt_pk_bf16_f32 v50, v40, v41
	v_cvt_pk_bf16_f32 v51, v42, v43
	global_store_dwordx4 v[64:65], v[48:51], off offset:256 nt
	v_cvt_pk_bf16_f32 v40, v52, v53
	v_cvt_pk_bf16_f32 v41, v54, v55
	v_cvt_pk_bf16_f32 v42, v44, v45
	v_add_co_u32_e32 v44, vcc, s59, v142
	s_nop 0
	v_lshl_add_u64 v[48:49], v[142:143], 0, s[26:27]
	v_addc_co_u32_e32 v45, vcc, 0, v143, vcc
	v_cvt_pk_bf16_f32 v43, v46, v47
	global_store_dwordx4 v[44:45], v[40:43], off nt
	v_cvt_pk_bf16_f32 v32, v32, v33
	v_cvt_pk_bf16_f32 v33, v34, v35
	v_cvt_pk_bf16_f32 v34, v24, v25
	v_cvt_pk_bf16_f32 v35, v26, v27
	global_store_dwordx4 v[48:49], v[32:35], off offset:256 nt
	v_cvt_pk_bf16_f32 v24, v36, v37
	v_cvt_pk_bf16_f32 v25, v38, v39
	v_cvt_pk_bf16_f32 v26, v28, v29
	v_add_co_u32_e32 v28, vcc, s60, v142
	s_nop 0
	v_lshl_add_u64 v[32:33], v[142:143], 0, s[28:29]
	v_addc_co_u32_e32 v29, vcc, 0, v143, vcc
	v_cvt_pk_bf16_f32 v27, v30, v31
	global_store_dwordx4 v[28:29], v[24:27], off nt
	v_cvt_pk_bf16_f32 v16, v16, v17
	v_cvt_pk_bf16_f32 v17, v18, v19
	v_cvt_pk_bf16_f32 v18, v8, v9
	v_cvt_pk_bf16_f32 v19, v10, v11
	global_store_dwordx4 v[32:33], v[16:19], off offset:256 nt
	v_cvt_pk_bf16_f32 v8, v20, v21
	v_cvt_pk_bf16_f32 v9, v22, v23
	v_cvt_pk_bf16_f32 v10, v12, v13
	v_add_co_u32_e32 v12, vcc, s61, v142
	s_nop 0
	v_lshl_add_u64 v[16:17], v[142:143], 0, s[30:31]
	v_addc_co_u32_e32 v13, vcc, 0, v143, vcc
	s_andn2_b64 vcc, exec, s[34:35]
	s_mov_b64 s[34:35], -1
	v_cvt_pk_bf16_f32 v11, v14, v15
	global_store_dwordx4 v[12:13], v[8:11], off nt
	v_cvt_pk_bf16_f32 v4, v4, v5
	v_cvt_pk_bf16_f32 v5, v6, v7
	v_cvt_pk_bf16_f32 v6, v0, v1
	v_cvt_pk_bf16_f32 v7, v2, v3
	global_store_dwordx4 v[16:17], v[4:7], off offset:256 nt
	s_cbranch_vccnz .LBB0_1689
	s_andn2_b64 vcc, exec, s[12:13]
	s_cbranch_vccnz .LBB0_1688
	s_barrier
	s_branch .LBB0_1688
